# PEER gather as three column-sliced passes (XCD-local L2 reuse): fixed a constant-register clobber and a 64-bit shift-range bug in the v-side pass; unnormalised rows via scratch
# speedup vs baseline: 1.0282x; 1.0029x over previous
.Lgba_1444:
	s_or_b64 exec, exec, s[2:3]
	s_waitcnt lgkmcnt(0)
	s_barrier
	s_mov_b64 exec, -1
	v_and_b32_e32 v1, 63, v0
	v_readfirstlane_b32 s16, v0
	s_load_dwordx2 s[12:13], s[0:1], 0xc0
	s_lshr_b32 s16, s16, 6
	s_and_b32 s18, s33, 7
	s_lshr_b32 s19, s33, 3
	s_lshl_b32 s19, s19, 8
	s_lshl_b32 s16, s16, 5
	s_add_i32 s16, s16, s19
	s_add_i32 s17, s16, 32
	s_add_i32 s24, s17, -1
	s_lshl_b32 s19, s18, 9
	v_lshl_add_u32 v162, v1, 3, s19
	v_mov_b32_e32 v163, 0
	s_mov_b32 s31, 0
	v_and_b32_e32 v4, 8, v1
	v_cmp_eq_u32_e64 s[8:9], 0, v4
	v_and_b32_e32 v4, 4, v1
	v_cmp_eq_u32_e64 s[10:11], 0, v4
	v_and_b32_e32 v4, 2, v1
	v_cmp_eq_u32_e64 s[14:15], 0, v4
	s_mov_b32 s2, 0x55555555
	s_mov_b32 s3, 0x55555555
	s_load_dwordx2 s[4:5], s[0:1], 0x88
	s_waitcnt lgkmcnt(0)
	v_lshl_add_u64 v[160:161], v[162:163], 2, s[4:5]
	global_load_dwordx4 v[100:103], v[160:161], off
	global_load_dwordx4 v[104:107], v[160:161], off offset:16
	s_lshl_b32 s19, s18, 20
	s_add_u32 s22, s12, 0x25c00000
	s_addc_u32 s23, s13, 0
	s_add_u32 s22, s22, s19
	s_addc_u32 s23, s23, 0
	s_add_u32 s26, s12, 0xfc00000
	s_addc_u32 s27, s13, 0
	s_add_u32 s20, s12, 0x100000
	s_addc_u32 s21, s13, 0
	v_lshl_add_u64 v[172:173], v[162:163], 1, s[20:21]
	s_add_u32 s20, s12, 0x4da00000
	s_addc_u32 s21, s13, 0
	v_mov_b32_e32 v4, v1
	v_mov_b32_e32 v5, 0
	v_lshl_add_u64 v[174:175], v[4:5], 2, s[20:21]
	s_lshl_b32 s19, s18, 22
	s_add_u32 s20, s12, 0x23c00000
	s_addc_u32 s21, s13, 0
	s_add_u32 s20, s20, s19
	s_addc_u32 s21, s21, 0
	v_lshl_add_u64 v[176:177], v[4:5], 1, s[20:21]
	s_lshl_b32 s30, s16, 13
	v_lshl_add_u64 v[160:161], v[172:173], 0, s[30:31]
	global_load_dwordx4 v[116:119], v[160:161], off
	s_lshl_b32 s30, s16, 9
	v_lshl_add_u64 v[160:161], v[174:175], 0, s[30:31]
	global_load_dword v122, v[160:161], off
	global_load_dword v123, v[160:161], off offset:256
	s_waitcnt vmcnt(0)
	v_readlane_b32 s30, v122, 0
	s_lshl_b32 s30, s30, 12
	s_add_u32 s28, s26, s30
	s_addc_u32 s29, s27, 0
	global_load_dwordx2 v[24:25], v162, s[28:29]
	v_readlane_b32 s30, v122, 1
	s_lshl_b32 s30, s30, 12
	s_add_u32 s28, s26, s30
	s_addc_u32 s29, s27, 0
	global_load_dwordx2 v[26:27], v162, s[28:29]
	v_readlane_b32 s30, v122, 2
	s_lshl_b32 s30, s30, 12
	s_add_u32 s28, s26, s30
	s_addc_u32 s29, s27, 0
	global_load_dwordx2 v[28:29], v162, s[28:29]
	v_readlane_b32 s30, v122, 3
	s_lshl_b32 s30, s30, 12
	s_add_u32 s28, s26, s30
	s_addc_u32 s29, s27, 0
	global_load_dwordx2 v[30:31], v162, s[28:29]
	v_readlane_b32 s30, v122, 4
	s_lshl_b32 s30, s30, 12
	s_add_u32 s28, s26, s30
	s_addc_u32 s29, s27, 0
	global_load_dwordx2 v[32:33], v162, s[28:29]
	v_readlane_b32 s30, v122, 5
	s_lshl_b32 s30, s30, 12
	s_add_u32 s28, s26, s30
	s_addc_u32 s29, s27, 0
	global_load_dwordx2 v[34:35], v162, s[28:29]
	v_readlane_b32 s30, v122, 6
	s_lshl_b32 s30, s30, 12
	s_add_u32 s28, s26, s30
	s_addc_u32 s29, s27, 0
	global_load_dwordx2 v[36:37], v162, s[28:29]
	v_readlane_b32 s30, v122, 7
	s_lshl_b32 s30, s30, 12
	s_add_u32 s28, s26, s30
	s_addc_u32 s29, s27, 0
	global_load_dwordx2 v[38:39], v162, s[28:29]
	v_readlane_b32 s30, v122, 8
	s_lshl_b32 s30, s30, 12
	s_add_u32 s28, s26, s30
	s_addc_u32 s29, s27, 0
	global_load_dwordx2 v[40:41], v162, s[28:29]
	v_readlane_b32 s30, v122, 9
	s_lshl_b32 s30, s30, 12
	s_add_u32 s28, s26, s30
	s_addc_u32 s29, s27, 0
	global_load_dwordx2 v[42:43], v162, s[28:29]
	v_readlane_b32 s30, v122, 10
	s_lshl_b32 s30, s30, 12
	s_add_u32 s28, s26, s30
	s_addc_u32 s29, s27, 0
	global_load_dwordx2 v[44:45], v162, s[28:29]
	v_readlane_b32 s30, v122, 11
	s_lshl_b32 s30, s30, 12
	s_add_u32 s28, s26, s30
	s_addc_u32 s29, s27, 0
	global_load_dwordx2 v[46:47], v162, s[28:29]
	v_readlane_b32 s30, v122, 12
	s_lshl_b32 s30, s30, 12
	s_add_u32 s28, s26, s30
	s_addc_u32 s29, s27, 0
	global_load_dwordx2 v[48:49], v162, s[28:29]
	v_readlane_b32 s30, v122, 13
	s_lshl_b32 s30, s30, 12
	s_add_u32 s28, s26, s30
	s_addc_u32 s29, s27, 0
	global_load_dwordx2 v[50:51], v162, s[28:29]
	v_readlane_b32 s30, v122, 14
	s_lshl_b32 s30, s30, 12
	s_add_u32 s28, s26, s30
	s_addc_u32 s29, s27, 0
	global_load_dwordx2 v[52:53], v162, s[28:29]
	v_readlane_b32 s30, v122, 15
	s_lshl_b32 s30, s30, 12
	s_add_u32 s28, s26, s30
	s_addc_u32 s29, s27, 0
	global_load_dwordx2 v[54:55], v162, s[28:29]
	v_readlane_b32 s30, v122, 16
	s_lshl_b32 s30, s30, 12
	s_add_u32 s28, s26, s30
	s_addc_u32 s29, s27, 0
	global_load_dwordx2 v[56:57], v162, s[28:29]
	v_readlane_b32 s30, v122, 17
	s_lshl_b32 s30, s30, 12
	s_add_u32 s28, s26, s30
	s_addc_u32 s29, s27, 0
	global_load_dwordx2 v[58:59], v162, s[28:29]
	v_readlane_b32 s30, v122, 18
	s_lshl_b32 s30, s30, 12
	s_add_u32 s28, s26, s30
	s_addc_u32 s29, s27, 0
	global_load_dwordx2 v[60:61], v162, s[28:29]
	v_readlane_b32 s30, v122, 19
	s_lshl_b32 s30, s30, 12
	s_add_u32 s28, s26, s30
	s_addc_u32 s29, s27, 0
	global_load_dwordx2 v[62:63], v162, s[28:29]
	v_readlane_b32 s30, v122, 20
	s_lshl_b32 s30, s30, 12
	s_add_u32 s28, s26, s30
	s_addc_u32 s29, s27, 0
	global_load_dwordx2 v[64:65], v162, s[28:29]
	v_readlane_b32 s30, v122, 21
	s_lshl_b32 s30, s30, 12
	s_add_u32 s28, s26, s30
	s_addc_u32 s29, s27, 0
	global_load_dwordx2 v[66:67], v162, s[28:29]
	v_readlane_b32 s30, v122, 22
	s_lshl_b32 s30, s30, 12
	s_add_u32 s28, s26, s30
	s_addc_u32 s29, s27, 0
	global_load_dwordx2 v[68:69], v162, s[28:29]
	v_readlane_b32 s30, v122, 23
	s_lshl_b32 s30, s30, 12
	s_add_u32 s28, s26, s30
	s_addc_u32 s29, s27, 0
	global_load_dwordx2 v[70:71], v162, s[28:29]
	v_readlane_b32 s30, v122, 24
	s_lshl_b32 s30, s30, 12
	s_add_u32 s28, s26, s30
	s_addc_u32 s29, s27, 0
	global_load_dwordx2 v[72:73], v162, s[28:29]
	v_readlane_b32 s30, v122, 25
	s_lshl_b32 s30, s30, 12
	s_add_u32 s28, s26, s30
	s_addc_u32 s29, s27, 0
	global_load_dwordx2 v[74:75], v162, s[28:29]
	v_readlane_b32 s30, v122, 26
	s_lshl_b32 s30, s30, 12
	s_add_u32 s28, s26, s30
	s_addc_u32 s29, s27, 0
	global_load_dwordx2 v[76:77], v162, s[28:29]
	v_readlane_b32 s30, v122, 27
	s_lshl_b32 s30, s30, 12
	s_add_u32 s28, s26, s30
	s_addc_u32 s29, s27, 0
	global_load_dwordx2 v[78:79], v162, s[28:29]
	v_readlane_b32 s30, v122, 28
	s_lshl_b32 s30, s30, 12
	s_add_u32 s28, s26, s30
	s_addc_u32 s29, s27, 0
	global_load_dwordx2 v[80:81], v162, s[28:29]
	v_readlane_b32 s30, v122, 29
	s_lshl_b32 s30, s30, 12
	s_add_u32 s28, s26, s30
	s_addc_u32 s29, s27, 0
	global_load_dwordx2 v[82:83], v162, s[28:29]
	v_readlane_b32 s30, v122, 30
	s_lshl_b32 s30, s30, 12
	s_add_u32 s28, s26, s30
	s_addc_u32 s29, s27, 0
	global_load_dwordx2 v[84:85], v162, s[28:29]
	v_readlane_b32 s30, v122, 31
	s_lshl_b32 s30, s30, 12
	s_add_u32 s28, s26, s30
	s_addc_u32 s29, s27, 0
	global_load_dwordx2 v[86:87], v162, s[28:29]
.Lpa_tok:
	v_lshlrev_b32_e32 v124, 16, v116
	v_and_b32_e32 v125, 0xffff0000, v116
	v_pk_mul_f32 v[108:109], v[124:125], v[100:101]
	v_lshlrev_b32_e32 v124, 16, v117
	v_and_b32_e32 v125, 0xffff0000, v117
	v_pk_mul_f32 v[110:111], v[124:125], v[102:103]
	v_lshlrev_b32_e32 v124, 16, v118
	v_and_b32_e32 v125, 0xffff0000, v118
	v_pk_mul_f32 v[112:113], v[124:125], v[104:105]
	v_lshlrev_b32_e32 v124, 16, v119
	v_and_b32_e32 v125, 0xffff0000, v119
	v_pk_mul_f32 v[114:115], v[124:125], v[106:107]
	v_add_f32_e32 v16, v108, v109
	v_add_f32_e32 v17, v110, v111
	v_add_f32_e32 v18, v112, v113
	v_add_f32_e32 v19, v114, v115
	v_add_f32_e32 v16, v16, v17
	v_add_f32_e32 v18, v18, v19
	v_add_f32_e32 v16, v16, v18
	s_nop 1
	v_add_f32_dpp v17, v16, v16 quad_perm:[1,0,3,2] row_mask:0xf bank_mask:0xf
	s_nop 1
	v_add_f32_dpp v16, v17, v17 quad_perm:[2,3,0,1] row_mask:0xf bank_mask:0xf
	s_nop 1
	v_add_f32_dpp v17, v16, v16 row_half_mirror row_mask:0xf bank_mask:0xf
	s_nop 1
	v_add_f32_dpp v16, v17, v17 row_ror:8 row_mask:0xf bank_mask:0xf
	v_mov_b32_e32 v17, v16
	s_nop 1
	v_permlane16_swap_b32_e32 v16, v17
	v_add_f32_e32 v16, v16, v17
	v_mov_b32_e32 v17, v16
	s_nop 1
	v_permlane32_swap_b32_e32 v16, v17
	v_add_f32_e32 v16, v16, v17
	s_lshl_b32 s30, s16, 7
	s_add_u32 s28, s22, s30
	s_addc_u32 s29, s23, 0
	v_lshlrev_b32_e32 v19, 1, v1
	s_mov_b64 exec, s[2:3]
	global_store_dword v19, v16, s[28:29]
	s_mov_b64 exec, -1
	v_mov_b32_e32 v120, v122
	v_mov_b32_e32 v121, v123
	s_lshl_b32 s30, s16, 9
	v_lshl_add_u64 v[22:23], v[176:177], 0, s[30:31]
	s_add_i32 s18, s16, 1
	s_min_i32 s18, s18, s24
	s_lshl_b32 s30, s18, 13
	v_lshl_add_u64 v[160:161], v[172:173], 0, s[30:31]
	global_load_dwordx4 v[116:119], v[160:161], off
	s_lshl_b32 s30, s18, 9
	v_lshl_add_u64 v[160:161], v[174:175], 0, s[30:31]
	global_load_dword v122, v[160:161], off
	global_load_dword v123, v[160:161], off offset:256
	s_waitcnt vmcnt(34)
	v_cvt_f32_ubyte0_e32 v124, v24
	v_cvt_f32_ubyte1_e32 v126, v24
	v_cvt_f32_ubyte2_e32 v128, v24
	v_cvt_f32_ubyte3_e32 v130, v24
	v_cvt_f32_ubyte0_e32 v132, v25
	v_cvt_f32_ubyte1_e32 v134, v25
	v_cvt_f32_ubyte2_e32 v136, v25
	v_cvt_f32_ubyte3_e32 v138, v25
	v_readlane_b32 s30, v120, 32
	s_lshl_b32 s30, s30, 12
	s_add_u32 s28, s26, s30
	s_addc_u32 s29, s27, 0
	global_load_dwordx2 v[24:25], v162, s[28:29]
	s_waitcnt vmcnt(34)
	v_cvt_f32_ubyte0_e32 v125, v26
	v_cvt_f32_ubyte1_e32 v127, v26
	v_cvt_f32_ubyte2_e32 v129, v26
	v_cvt_f32_ubyte3_e32 v131, v26
	v_cvt_f32_ubyte0_e32 v133, v27
	v_cvt_f32_ubyte1_e32 v135, v27
	v_cvt_f32_ubyte2_e32 v137, v27
	v_cvt_f32_ubyte3_e32 v139, v27
	v_readlane_b32 s30, v120, 33
	s_lshl_b32 s30, s30, 12
	s_add_u32 s28, s26, s30
	s_addc_u32 s29, s27, 0
	global_load_dwordx2 v[26:27], v162, s[28:29]
	s_waitcnt vmcnt(34)
	v_cvt_f32_ubyte0_e32 v140, v28
	v_cvt_f32_ubyte1_e32 v142, v28
	v_cvt_f32_ubyte2_e32 v144, v28
	v_cvt_f32_ubyte3_e32 v146, v28
	v_cvt_f32_ubyte0_e32 v148, v29
	v_cvt_f32_ubyte1_e32 v150, v29
	v_cvt_f32_ubyte2_e32 v152, v29
	v_cvt_f32_ubyte3_e32 v154, v29
	v_readlane_b32 s30, v120, 34
	s_lshl_b32 s30, s30, 12
	s_add_u32 s28, s26, s30
	s_addc_u32 s29, s27, 0
	global_load_dwordx2 v[28:29], v162, s[28:29]
	s_waitcnt vmcnt(34)
	v_cvt_f32_ubyte0_e32 v141, v30
	v_cvt_f32_ubyte1_e32 v143, v30
	v_cvt_f32_ubyte2_e32 v145, v30
	v_cvt_f32_ubyte3_e32 v147, v30
	v_cvt_f32_ubyte0_e32 v149, v31
	v_cvt_f32_ubyte1_e32 v151, v31
	v_cvt_f32_ubyte2_e32 v153, v31
	v_cvt_f32_ubyte3_e32 v155, v31
	v_readlane_b32 s30, v120, 35
	s_lshl_b32 s30, s30, 12
	s_add_u32 s28, s26, s30
	s_addc_u32 s29, s27, 0
	global_load_dwordx2 v[30:31], v162, s[28:29]
	v_mul_f32_e32 v178, v124, v108
	v_mul_f32_e32 v179, v125, v108
	v_mul_f32_e32 v180, v140, v108
	v_mul_f32_e32 v181, v141, v108
	v_fmac_f32_e32 v178, v126, v109
	v_fmac_f32_e32 v179, v127, v109
	v_fmac_f32_e32 v180, v142, v109
	v_fmac_f32_e32 v181, v143, v109
	v_fmac_f32_e32 v178, v128, v110
	v_fmac_f32_e32 v179, v129, v110
	v_fmac_f32_e32 v180, v144, v110
	v_fmac_f32_e32 v181, v145, v110
	v_fmac_f32_e32 v178, v130, v111
	v_fmac_f32_e32 v179, v131, v111
	v_fmac_f32_e32 v180, v146, v111
	v_fmac_f32_e32 v181, v147, v111
	v_fmac_f32_e32 v178, v132, v112
	v_fmac_f32_e32 v179, v133, v112
	v_fmac_f32_e32 v180, v148, v112
	v_fmac_f32_e32 v181, v149, v112
	v_fmac_f32_e32 v178, v134, v113
	v_fmac_f32_e32 v179, v135, v113
	v_fmac_f32_e32 v180, v150, v113
	v_fmac_f32_e32 v181, v151, v113
	v_fmac_f32_e32 v178, v136, v114
	v_fmac_f32_e32 v179, v137, v114
	v_fmac_f32_e32 v180, v152, v114
	v_fmac_f32_e32 v181, v153, v114
	v_fmac_f32_e32 v178, v138, v115
	v_fmac_f32_e32 v179, v139, v115
	v_fmac_f32_e32 v180, v154, v115
	v_fmac_f32_e32 v181, v155, v115
	s_waitcnt vmcnt(34)
	v_cvt_f32_ubyte0_e32 v124, v32
	v_cvt_f32_ubyte1_e32 v126, v32
	v_cvt_f32_ubyte2_e32 v128, v32
	v_cvt_f32_ubyte3_e32 v130, v32
	v_cvt_f32_ubyte0_e32 v132, v33
	v_cvt_f32_ubyte1_e32 v134, v33
	v_cvt_f32_ubyte2_e32 v136, v33
	v_cvt_f32_ubyte3_e32 v138, v33
	v_readlane_b32 s30, v120, 36
	s_lshl_b32 s30, s30, 12
	s_add_u32 s28, s26, s30
	s_addc_u32 s29, s27, 0
	global_load_dwordx2 v[32:33], v162, s[28:29]
	s_waitcnt vmcnt(34)
	v_cvt_f32_ubyte0_e32 v125, v34
	v_cvt_f32_ubyte1_e32 v127, v34
	v_cvt_f32_ubyte2_e32 v129, v34
	v_cvt_f32_ubyte3_e32 v131, v34
	v_cvt_f32_ubyte0_e32 v133, v35
	v_cvt_f32_ubyte1_e32 v135, v35
	v_cvt_f32_ubyte2_e32 v137, v35
	v_cvt_f32_ubyte3_e32 v139, v35
	v_readlane_b32 s30, v120, 37
	s_lshl_b32 s30, s30, 12
	s_add_u32 s28, s26, s30
	s_addc_u32 s29, s27, 0
	global_load_dwordx2 v[34:35], v162, s[28:29]
	s_waitcnt vmcnt(34)
	v_cvt_f32_ubyte0_e32 v140, v36
	v_cvt_f32_ubyte1_e32 v142, v36
	v_cvt_f32_ubyte2_e32 v144, v36
	v_cvt_f32_ubyte3_e32 v146, v36
	v_cvt_f32_ubyte0_e32 v148, v37
	v_cvt_f32_ubyte1_e32 v150, v37
	v_cvt_f32_ubyte2_e32 v152, v37
	v_cvt_f32_ubyte3_e32 v154, v37
	v_readlane_b32 s30, v120, 38
	s_lshl_b32 s30, s30, 12
	s_add_u32 s28, s26, s30
	s_addc_u32 s29, s27, 0
	global_load_dwordx2 v[36:37], v162, s[28:29]
	s_waitcnt vmcnt(34)
	v_cvt_f32_ubyte0_e32 v141, v38
	v_cvt_f32_ubyte1_e32 v143, v38
	v_cvt_f32_ubyte2_e32 v145, v38
	v_cvt_f32_ubyte3_e32 v147, v38
	v_cvt_f32_ubyte0_e32 v149, v39
	v_cvt_f32_ubyte1_e32 v151, v39
	v_cvt_f32_ubyte2_e32 v153, v39
	v_cvt_f32_ubyte3_e32 v155, v39
	v_readlane_b32 s30, v120, 39
	s_lshl_b32 s30, s30, 12
	s_add_u32 s28, s26, s30
	s_addc_u32 s29, s27, 0
	global_load_dwordx2 v[38:39], v162, s[28:29]
	v_mul_f32_e32 v182, v124, v108
	v_mul_f32_e32 v183, v125, v108
	v_mul_f32_e32 v184, v140, v108
	v_mul_f32_e32 v185, v141, v108
	v_fmac_f32_e32 v182, v126, v109
	v_fmac_f32_e32 v183, v127, v109
	v_fmac_f32_e32 v184, v142, v109
	v_fmac_f32_e32 v185, v143, v109
	v_fmac_f32_e32 v182, v128, v110
	v_fmac_f32_e32 v183, v129, v110
	v_fmac_f32_e32 v184, v144, v110
	v_fmac_f32_e32 v185, v145, v110
	v_fmac_f32_e32 v182, v130, v111
	v_fmac_f32_e32 v183, v131, v111
	v_fmac_f32_e32 v184, v146, v111
	v_fmac_f32_e32 v185, v147, v111
	v_fmac_f32_e32 v182, v132, v112
	v_fmac_f32_e32 v183, v133, v112
	v_fmac_f32_e32 v184, v148, v112
	v_fmac_f32_e32 v185, v149, v112
	v_fmac_f32_e32 v182, v134, v113
	v_fmac_f32_e32 v183, v135, v113
	v_fmac_f32_e32 v184, v150, v113
	v_fmac_f32_e32 v185, v151, v113
	v_fmac_f32_e32 v182, v136, v114
	v_fmac_f32_e32 v183, v137, v114
	v_fmac_f32_e32 v184, v152, v114
	v_fmac_f32_e32 v185, v153, v114
	v_fmac_f32_e32 v182, v138, v115
	v_fmac_f32_e32 v183, v139, v115
	v_fmac_f32_e32 v184, v154, v115
	v_fmac_f32_e32 v185, v155, v115
	s_waitcnt vmcnt(34)
	v_cvt_f32_ubyte0_e32 v124, v40
	v_cvt_f32_ubyte1_e32 v126, v40
	v_cvt_f32_ubyte2_e32 v128, v40
	v_cvt_f32_ubyte3_e32 v130, v40
	v_cvt_f32_ubyte0_e32 v132, v41
	v_cvt_f32_ubyte1_e32 v134, v41
	v_cvt_f32_ubyte2_e32 v136, v41
	v_cvt_f32_ubyte3_e32 v138, v41
	v_readlane_b32 s30, v120, 40
	s_lshl_b32 s30, s30, 12
	s_add_u32 s28, s26, s30
	s_addc_u32 s29, s27, 0
	global_load_dwordx2 v[40:41], v162, s[28:29]
	s_waitcnt vmcnt(34)
	v_cvt_f32_ubyte0_e32 v125, v42
	v_cvt_f32_ubyte1_e32 v127, v42
	v_cvt_f32_ubyte2_e32 v129, v42
	v_cvt_f32_ubyte3_e32 v131, v42
	v_cvt_f32_ubyte0_e32 v133, v43
	v_cvt_f32_ubyte1_e32 v135, v43
	v_cvt_f32_ubyte2_e32 v137, v43
	v_cvt_f32_ubyte3_e32 v139, v43
	v_readlane_b32 s30, v120, 41
	s_lshl_b32 s30, s30, 12
	s_add_u32 s28, s26, s30
	s_addc_u32 s29, s27, 0
	global_load_dwordx2 v[42:43], v162, s[28:29]
	s_waitcnt vmcnt(34)
	v_cvt_f32_ubyte0_e32 v140, v44
	v_cvt_f32_ubyte1_e32 v142, v44
	v_cvt_f32_ubyte2_e32 v144, v44
	v_cvt_f32_ubyte3_e32 v146, v44
	v_cvt_f32_ubyte0_e32 v148, v45
	v_cvt_f32_ubyte1_e32 v150, v45
	v_cvt_f32_ubyte2_e32 v152, v45
	v_cvt_f32_ubyte3_e32 v154, v45
	v_readlane_b32 s30, v120, 42
	s_lshl_b32 s30, s30, 12
	s_add_u32 s28, s26, s30
	s_addc_u32 s29, s27, 0
	global_load_dwordx2 v[44:45], v162, s[28:29]
	s_waitcnt vmcnt(34)
	v_cvt_f32_ubyte0_e32 v141, v46
	v_cvt_f32_ubyte1_e32 v143, v46
	v_cvt_f32_ubyte2_e32 v145, v46
	v_cvt_f32_ubyte3_e32 v147, v46
	v_cvt_f32_ubyte0_e32 v149, v47
	v_cvt_f32_ubyte1_e32 v151, v47
	v_cvt_f32_ubyte2_e32 v153, v47
	v_cvt_f32_ubyte3_e32 v155, v47
	v_readlane_b32 s30, v120, 43
	s_lshl_b32 s30, s30, 12
	s_add_u32 s28, s26, s30
	s_addc_u32 s29, s27, 0
	global_load_dwordx2 v[46:47], v162, s[28:29]
	v_mul_f32_e32 v186, v124, v108
	v_mul_f32_e32 v187, v125, v108
	v_mul_f32_e32 v188, v140, v108
	v_mul_f32_e32 v189, v141, v108
	v_fmac_f32_e32 v186, v126, v109
	v_fmac_f32_e32 v187, v127, v109
	v_fmac_f32_e32 v188, v142, v109
	v_fmac_f32_e32 v189, v143, v109
	v_fmac_f32_e32 v186, v128, v110
	v_fmac_f32_e32 v187, v129, v110
	v_fmac_f32_e32 v188, v144, v110
	v_fmac_f32_e32 v189, v145, v110
	v_fmac_f32_e32 v186, v130, v111
	v_fmac_f32_e32 v187, v131, v111
	v_fmac_f32_e32 v188, v146, v111
	v_fmac_f32_e32 v189, v147, v111
	v_fmac_f32_e32 v186, v132, v112
	v_fmac_f32_e32 v187, v133, v112
	v_fmac_f32_e32 v188, v148, v112
	v_fmac_f32_e32 v189, v149, v112
	v_fmac_f32_e32 v186, v134, v113
	v_fmac_f32_e32 v187, v135, v113
	v_fmac_f32_e32 v188, v150, v113
	v_fmac_f32_e32 v189, v151, v113
	v_fmac_f32_e32 v186, v136, v114
	v_fmac_f32_e32 v187, v137, v114
	v_fmac_f32_e32 v188, v152, v114
	v_fmac_f32_e32 v189, v153, v114
	v_fmac_f32_e32 v186, v138, v115
	v_fmac_f32_e32 v187, v139, v115
	v_fmac_f32_e32 v188, v154, v115
	v_fmac_f32_e32 v189, v155, v115
	s_waitcnt vmcnt(34)
	v_cvt_f32_ubyte0_e32 v124, v48
	v_cvt_f32_ubyte1_e32 v126, v48
	v_cvt_f32_ubyte2_e32 v128, v48
	v_cvt_f32_ubyte3_e32 v130, v48
	v_cvt_f32_ubyte0_e32 v132, v49
	v_cvt_f32_ubyte1_e32 v134, v49
	v_cvt_f32_ubyte2_e32 v136, v49
	v_cvt_f32_ubyte3_e32 v138, v49
	v_readlane_b32 s30, v120, 44
	s_lshl_b32 s30, s30, 12
	s_add_u32 s28, s26, s30
	s_addc_u32 s29, s27, 0
	global_load_dwordx2 v[48:49], v162, s[28:29]
	s_waitcnt vmcnt(34)
	v_cvt_f32_ubyte0_e32 v125, v50
	v_cvt_f32_ubyte1_e32 v127, v50
	v_cvt_f32_ubyte2_e32 v129, v50
	v_cvt_f32_ubyte3_e32 v131, v50
	v_cvt_f32_ubyte0_e32 v133, v51
	v_cvt_f32_ubyte1_e32 v135, v51
	v_cvt_f32_ubyte2_e32 v137, v51
	v_cvt_f32_ubyte3_e32 v139, v51
	v_readlane_b32 s30, v120, 45
	s_lshl_b32 s30, s30, 12
	s_add_u32 s28, s26, s30
	s_addc_u32 s29, s27, 0
	global_load_dwordx2 v[50:51], v162, s[28:29]
	s_waitcnt vmcnt(34)
	v_cvt_f32_ubyte0_e32 v140, v52
	v_cvt_f32_ubyte1_e32 v142, v52
	v_cvt_f32_ubyte2_e32 v144, v52
	v_cvt_f32_ubyte3_e32 v146, v52
	v_cvt_f32_ubyte0_e32 v148, v53
	v_cvt_f32_ubyte1_e32 v150, v53
	v_cvt_f32_ubyte2_e32 v152, v53
	v_cvt_f32_ubyte3_e32 v154, v53
	v_readlane_b32 s30, v120, 46
	s_lshl_b32 s30, s30, 12
	s_add_u32 s28, s26, s30
	s_addc_u32 s29, s27, 0
	global_load_dwordx2 v[52:53], v162, s[28:29]
	s_waitcnt vmcnt(34)
	v_cvt_f32_ubyte0_e32 v141, v54
	v_cvt_f32_ubyte1_e32 v143, v54
	v_cvt_f32_ubyte2_e32 v145, v54
	v_cvt_f32_ubyte3_e32 v147, v54
	v_cvt_f32_ubyte0_e32 v149, v55
	v_cvt_f32_ubyte1_e32 v151, v55
	v_cvt_f32_ubyte2_e32 v153, v55
	v_cvt_f32_ubyte3_e32 v155, v55
	v_readlane_b32 s30, v120, 47
	s_lshl_b32 s30, s30, 12
	s_add_u32 s28, s26, s30
	s_addc_u32 s29, s27, 0
	global_load_dwordx2 v[54:55], v162, s[28:29]
	v_mul_f32_e32 v190, v124, v108
	v_mul_f32_e32 v191, v125, v108
	v_mul_f32_e32 v192, v140, v108
	v_mul_f32_e32 v193, v141, v108
	v_fmac_f32_e32 v190, v126, v109
	v_fmac_f32_e32 v191, v127, v109
	v_fmac_f32_e32 v192, v142, v109
	v_fmac_f32_e32 v193, v143, v109
	v_fmac_f32_e32 v190, v128, v110
	v_fmac_f32_e32 v191, v129, v110
	v_fmac_f32_e32 v192, v144, v110
	v_fmac_f32_e32 v193, v145, v110
	v_fmac_f32_e32 v190, v130, v111
	v_fmac_f32_e32 v191, v131, v111
	v_fmac_f32_e32 v192, v146, v111
	v_fmac_f32_e32 v193, v147, v111
	v_fmac_f32_e32 v190, v132, v112
	v_fmac_f32_e32 v191, v133, v112
	v_fmac_f32_e32 v192, v148, v112
	v_fmac_f32_e32 v193, v149, v112
	v_fmac_f32_e32 v190, v134, v113
	v_fmac_f32_e32 v191, v135, v113
	v_fmac_f32_e32 v192, v150, v113
	v_fmac_f32_e32 v193, v151, v113
	v_fmac_f32_e32 v190, v136, v114
	v_fmac_f32_e32 v191, v137, v114
	v_fmac_f32_e32 v192, v152, v114
	v_fmac_f32_e32 v193, v153, v114
	v_fmac_f32_e32 v190, v138, v115
	v_fmac_f32_e32 v191, v139, v115
	v_fmac_f32_e32 v192, v154, v115
	v_fmac_f32_e32 v193, v155, v115
	s_waitcnt vmcnt(34)
	v_cvt_f32_ubyte0_e32 v124, v56
	v_cvt_f32_ubyte1_e32 v126, v56
	v_cvt_f32_ubyte2_e32 v128, v56
	v_cvt_f32_ubyte3_e32 v130, v56
	v_cvt_f32_ubyte0_e32 v132, v57
	v_cvt_f32_ubyte1_e32 v134, v57
	v_cvt_f32_ubyte2_e32 v136, v57
	v_cvt_f32_ubyte3_e32 v138, v57
	v_readlane_b32 s30, v120, 48
	s_lshl_b32 s30, s30, 12
	s_add_u32 s28, s26, s30
	s_addc_u32 s29, s27, 0
	global_load_dwordx2 v[56:57], v162, s[28:29]
	s_waitcnt vmcnt(34)
	v_cvt_f32_ubyte0_e32 v125, v58
	v_cvt_f32_ubyte1_e32 v127, v58
	v_cvt_f32_ubyte2_e32 v129, v58
	v_cvt_f32_ubyte3_e32 v131, v58
	v_cvt_f32_ubyte0_e32 v133, v59
	v_cvt_f32_ubyte1_e32 v135, v59
	v_cvt_f32_ubyte2_e32 v137, v59
	v_cvt_f32_ubyte3_e32 v139, v59
	v_readlane_b32 s30, v120, 49
	s_lshl_b32 s30, s30, 12
	s_add_u32 s28, s26, s30
	s_addc_u32 s29, s27, 0
	global_load_dwordx2 v[58:59], v162, s[28:29]
	s_waitcnt vmcnt(34)
	v_cvt_f32_ubyte0_e32 v140, v60
	v_cvt_f32_ubyte1_e32 v142, v60
	v_cvt_f32_ubyte2_e32 v144, v60
	v_cvt_f32_ubyte3_e32 v146, v60
	v_cvt_f32_ubyte0_e32 v148, v61
	v_cvt_f32_ubyte1_e32 v150, v61
	v_cvt_f32_ubyte2_e32 v152, v61
	v_cvt_f32_ubyte3_e32 v154, v61
	v_readlane_b32 s30, v120, 50
	s_lshl_b32 s30, s30, 12
	s_add_u32 s28, s26, s30
	s_addc_u32 s29, s27, 0
	global_load_dwordx2 v[60:61], v162, s[28:29]
	s_waitcnt vmcnt(34)
	v_cvt_f32_ubyte0_e32 v141, v62
	v_cvt_f32_ubyte1_e32 v143, v62
	v_cvt_f32_ubyte2_e32 v145, v62
	v_cvt_f32_ubyte3_e32 v147, v62
	v_cvt_f32_ubyte0_e32 v149, v63
	v_cvt_f32_ubyte1_e32 v151, v63
	v_cvt_f32_ubyte2_e32 v153, v63
	v_cvt_f32_ubyte3_e32 v155, v63
	v_readlane_b32 s30, v120, 51
	s_lshl_b32 s30, s30, 12
	s_add_u32 s28, s26, s30
	s_addc_u32 s29, s27, 0
	global_load_dwordx2 v[62:63], v162, s[28:29]
	v_mul_f32_e32 v194, v124, v108
	v_mul_f32_e32 v195, v125, v108
	v_mul_f32_e32 v196, v140, v108
	v_mul_f32_e32 v197, v141, v108
	v_fmac_f32_e32 v194, v126, v109
	v_fmac_f32_e32 v195, v127, v109
	v_fmac_f32_e32 v196, v142, v109
	v_fmac_f32_e32 v197, v143, v109
	v_fmac_f32_e32 v194, v128, v110
	v_fmac_f32_e32 v195, v129, v110
	v_fmac_f32_e32 v196, v144, v110
	v_fmac_f32_e32 v197, v145, v110
	v_fmac_f32_e32 v194, v130, v111
	v_fmac_f32_e32 v195, v131, v111
	v_fmac_f32_e32 v196, v146, v111
	v_fmac_f32_e32 v197, v147, v111
	v_fmac_f32_e32 v194, v132, v112
	v_fmac_f32_e32 v195, v133, v112
	v_fmac_f32_e32 v196, v148, v112
	v_fmac_f32_e32 v197, v149, v112
	v_fmac_f32_e32 v194, v134, v113
	v_fmac_f32_e32 v195, v135, v113
	v_fmac_f32_e32 v196, v150, v113
	v_fmac_f32_e32 v197, v151, v113
	v_fmac_f32_e32 v194, v136, v114
	v_fmac_f32_e32 v195, v137, v114
	v_fmac_f32_e32 v196, v152, v114
	v_fmac_f32_e32 v197, v153, v114
	v_fmac_f32_e32 v194, v138, v115
	v_fmac_f32_e32 v195, v139, v115
	v_fmac_f32_e32 v196, v154, v115
	v_fmac_f32_e32 v197, v155, v115
	s_waitcnt vmcnt(34)
	v_cvt_f32_ubyte0_e32 v124, v64
	v_cvt_f32_ubyte1_e32 v126, v64
	v_cvt_f32_ubyte2_e32 v128, v64
	v_cvt_f32_ubyte3_e32 v130, v64
	v_cvt_f32_ubyte0_e32 v132, v65
	v_cvt_f32_ubyte1_e32 v134, v65
	v_cvt_f32_ubyte2_e32 v136, v65
	v_cvt_f32_ubyte3_e32 v138, v65
	v_readlane_b32 s30, v120, 52
	s_lshl_b32 s30, s30, 12
	s_add_u32 s28, s26, s30
	s_addc_u32 s29, s27, 0
	global_load_dwordx2 v[64:65], v162, s[28:29]
	s_waitcnt vmcnt(34)
	v_cvt_f32_ubyte0_e32 v125, v66
	v_cvt_f32_ubyte1_e32 v127, v66
	v_cvt_f32_ubyte2_e32 v129, v66
	v_cvt_f32_ubyte3_e32 v131, v66
	v_cvt_f32_ubyte0_e32 v133, v67
	v_cvt_f32_ubyte1_e32 v135, v67
	v_cvt_f32_ubyte2_e32 v137, v67
	v_cvt_f32_ubyte3_e32 v139, v67
	v_readlane_b32 s30, v120, 53
	s_lshl_b32 s30, s30, 12
	s_add_u32 s28, s26, s30
	s_addc_u32 s29, s27, 0
	global_load_dwordx2 v[66:67], v162, s[28:29]
	s_waitcnt vmcnt(34)
	v_cvt_f32_ubyte0_e32 v140, v68
	v_cvt_f32_ubyte1_e32 v142, v68
	v_cvt_f32_ubyte2_e32 v144, v68
	v_cvt_f32_ubyte3_e32 v146, v68
	v_cvt_f32_ubyte0_e32 v148, v69
	v_cvt_f32_ubyte1_e32 v150, v69
	v_cvt_f32_ubyte2_e32 v152, v69
	v_cvt_f32_ubyte3_e32 v154, v69
	v_readlane_b32 s30, v120, 54
	s_lshl_b32 s30, s30, 12
	s_add_u32 s28, s26, s30
	s_addc_u32 s29, s27, 0
	global_load_dwordx2 v[68:69], v162, s[28:29]
	s_waitcnt vmcnt(34)
	v_cvt_f32_ubyte0_e32 v141, v70
	v_cvt_f32_ubyte1_e32 v143, v70
	v_cvt_f32_ubyte2_e32 v145, v70
	v_cvt_f32_ubyte3_e32 v147, v70
	v_cvt_f32_ubyte0_e32 v149, v71
	v_cvt_f32_ubyte1_e32 v151, v71
	v_cvt_f32_ubyte2_e32 v153, v71
	v_cvt_f32_ubyte3_e32 v155, v71
	v_readlane_b32 s30, v120, 55
	s_lshl_b32 s30, s30, 12
	s_add_u32 s28, s26, s30
	s_addc_u32 s29, s27, 0
	global_load_dwordx2 v[70:71], v162, s[28:29]
	v_mul_f32_e32 v198, v124, v108
	v_mul_f32_e32 v199, v125, v108
	v_mul_f32_e32 v200, v140, v108
	v_mul_f32_e32 v201, v141, v108
	v_fmac_f32_e32 v198, v126, v109
	v_fmac_f32_e32 v199, v127, v109
	v_fmac_f32_e32 v200, v142, v109
	v_fmac_f32_e32 v201, v143, v109
	v_fmac_f32_e32 v198, v128, v110
	v_fmac_f32_e32 v199, v129, v110
	v_fmac_f32_e32 v200, v144, v110
	v_fmac_f32_e32 v201, v145, v110
	v_fmac_f32_e32 v198, v130, v111
	v_fmac_f32_e32 v199, v131, v111
	v_fmac_f32_e32 v200, v146, v111
	v_fmac_f32_e32 v201, v147, v111
	v_fmac_f32_e32 v198, v132, v112
	v_fmac_f32_e32 v199, v133, v112
	v_fmac_f32_e32 v200, v148, v112
	v_fmac_f32_e32 v201, v149, v112
	v_fmac_f32_e32 v198, v134, v113
	v_fmac_f32_e32 v199, v135, v113
	v_fmac_f32_e32 v200, v150, v113
	v_fmac_f32_e32 v201, v151, v113
	v_fmac_f32_e32 v198, v136, v114
	v_fmac_f32_e32 v199, v137, v114
	v_fmac_f32_e32 v200, v152, v114
	v_fmac_f32_e32 v201, v153, v114
	v_fmac_f32_e32 v198, v138, v115
	v_fmac_f32_e32 v199, v139, v115
	v_fmac_f32_e32 v200, v154, v115
	v_fmac_f32_e32 v201, v155, v115
	s_waitcnt vmcnt(34)
	v_cvt_f32_ubyte0_e32 v124, v72
	v_cvt_f32_ubyte1_e32 v126, v72
	v_cvt_f32_ubyte2_e32 v128, v72
	v_cvt_f32_ubyte3_e32 v130, v72
	v_cvt_f32_ubyte0_e32 v132, v73
	v_cvt_f32_ubyte1_e32 v134, v73
	v_cvt_f32_ubyte2_e32 v136, v73
	v_cvt_f32_ubyte3_e32 v138, v73
	v_readlane_b32 s30, v120, 56
	s_lshl_b32 s30, s30, 12
	s_add_u32 s28, s26, s30
	s_addc_u32 s29, s27, 0
	global_load_dwordx2 v[72:73], v162, s[28:29]
	s_waitcnt vmcnt(34)
	v_cvt_f32_ubyte0_e32 v125, v74
	v_cvt_f32_ubyte1_e32 v127, v74
	v_cvt_f32_ubyte2_e32 v129, v74
	v_cvt_f32_ubyte3_e32 v131, v74
	v_cvt_f32_ubyte0_e32 v133, v75
	v_cvt_f32_ubyte1_e32 v135, v75
	v_cvt_f32_ubyte2_e32 v137, v75
	v_cvt_f32_ubyte3_e32 v139, v75
	v_readlane_b32 s30, v120, 57
	s_lshl_b32 s30, s30, 12
	s_add_u32 s28, s26, s30
	s_addc_u32 s29, s27, 0
	global_load_dwordx2 v[74:75], v162, s[28:29]
	s_waitcnt vmcnt(34)
	v_cvt_f32_ubyte0_e32 v140, v76
	v_cvt_f32_ubyte1_e32 v142, v76
	v_cvt_f32_ubyte2_e32 v144, v76
	v_cvt_f32_ubyte3_e32 v146, v76
	v_cvt_f32_ubyte0_e32 v148, v77
	v_cvt_f32_ubyte1_e32 v150, v77
	v_cvt_f32_ubyte2_e32 v152, v77
	v_cvt_f32_ubyte3_e32 v154, v77
	v_readlane_b32 s30, v120, 58
	s_lshl_b32 s30, s30, 12
	s_add_u32 s28, s26, s30
	s_addc_u32 s29, s27, 0
	global_load_dwordx2 v[76:77], v162, s[28:29]
	s_waitcnt vmcnt(34)
	v_cvt_f32_ubyte0_e32 v141, v78
	v_cvt_f32_ubyte1_e32 v143, v78
	v_cvt_f32_ubyte2_e32 v145, v78
	v_cvt_f32_ubyte3_e32 v147, v78
	v_cvt_f32_ubyte0_e32 v149, v79
	v_cvt_f32_ubyte1_e32 v151, v79
	v_cvt_f32_ubyte2_e32 v153, v79
	v_cvt_f32_ubyte3_e32 v155, v79
	v_readlane_b32 s30, v120, 59
	s_lshl_b32 s30, s30, 12
	s_add_u32 s28, s26, s30
	s_addc_u32 s29, s27, 0
	global_load_dwordx2 v[78:79], v162, s[28:29]
	v_mul_f32_e32 v202, v124, v108
	v_mul_f32_e32 v203, v125, v108
	v_mul_f32_e32 v204, v140, v108
	v_mul_f32_e32 v205, v141, v108
	v_fmac_f32_e32 v202, v126, v109
	v_fmac_f32_e32 v203, v127, v109
	v_fmac_f32_e32 v204, v142, v109
	v_fmac_f32_e32 v205, v143, v109
	v_fmac_f32_e32 v202, v128, v110
	v_fmac_f32_e32 v203, v129, v110
	v_fmac_f32_e32 v204, v144, v110
	v_fmac_f32_e32 v205, v145, v110
	v_fmac_f32_e32 v202, v130, v111
	v_fmac_f32_e32 v203, v131, v111
	v_fmac_f32_e32 v204, v146, v111
	v_fmac_f32_e32 v205, v147, v111
	v_fmac_f32_e32 v202, v132, v112
	v_fmac_f32_e32 v203, v133, v112
	v_fmac_f32_e32 v204, v148, v112
	v_fmac_f32_e32 v205, v149, v112
	v_fmac_f32_e32 v202, v134, v113
	v_fmac_f32_e32 v203, v135, v113
	v_fmac_f32_e32 v204, v150, v113
	v_fmac_f32_e32 v205, v151, v113
	v_fmac_f32_e32 v202, v136, v114
	v_fmac_f32_e32 v203, v137, v114
	v_fmac_f32_e32 v204, v152, v114
	v_fmac_f32_e32 v205, v153, v114
	v_fmac_f32_e32 v202, v138, v115
	v_fmac_f32_e32 v203, v139, v115
	v_fmac_f32_e32 v204, v154, v115
	v_fmac_f32_e32 v205, v155, v115
	s_waitcnt vmcnt(34)
	v_cvt_f32_ubyte0_e32 v124, v80
	v_cvt_f32_ubyte1_e32 v126, v80
	v_cvt_f32_ubyte2_e32 v128, v80
	v_cvt_f32_ubyte3_e32 v130, v80
	v_cvt_f32_ubyte0_e32 v132, v81
	v_cvt_f32_ubyte1_e32 v134, v81
	v_cvt_f32_ubyte2_e32 v136, v81
	v_cvt_f32_ubyte3_e32 v138, v81
	v_readlane_b32 s30, v120, 60
	s_lshl_b32 s30, s30, 12
	s_add_u32 s28, s26, s30
	s_addc_u32 s29, s27, 0
	global_load_dwordx2 v[80:81], v162, s[28:29]
	s_waitcnt vmcnt(34)
	v_cvt_f32_ubyte0_e32 v125, v82
	v_cvt_f32_ubyte1_e32 v127, v82
	v_cvt_f32_ubyte2_e32 v129, v82
	v_cvt_f32_ubyte3_e32 v131, v82
	v_cvt_f32_ubyte0_e32 v133, v83
	v_cvt_f32_ubyte1_e32 v135, v83
	v_cvt_f32_ubyte2_e32 v137, v83
	v_cvt_f32_ubyte3_e32 v139, v83
	v_readlane_b32 s30, v120, 61
	s_lshl_b32 s30, s30, 12
	s_add_u32 s28, s26, s30
	s_addc_u32 s29, s27, 0
	global_load_dwordx2 v[82:83], v162, s[28:29]
	s_waitcnt vmcnt(34)
	v_cvt_f32_ubyte0_e32 v140, v84
	v_cvt_f32_ubyte1_e32 v142, v84
	v_cvt_f32_ubyte2_e32 v144, v84
	v_cvt_f32_ubyte3_e32 v146, v84
	v_cvt_f32_ubyte0_e32 v148, v85
	v_cvt_f32_ubyte1_e32 v150, v85
	v_cvt_f32_ubyte2_e32 v152, v85
	v_cvt_f32_ubyte3_e32 v154, v85
	v_readlane_b32 s30, v120, 62
	s_lshl_b32 s30, s30, 12
	s_add_u32 s28, s26, s30
	s_addc_u32 s29, s27, 0
	global_load_dwordx2 v[84:85], v162, s[28:29]
	s_waitcnt vmcnt(34)
	v_cvt_f32_ubyte0_e32 v141, v86
	v_cvt_f32_ubyte1_e32 v143, v86
	v_cvt_f32_ubyte2_e32 v145, v86
	v_cvt_f32_ubyte3_e32 v147, v86
	v_cvt_f32_ubyte0_e32 v149, v87
	v_cvt_f32_ubyte1_e32 v151, v87
	v_cvt_f32_ubyte2_e32 v153, v87
	v_cvt_f32_ubyte3_e32 v155, v87
	v_readlane_b32 s30, v120, 63
	s_lshl_b32 s30, s30, 12
	s_add_u32 s28, s26, s30
	s_addc_u32 s29, s27, 0
	global_load_dwordx2 v[86:87], v162, s[28:29]
	v_mul_f32_e32 v206, v124, v108
	v_mul_f32_e32 v207, v125, v108
	v_mul_f32_e32 v208, v140, v108
	v_mul_f32_e32 v209, v141, v108
	v_fmac_f32_e32 v206, v126, v109
	v_fmac_f32_e32 v207, v127, v109
	v_fmac_f32_e32 v208, v142, v109
	v_fmac_f32_e32 v209, v143, v109
	v_fmac_f32_e32 v206, v128, v110
	v_fmac_f32_e32 v207, v129, v110
	v_fmac_f32_e32 v208, v144, v110
	v_fmac_f32_e32 v209, v145, v110
	v_fmac_f32_e32 v206, v130, v111
	v_fmac_f32_e32 v207, v131, v111
	v_fmac_f32_e32 v208, v146, v111
	v_fmac_f32_e32 v209, v147, v111
	v_fmac_f32_e32 v206, v132, v112
	v_fmac_f32_e32 v207, v133, v112
	v_fmac_f32_e32 v208, v148, v112
	v_fmac_f32_e32 v209, v149, v112
	v_fmac_f32_e32 v206, v134, v113
	v_fmac_f32_e32 v207, v135, v113
	v_fmac_f32_e32 v208, v150, v113
	v_fmac_f32_e32 v209, v151, v113
	v_fmac_f32_e32 v206, v136, v114
	v_fmac_f32_e32 v207, v137, v114
	v_fmac_f32_e32 v208, v152, v114
	v_fmac_f32_e32 v209, v153, v114
	v_fmac_f32_e32 v206, v138, v115
	v_fmac_f32_e32 v207, v139, v115
	v_fmac_f32_e32 v208, v154, v115
	v_fmac_f32_e32 v209, v155, v115
	v_permlane32_swap_b32_e32 v178, v194
	v_permlane32_swap_b32_e32 v179, v195
	v_permlane32_swap_b32_e32 v180, v196
	v_permlane32_swap_b32_e32 v181, v197
	v_permlane32_swap_b32_e32 v182, v198
	v_permlane32_swap_b32_e32 v183, v199
	v_permlane32_swap_b32_e32 v184, v200
	v_permlane32_swap_b32_e32 v185, v201
	v_permlane32_swap_b32_e32 v186, v202
	v_permlane32_swap_b32_e32 v187, v203
	v_permlane32_swap_b32_e32 v188, v204
	v_permlane32_swap_b32_e32 v189, v205
	v_permlane32_swap_b32_e32 v190, v206
	v_permlane32_swap_b32_e32 v191, v207
	v_permlane32_swap_b32_e32 v192, v208
	v_permlane32_swap_b32_e32 v193, v209
	v_add_f32_e32 v178, v178, v194
	v_add_f32_e32 v179, v179, v195
	v_add_f32_e32 v180, v180, v196
	v_add_f32_e32 v181, v181, v197
	v_add_f32_e32 v182, v182, v198
	v_add_f32_e32 v183, v183, v199
	v_add_f32_e32 v184, v184, v200
	v_add_f32_e32 v185, v185, v201
	v_add_f32_e32 v186, v186, v202
	v_add_f32_e32 v187, v187, v203
	v_add_f32_e32 v188, v188, v204
	v_add_f32_e32 v189, v189, v205
	v_add_f32_e32 v190, v190, v206
	v_add_f32_e32 v191, v191, v207
	v_add_f32_e32 v192, v192, v208
	v_add_f32_e32 v193, v193, v209
	v_permlane16_swap_b32_e32 v178, v186
	v_permlane16_swap_b32_e32 v179, v187
	v_permlane16_swap_b32_e32 v180, v188
	v_permlane16_swap_b32_e32 v181, v189
	v_permlane16_swap_b32_e32 v182, v190
	v_permlane16_swap_b32_e32 v183, v191
	v_permlane16_swap_b32_e32 v184, v192
	v_permlane16_swap_b32_e32 v185, v193
	v_add_f32_e32 v178, v178, v186
	v_add_f32_e32 v179, v179, v187
	v_add_f32_e32 v180, v180, v188
	v_add_f32_e32 v181, v181, v189
	v_add_f32_e32 v182, v182, v190
	v_add_f32_e32 v183, v183, v191
	v_add_f32_e32 v184, v184, v192
	v_add_f32_e32 v185, v185, v193
	v_cndmask_b32_e64 v2, v178, v182, s[8:9]
	v_cndmask_b32_e64 v3, v179, v183, s[8:9]
	v_cndmask_b32_e64 v4, v180, v184, s[8:9]
	v_cndmask_b32_e64 v5, v181, v185, s[8:9]
	v_cndmask_b32_e64 v6, v182, v178, s[8:9]
	v_cndmask_b32_e64 v7, v183, v179, s[8:9]
	v_cndmask_b32_e64 v8, v184, v180, s[8:9]
	v_cndmask_b32_e64 v9, v185, v181, s[8:9]
	v_add_f32_dpp v6, v2, v6 row_ror:8 row_mask:0xf bank_mask:0xf
	v_add_f32_dpp v7, v3, v7 row_ror:8 row_mask:0xf bank_mask:0xf
	v_add_f32_dpp v8, v4, v8 row_ror:8 row_mask:0xf bank_mask:0xf
	v_add_f32_dpp v9, v5, v9 row_ror:8 row_mask:0xf bank_mask:0xf
	v_cndmask_b32_e64 v2, v6, v8, s[10:11]
	v_cndmask_b32_e64 v3, v7, v9, s[10:11]
	v_cndmask_b32_e64 v4, v8, v6, s[10:11]
	v_cndmask_b32_e64 v5, v9, v7, s[10:11]
	v_add_f32_dpp v4, v2, v4 row_half_mirror row_mask:0xf bank_mask:0xf
	v_add_f32_dpp v5, v3, v5 row_half_mirror row_mask:0xf bank_mask:0xf
	v_cndmask_b32_e64 v2, v4, v5, s[14:15]
	v_cndmask_b32_e64 v3, v5, v4, s[14:15]
	s_nop 0
	v_add_f32_dpp v3, v2, v3 quad_perm:[2,3,0,1] row_mask:0xf bank_mask:0xf
	s_nop 1
	v_add_f32_dpp v11, v3, v3 quad_perm:[1,0,3,2] row_mask:0xf bank_mask:0xf
	s_mov_b64 exec, s[2:3]
	global_store_dword v[22:23], v11, off
	s_mov_b64 exec, -1
	s_waitcnt vmcnt(32)
	v_cvt_f32_ubyte0_e32 v124, v24
	v_cvt_f32_ubyte1_e32 v126, v24
	v_cvt_f32_ubyte2_e32 v128, v24
	v_cvt_f32_ubyte3_e32 v130, v24
	v_cvt_f32_ubyte0_e32 v132, v25
	v_cvt_f32_ubyte1_e32 v134, v25
	v_cvt_f32_ubyte2_e32 v136, v25
	v_cvt_f32_ubyte3_e32 v138, v25
	v_readlane_b32 s30, v121, 0
	s_lshl_b32 s30, s30, 12
	s_add_u32 s28, s26, s30
	s_addc_u32 s29, s27, 0
	global_load_dwordx2 v[24:25], v162, s[28:29]
	s_waitcnt vmcnt(32)
	v_cvt_f32_ubyte0_e32 v125, v26
	v_cvt_f32_ubyte1_e32 v127, v26
	v_cvt_f32_ubyte2_e32 v129, v26
	v_cvt_f32_ubyte3_e32 v131, v26
	v_cvt_f32_ubyte0_e32 v133, v27
	v_cvt_f32_ubyte1_e32 v135, v27
	v_cvt_f32_ubyte2_e32 v137, v27
	v_cvt_f32_ubyte3_e32 v139, v27
	v_readlane_b32 s30, v121, 1
	s_lshl_b32 s30, s30, 12
	s_add_u32 s28, s26, s30
	s_addc_u32 s29, s27, 0
	global_load_dwordx2 v[26:27], v162, s[28:29]
	s_waitcnt vmcnt(32)
	v_cvt_f32_ubyte0_e32 v140, v28
	v_cvt_f32_ubyte1_e32 v142, v28
	v_cvt_f32_ubyte2_e32 v144, v28
	v_cvt_f32_ubyte3_e32 v146, v28
	v_cvt_f32_ubyte0_e32 v148, v29
	v_cvt_f32_ubyte1_e32 v150, v29
	v_cvt_f32_ubyte2_e32 v152, v29
	v_cvt_f32_ubyte3_e32 v154, v29
	v_readlane_b32 s30, v121, 2
	s_lshl_b32 s30, s30, 12
	s_add_u32 s28, s26, s30
	s_addc_u32 s29, s27, 0
	global_load_dwordx2 v[28:29], v162, s[28:29]
	s_waitcnt vmcnt(32)
	v_cvt_f32_ubyte0_e32 v141, v30
	v_cvt_f32_ubyte1_e32 v143, v30
	v_cvt_f32_ubyte2_e32 v145, v30
	v_cvt_f32_ubyte3_e32 v147, v30
	v_cvt_f32_ubyte0_e32 v149, v31
	v_cvt_f32_ubyte1_e32 v151, v31
	v_cvt_f32_ubyte2_e32 v153, v31
	v_cvt_f32_ubyte3_e32 v155, v31
	v_readlane_b32 s30, v121, 3
	s_lshl_b32 s30, s30, 12
	s_add_u32 s28, s26, s30
	s_addc_u32 s29, s27, 0
	global_load_dwordx2 v[30:31], v162, s[28:29]
	v_mul_f32_e32 v178, v124, v108
	v_mul_f32_e32 v179, v125, v108
	v_mul_f32_e32 v180, v140, v108
	v_mul_f32_e32 v181, v141, v108
	v_fmac_f32_e32 v178, v126, v109
	v_fmac_f32_e32 v179, v127, v109
	v_fmac_f32_e32 v180, v142, v109
	v_fmac_f32_e32 v181, v143, v109
	v_fmac_f32_e32 v178, v128, v110
	v_fmac_f32_e32 v179, v129, v110
	v_fmac_f32_e32 v180, v144, v110
	v_fmac_f32_e32 v181, v145, v110
	v_fmac_f32_e32 v178, v130, v111
	v_fmac_f32_e32 v179, v131, v111
	v_fmac_f32_e32 v180, v146, v111
	v_fmac_f32_e32 v181, v147, v111
	v_fmac_f32_e32 v178, v132, v112
	v_fmac_f32_e32 v179, v133, v112
	v_fmac_f32_e32 v180, v148, v112
	v_fmac_f32_e32 v181, v149, v112
	v_fmac_f32_e32 v178, v134, v113
	v_fmac_f32_e32 v179, v135, v113
	v_fmac_f32_e32 v180, v150, v113
	v_fmac_f32_e32 v181, v151, v113
	v_fmac_f32_e32 v178, v136, v114
	v_fmac_f32_e32 v179, v137, v114
	v_fmac_f32_e32 v180, v152, v114
	v_fmac_f32_e32 v181, v153, v114
	v_fmac_f32_e32 v178, v138, v115
	v_fmac_f32_e32 v179, v139, v115
	v_fmac_f32_e32 v180, v154, v115
	v_fmac_f32_e32 v181, v155, v115
	s_waitcnt vmcnt(32)
	v_cvt_f32_ubyte0_e32 v124, v32
	v_cvt_f32_ubyte1_e32 v126, v32
	v_cvt_f32_ubyte2_e32 v128, v32
	v_cvt_f32_ubyte3_e32 v130, v32
	v_cvt_f32_ubyte0_e32 v132, v33
	v_cvt_f32_ubyte1_e32 v134, v33
	v_cvt_f32_ubyte2_e32 v136, v33
	v_cvt_f32_ubyte3_e32 v138, v33
	v_readlane_b32 s30, v121, 4
	s_lshl_b32 s30, s30, 12
	s_add_u32 s28, s26, s30
	s_addc_u32 s29, s27, 0
	global_load_dwordx2 v[32:33], v162, s[28:29]
	s_waitcnt vmcnt(32)
	v_cvt_f32_ubyte0_e32 v125, v34
	v_cvt_f32_ubyte1_e32 v127, v34
	v_cvt_f32_ubyte2_e32 v129, v34
	v_cvt_f32_ubyte3_e32 v131, v34
	v_cvt_f32_ubyte0_e32 v133, v35
	v_cvt_f32_ubyte1_e32 v135, v35
	v_cvt_f32_ubyte2_e32 v137, v35
	v_cvt_f32_ubyte3_e32 v139, v35
	v_readlane_b32 s30, v121, 5
	s_lshl_b32 s30, s30, 12
	s_add_u32 s28, s26, s30
	s_addc_u32 s29, s27, 0
	global_load_dwordx2 v[34:35], v162, s[28:29]
	s_waitcnt vmcnt(32)
	v_cvt_f32_ubyte0_e32 v140, v36
	v_cvt_f32_ubyte1_e32 v142, v36
	v_cvt_f32_ubyte2_e32 v144, v36
	v_cvt_f32_ubyte3_e32 v146, v36
	v_cvt_f32_ubyte0_e32 v148, v37
	v_cvt_f32_ubyte1_e32 v150, v37
	v_cvt_f32_ubyte2_e32 v152, v37
	v_cvt_f32_ubyte3_e32 v154, v37
	v_readlane_b32 s30, v121, 6
	s_lshl_b32 s30, s30, 12
	s_add_u32 s28, s26, s30
	s_addc_u32 s29, s27, 0
	global_load_dwordx2 v[36:37], v162, s[28:29]
	s_waitcnt vmcnt(32)
	v_cvt_f32_ubyte0_e32 v141, v38
	v_cvt_f32_ubyte1_e32 v143, v38
	v_cvt_f32_ubyte2_e32 v145, v38
	v_cvt_f32_ubyte3_e32 v147, v38
	v_cvt_f32_ubyte0_e32 v149, v39
	v_cvt_f32_ubyte1_e32 v151, v39
	v_cvt_f32_ubyte2_e32 v153, v39
	v_cvt_f32_ubyte3_e32 v155, v39
	v_readlane_b32 s30, v121, 7
	s_lshl_b32 s30, s30, 12
	s_add_u32 s28, s26, s30
	s_addc_u32 s29, s27, 0
	global_load_dwordx2 v[38:39], v162, s[28:29]
	v_mul_f32_e32 v182, v124, v108
	v_mul_f32_e32 v183, v125, v108
	v_mul_f32_e32 v184, v140, v108
	v_mul_f32_e32 v185, v141, v108
	v_fmac_f32_e32 v182, v126, v109
	v_fmac_f32_e32 v183, v127, v109
	v_fmac_f32_e32 v184, v142, v109
	v_fmac_f32_e32 v185, v143, v109
	v_fmac_f32_e32 v182, v128, v110
	v_fmac_f32_e32 v183, v129, v110
	v_fmac_f32_e32 v184, v144, v110
	v_fmac_f32_e32 v185, v145, v110
	v_fmac_f32_e32 v182, v130, v111
	v_fmac_f32_e32 v183, v131, v111
	v_fmac_f32_e32 v184, v146, v111
	v_fmac_f32_e32 v185, v147, v111
	v_fmac_f32_e32 v182, v132, v112
	v_fmac_f32_e32 v183, v133, v112
	v_fmac_f32_e32 v184, v148, v112
	v_fmac_f32_e32 v185, v149, v112
	v_fmac_f32_e32 v182, v134, v113
	v_fmac_f32_e32 v183, v135, v113
	v_fmac_f32_e32 v184, v150, v113
	v_fmac_f32_e32 v185, v151, v113
	v_fmac_f32_e32 v182, v136, v114
	v_fmac_f32_e32 v183, v137, v114
	v_fmac_f32_e32 v184, v152, v114
	v_fmac_f32_e32 v185, v153, v114
	v_fmac_f32_e32 v182, v138, v115
	v_fmac_f32_e32 v183, v139, v115
	v_fmac_f32_e32 v184, v154, v115
	v_fmac_f32_e32 v185, v155, v115
	s_waitcnt vmcnt(32)
	v_cvt_f32_ubyte0_e32 v124, v40
	v_cvt_f32_ubyte1_e32 v126, v40
	v_cvt_f32_ubyte2_e32 v128, v40
	v_cvt_f32_ubyte3_e32 v130, v40
	v_cvt_f32_ubyte0_e32 v132, v41
	v_cvt_f32_ubyte1_e32 v134, v41
	v_cvt_f32_ubyte2_e32 v136, v41
	v_cvt_f32_ubyte3_e32 v138, v41
	v_readlane_b32 s30, v121, 8
	s_lshl_b32 s30, s30, 12
	s_add_u32 s28, s26, s30
	s_addc_u32 s29, s27, 0
	global_load_dwordx2 v[40:41], v162, s[28:29]
	s_waitcnt vmcnt(32)
	v_cvt_f32_ubyte0_e32 v125, v42
	v_cvt_f32_ubyte1_e32 v127, v42
	v_cvt_f32_ubyte2_e32 v129, v42
	v_cvt_f32_ubyte3_e32 v131, v42
	v_cvt_f32_ubyte0_e32 v133, v43
	v_cvt_f32_ubyte1_e32 v135, v43
	v_cvt_f32_ubyte2_e32 v137, v43
	v_cvt_f32_ubyte3_e32 v139, v43
	v_readlane_b32 s30, v121, 9
	s_lshl_b32 s30, s30, 12
	s_add_u32 s28, s26, s30
	s_addc_u32 s29, s27, 0
	global_load_dwordx2 v[42:43], v162, s[28:29]
	s_waitcnt vmcnt(32)
	v_cvt_f32_ubyte0_e32 v140, v44
	v_cvt_f32_ubyte1_e32 v142, v44
	v_cvt_f32_ubyte2_e32 v144, v44
	v_cvt_f32_ubyte3_e32 v146, v44
	v_cvt_f32_ubyte0_e32 v148, v45
	v_cvt_f32_ubyte1_e32 v150, v45
	v_cvt_f32_ubyte2_e32 v152, v45
	v_cvt_f32_ubyte3_e32 v154, v45
	v_readlane_b32 s30, v121, 10
	s_lshl_b32 s30, s30, 12
	s_add_u32 s28, s26, s30
	s_addc_u32 s29, s27, 0
	global_load_dwordx2 v[44:45], v162, s[28:29]
	s_waitcnt vmcnt(32)
	v_cvt_f32_ubyte0_e32 v141, v46
	v_cvt_f32_ubyte1_e32 v143, v46
	v_cvt_f32_ubyte2_e32 v145, v46
	v_cvt_f32_ubyte3_e32 v147, v46
	v_cvt_f32_ubyte0_e32 v149, v47
	v_cvt_f32_ubyte1_e32 v151, v47
	v_cvt_f32_ubyte2_e32 v153, v47
	v_cvt_f32_ubyte3_e32 v155, v47
	v_readlane_b32 s30, v121, 11
	s_lshl_b32 s30, s30, 12
	s_add_u32 s28, s26, s30
	s_addc_u32 s29, s27, 0
	global_load_dwordx2 v[46:47], v162, s[28:29]
	v_mul_f32_e32 v186, v124, v108
	v_mul_f32_e32 v187, v125, v108
	v_mul_f32_e32 v188, v140, v108
	v_mul_f32_e32 v189, v141, v108
	v_fmac_f32_e32 v186, v126, v109
	v_fmac_f32_e32 v187, v127, v109
	v_fmac_f32_e32 v188, v142, v109
	v_fmac_f32_e32 v189, v143, v109
	v_fmac_f32_e32 v186, v128, v110
	v_fmac_f32_e32 v187, v129, v110
	v_fmac_f32_e32 v188, v144, v110
	v_fmac_f32_e32 v189, v145, v110
	v_fmac_f32_e32 v186, v130, v111
	v_fmac_f32_e32 v187, v131, v111
	v_fmac_f32_e32 v188, v146, v111
	v_fmac_f32_e32 v189, v147, v111
	v_fmac_f32_e32 v186, v132, v112
	v_fmac_f32_e32 v187, v133, v112
	v_fmac_f32_e32 v188, v148, v112
	v_fmac_f32_e32 v189, v149, v112
	v_fmac_f32_e32 v186, v134, v113
	v_fmac_f32_e32 v187, v135, v113
	v_fmac_f32_e32 v188, v150, v113
	v_fmac_f32_e32 v189, v151, v113
	v_fmac_f32_e32 v186, v136, v114
	v_fmac_f32_e32 v187, v137, v114
	v_fmac_f32_e32 v188, v152, v114
	v_fmac_f32_e32 v189, v153, v114
	v_fmac_f32_e32 v186, v138, v115
	v_fmac_f32_e32 v187, v139, v115
	v_fmac_f32_e32 v188, v154, v115
	v_fmac_f32_e32 v189, v155, v115
	s_waitcnt vmcnt(32)
	v_cvt_f32_ubyte0_e32 v124, v48
	v_cvt_f32_ubyte1_e32 v126, v48
	v_cvt_f32_ubyte2_e32 v128, v48
	v_cvt_f32_ubyte3_e32 v130, v48
	v_cvt_f32_ubyte0_e32 v132, v49
	v_cvt_f32_ubyte1_e32 v134, v49
	v_cvt_f32_ubyte2_e32 v136, v49
	v_cvt_f32_ubyte3_e32 v138, v49
	v_readlane_b32 s30, v121, 12
	s_lshl_b32 s30, s30, 12
	s_add_u32 s28, s26, s30
	s_addc_u32 s29, s27, 0
	global_load_dwordx2 v[48:49], v162, s[28:29]
	s_waitcnt vmcnt(32)
	v_cvt_f32_ubyte0_e32 v125, v50
	v_cvt_f32_ubyte1_e32 v127, v50
	v_cvt_f32_ubyte2_e32 v129, v50
	v_cvt_f32_ubyte3_e32 v131, v50
	v_cvt_f32_ubyte0_e32 v133, v51
	v_cvt_f32_ubyte1_e32 v135, v51
	v_cvt_f32_ubyte2_e32 v137, v51
	v_cvt_f32_ubyte3_e32 v139, v51
	v_readlane_b32 s30, v121, 13
	s_lshl_b32 s30, s30, 12
	s_add_u32 s28, s26, s30
	s_addc_u32 s29, s27, 0
	global_load_dwordx2 v[50:51], v162, s[28:29]
	s_waitcnt vmcnt(32)
	v_cvt_f32_ubyte0_e32 v140, v52
	v_cvt_f32_ubyte1_e32 v142, v52
	v_cvt_f32_ubyte2_e32 v144, v52
	v_cvt_f32_ubyte3_e32 v146, v52
	v_cvt_f32_ubyte0_e32 v148, v53
	v_cvt_f32_ubyte1_e32 v150, v53
	v_cvt_f32_ubyte2_e32 v152, v53
	v_cvt_f32_ubyte3_e32 v154, v53
	v_readlane_b32 s30, v121, 14
	s_lshl_b32 s30, s30, 12
	s_add_u32 s28, s26, s30
	s_addc_u32 s29, s27, 0
	global_load_dwordx2 v[52:53], v162, s[28:29]
	s_waitcnt vmcnt(32)
	v_cvt_f32_ubyte0_e32 v141, v54
	v_cvt_f32_ubyte1_e32 v143, v54
	v_cvt_f32_ubyte2_e32 v145, v54
	v_cvt_f32_ubyte3_e32 v147, v54
	v_cvt_f32_ubyte0_e32 v149, v55
	v_cvt_f32_ubyte1_e32 v151, v55
	v_cvt_f32_ubyte2_e32 v153, v55
	v_cvt_f32_ubyte3_e32 v155, v55
	v_readlane_b32 s30, v121, 15
	s_lshl_b32 s30, s30, 12
	s_add_u32 s28, s26, s30
	s_addc_u32 s29, s27, 0
	global_load_dwordx2 v[54:55], v162, s[28:29]
	v_mul_f32_e32 v190, v124, v108
	v_mul_f32_e32 v191, v125, v108
	v_mul_f32_e32 v192, v140, v108
	v_mul_f32_e32 v193, v141, v108
	v_fmac_f32_e32 v190, v126, v109
	v_fmac_f32_e32 v191, v127, v109
	v_fmac_f32_e32 v192, v142, v109
	v_fmac_f32_e32 v193, v143, v109
	v_fmac_f32_e32 v190, v128, v110
	v_fmac_f32_e32 v191, v129, v110
	v_fmac_f32_e32 v192, v144, v110
	v_fmac_f32_e32 v193, v145, v110
	v_fmac_f32_e32 v190, v130, v111
	v_fmac_f32_e32 v191, v131, v111
	v_fmac_f32_e32 v192, v146, v111
	v_fmac_f32_e32 v193, v147, v111
	v_fmac_f32_e32 v190, v132, v112
	v_fmac_f32_e32 v191, v133, v112
	v_fmac_f32_e32 v192, v148, v112
	v_fmac_f32_e32 v193, v149, v112
	v_fmac_f32_e32 v190, v134, v113
	v_fmac_f32_e32 v191, v135, v113
	v_fmac_f32_e32 v192, v150, v113
	v_fmac_f32_e32 v193, v151, v113
	v_fmac_f32_e32 v190, v136, v114
	v_fmac_f32_e32 v191, v137, v114
	v_fmac_f32_e32 v192, v152, v114
	v_fmac_f32_e32 v193, v153, v114
	v_fmac_f32_e32 v190, v138, v115
	v_fmac_f32_e32 v191, v139, v115
	v_fmac_f32_e32 v192, v154, v115
	v_fmac_f32_e32 v193, v155, v115
	s_waitcnt vmcnt(32)
	v_cvt_f32_ubyte0_e32 v124, v56
	v_cvt_f32_ubyte1_e32 v126, v56
	v_cvt_f32_ubyte2_e32 v128, v56
	v_cvt_f32_ubyte3_e32 v130, v56
	v_cvt_f32_ubyte0_e32 v132, v57
	v_cvt_f32_ubyte1_e32 v134, v57
	v_cvt_f32_ubyte2_e32 v136, v57
	v_cvt_f32_ubyte3_e32 v138, v57
	v_readlane_b32 s30, v121, 16
	s_lshl_b32 s30, s30, 12
	s_add_u32 s28, s26, s30
	s_addc_u32 s29, s27, 0
	global_load_dwordx2 v[56:57], v162, s[28:29]
	s_waitcnt vmcnt(32)
	v_cvt_f32_ubyte0_e32 v125, v58
	v_cvt_f32_ubyte1_e32 v127, v58
	v_cvt_f32_ubyte2_e32 v129, v58
	v_cvt_f32_ubyte3_e32 v131, v58
	v_cvt_f32_ubyte0_e32 v133, v59
	v_cvt_f32_ubyte1_e32 v135, v59
	v_cvt_f32_ubyte2_e32 v137, v59
	v_cvt_f32_ubyte3_e32 v139, v59
	v_readlane_b32 s30, v121, 17
	s_lshl_b32 s30, s30, 12
	s_add_u32 s28, s26, s30
	s_addc_u32 s29, s27, 0
	global_load_dwordx2 v[58:59], v162, s[28:29]
	s_waitcnt vmcnt(32)
	v_cvt_f32_ubyte0_e32 v140, v60
	v_cvt_f32_ubyte1_e32 v142, v60
	v_cvt_f32_ubyte2_e32 v144, v60
	v_cvt_f32_ubyte3_e32 v146, v60
	v_cvt_f32_ubyte0_e32 v148, v61
	v_cvt_f32_ubyte1_e32 v150, v61
	v_cvt_f32_ubyte2_e32 v152, v61
	v_cvt_f32_ubyte3_e32 v154, v61
	v_readlane_b32 s30, v121, 18
	s_lshl_b32 s30, s30, 12
	s_add_u32 s28, s26, s30
	s_addc_u32 s29, s27, 0
	global_load_dwordx2 v[60:61], v162, s[28:29]
	s_waitcnt vmcnt(32)
	v_cvt_f32_ubyte0_e32 v141, v62
	v_cvt_f32_ubyte1_e32 v143, v62
	v_cvt_f32_ubyte2_e32 v145, v62
	v_cvt_f32_ubyte3_e32 v147, v62
	v_cvt_f32_ubyte0_e32 v149, v63
	v_cvt_f32_ubyte1_e32 v151, v63
	v_cvt_f32_ubyte2_e32 v153, v63
	v_cvt_f32_ubyte3_e32 v155, v63
	v_readlane_b32 s30, v121, 19
	s_lshl_b32 s30, s30, 12
	s_add_u32 s28, s26, s30
	s_addc_u32 s29, s27, 0
	global_load_dwordx2 v[62:63], v162, s[28:29]
	v_mul_f32_e32 v194, v124, v108
	v_mul_f32_e32 v195, v125, v108
	v_mul_f32_e32 v196, v140, v108
	v_mul_f32_e32 v197, v141, v108
	v_fmac_f32_e32 v194, v126, v109
	v_fmac_f32_e32 v195, v127, v109
	v_fmac_f32_e32 v196, v142, v109
	v_fmac_f32_e32 v197, v143, v109
	v_fmac_f32_e32 v194, v128, v110
	v_fmac_f32_e32 v195, v129, v110
	v_fmac_f32_e32 v196, v144, v110
	v_fmac_f32_e32 v197, v145, v110
	v_fmac_f32_e32 v194, v130, v111
	v_fmac_f32_e32 v195, v131, v111
	v_fmac_f32_e32 v196, v146, v111
	v_fmac_f32_e32 v197, v147, v111
	v_fmac_f32_e32 v194, v132, v112
	v_fmac_f32_e32 v195, v133, v112
	v_fmac_f32_e32 v196, v148, v112
	v_fmac_f32_e32 v197, v149, v112
	v_fmac_f32_e32 v194, v134, v113
	v_fmac_f32_e32 v195, v135, v113
	v_fmac_f32_e32 v196, v150, v113
	v_fmac_f32_e32 v197, v151, v113
	v_fmac_f32_e32 v194, v136, v114
	v_fmac_f32_e32 v195, v137, v114
	v_fmac_f32_e32 v196, v152, v114
	v_fmac_f32_e32 v197, v153, v114
	v_fmac_f32_e32 v194, v138, v115
	v_fmac_f32_e32 v195, v139, v115
	v_fmac_f32_e32 v196, v154, v115
	v_fmac_f32_e32 v197, v155, v115
	s_waitcnt vmcnt(32)
	v_cvt_f32_ubyte0_e32 v124, v64
	v_cvt_f32_ubyte1_e32 v126, v64
	v_cvt_f32_ubyte2_e32 v128, v64
	v_cvt_f32_ubyte3_e32 v130, v64
	v_cvt_f32_ubyte0_e32 v132, v65
	v_cvt_f32_ubyte1_e32 v134, v65
	v_cvt_f32_ubyte2_e32 v136, v65
	v_cvt_f32_ubyte3_e32 v138, v65
	v_readlane_b32 s30, v121, 20
	s_lshl_b32 s30, s30, 12
	s_add_u32 s28, s26, s30
	s_addc_u32 s29, s27, 0
	global_load_dwordx2 v[64:65], v162, s[28:29]
	s_waitcnt vmcnt(32)
	v_cvt_f32_ubyte0_e32 v125, v66
	v_cvt_f32_ubyte1_e32 v127, v66
	v_cvt_f32_ubyte2_e32 v129, v66
	v_cvt_f32_ubyte3_e32 v131, v66
	v_cvt_f32_ubyte0_e32 v133, v67
	v_cvt_f32_ubyte1_e32 v135, v67
	v_cvt_f32_ubyte2_e32 v137, v67
	v_cvt_f32_ubyte3_e32 v139, v67
	v_readlane_b32 s30, v121, 21
	s_lshl_b32 s30, s30, 12
	s_add_u32 s28, s26, s30
	s_addc_u32 s29, s27, 0
	global_load_dwordx2 v[66:67], v162, s[28:29]
	s_waitcnt vmcnt(32)
	v_cvt_f32_ubyte0_e32 v140, v68
	v_cvt_f32_ubyte1_e32 v142, v68
	v_cvt_f32_ubyte2_e32 v144, v68
	v_cvt_f32_ubyte3_e32 v146, v68
	v_cvt_f32_ubyte0_e32 v148, v69
	v_cvt_f32_ubyte1_e32 v150, v69
	v_cvt_f32_ubyte2_e32 v152, v69
	v_cvt_f32_ubyte3_e32 v154, v69
	v_readlane_b32 s30, v121, 22
	s_lshl_b32 s30, s30, 12
	s_add_u32 s28, s26, s30
	s_addc_u32 s29, s27, 0
	global_load_dwordx2 v[68:69], v162, s[28:29]
	s_waitcnt vmcnt(32)
	v_cvt_f32_ubyte0_e32 v141, v70
	v_cvt_f32_ubyte1_e32 v143, v70
	v_cvt_f32_ubyte2_e32 v145, v70
	v_cvt_f32_ubyte3_e32 v147, v70
	v_cvt_f32_ubyte0_e32 v149, v71
	v_cvt_f32_ubyte1_e32 v151, v71
	v_cvt_f32_ubyte2_e32 v153, v71
	v_cvt_f32_ubyte3_e32 v155, v71
	v_readlane_b32 s30, v121, 23
	s_lshl_b32 s30, s30, 12
	s_add_u32 s28, s26, s30
	s_addc_u32 s29, s27, 0
	global_load_dwordx2 v[70:71], v162, s[28:29]
	v_mul_f32_e32 v198, v124, v108
	v_mul_f32_e32 v199, v125, v108
	v_mul_f32_e32 v200, v140, v108
	v_mul_f32_e32 v201, v141, v108
	v_fmac_f32_e32 v198, v126, v109
	v_fmac_f32_e32 v199, v127, v109
	v_fmac_f32_e32 v200, v142, v109
	v_fmac_f32_e32 v201, v143, v109
	v_fmac_f32_e32 v198, v128, v110
	v_fmac_f32_e32 v199, v129, v110
	v_fmac_f32_e32 v200, v144, v110
	v_fmac_f32_e32 v201, v145, v110
	v_fmac_f32_e32 v198, v130, v111
	v_fmac_f32_e32 v199, v131, v111
	v_fmac_f32_e32 v200, v146, v111
	v_fmac_f32_e32 v201, v147, v111
	v_fmac_f32_e32 v198, v132, v112
	v_fmac_f32_e32 v199, v133, v112
	v_fmac_f32_e32 v200, v148, v112
	v_fmac_f32_e32 v201, v149, v112
	v_fmac_f32_e32 v198, v134, v113
	v_fmac_f32_e32 v199, v135, v113
	v_fmac_f32_e32 v200, v150, v113
	v_fmac_f32_e32 v201, v151, v113
	v_fmac_f32_e32 v198, v136, v114
	v_fmac_f32_e32 v199, v137, v114
	v_fmac_f32_e32 v200, v152, v114
	v_fmac_f32_e32 v201, v153, v114
	v_fmac_f32_e32 v198, v138, v115
	v_fmac_f32_e32 v199, v139, v115
	v_fmac_f32_e32 v200, v154, v115
	v_fmac_f32_e32 v201, v155, v115
	s_waitcnt vmcnt(32)
	v_cvt_f32_ubyte0_e32 v124, v72
	v_cvt_f32_ubyte1_e32 v126, v72
	v_cvt_f32_ubyte2_e32 v128, v72
	v_cvt_f32_ubyte3_e32 v130, v72
	v_cvt_f32_ubyte0_e32 v132, v73
	v_cvt_f32_ubyte1_e32 v134, v73
	v_cvt_f32_ubyte2_e32 v136, v73
	v_cvt_f32_ubyte3_e32 v138, v73
	v_readlane_b32 s30, v121, 24
	s_lshl_b32 s30, s30, 12
	s_add_u32 s28, s26, s30
	s_addc_u32 s29, s27, 0
	global_load_dwordx2 v[72:73], v162, s[28:29]
	s_waitcnt vmcnt(32)
	v_cvt_f32_ubyte0_e32 v125, v74
	v_cvt_f32_ubyte1_e32 v127, v74
	v_cvt_f32_ubyte2_e32 v129, v74
	v_cvt_f32_ubyte3_e32 v131, v74
	v_cvt_f32_ubyte0_e32 v133, v75
	v_cvt_f32_ubyte1_e32 v135, v75
	v_cvt_f32_ubyte2_e32 v137, v75
	v_cvt_f32_ubyte3_e32 v139, v75
	v_readlane_b32 s30, v121, 25
	s_lshl_b32 s30, s30, 12
	s_add_u32 s28, s26, s30
	s_addc_u32 s29, s27, 0
	global_load_dwordx2 v[74:75], v162, s[28:29]
	s_waitcnt vmcnt(32)
	v_cvt_f32_ubyte0_e32 v140, v76
	v_cvt_f32_ubyte1_e32 v142, v76
	v_cvt_f32_ubyte2_e32 v144, v76
	v_cvt_f32_ubyte3_e32 v146, v76
	v_cvt_f32_ubyte0_e32 v148, v77
	v_cvt_f32_ubyte1_e32 v150, v77
	v_cvt_f32_ubyte2_e32 v152, v77
	v_cvt_f32_ubyte3_e32 v154, v77
	v_readlane_b32 s30, v121, 26
	s_lshl_b32 s30, s30, 12
	s_add_u32 s28, s26, s30
	s_addc_u32 s29, s27, 0
	global_load_dwordx2 v[76:77], v162, s[28:29]
	s_waitcnt vmcnt(32)
	v_cvt_f32_ubyte0_e32 v141, v78
	v_cvt_f32_ubyte1_e32 v143, v78
	v_cvt_f32_ubyte2_e32 v145, v78
	v_cvt_f32_ubyte3_e32 v147, v78
	v_cvt_f32_ubyte0_e32 v149, v79
	v_cvt_f32_ubyte1_e32 v151, v79
	v_cvt_f32_ubyte2_e32 v153, v79
	v_cvt_f32_ubyte3_e32 v155, v79
	v_readlane_b32 s30, v121, 27
	s_lshl_b32 s30, s30, 12
	s_add_u32 s28, s26, s30
	s_addc_u32 s29, s27, 0
	global_load_dwordx2 v[78:79], v162, s[28:29]
	v_mul_f32_e32 v202, v124, v108
	v_mul_f32_e32 v203, v125, v108
	v_mul_f32_e32 v204, v140, v108
	v_mul_f32_e32 v205, v141, v108
	v_fmac_f32_e32 v202, v126, v109
	v_fmac_f32_e32 v203, v127, v109
	v_fmac_f32_e32 v204, v142, v109
	v_fmac_f32_e32 v205, v143, v109
	v_fmac_f32_e32 v202, v128, v110
	v_fmac_f32_e32 v203, v129, v110
	v_fmac_f32_e32 v204, v144, v110
	v_fmac_f32_e32 v205, v145, v110
	v_fmac_f32_e32 v202, v130, v111
	v_fmac_f32_e32 v203, v131, v111
	v_fmac_f32_e32 v204, v146, v111
	v_fmac_f32_e32 v205, v147, v111
	v_fmac_f32_e32 v202, v132, v112
	v_fmac_f32_e32 v203, v133, v112
	v_fmac_f32_e32 v204, v148, v112
	v_fmac_f32_e32 v205, v149, v112
	v_fmac_f32_e32 v202, v134, v113
	v_fmac_f32_e32 v203, v135, v113
	v_fmac_f32_e32 v204, v150, v113
	v_fmac_f32_e32 v205, v151, v113
	v_fmac_f32_e32 v202, v136, v114
	v_fmac_f32_e32 v203, v137, v114
	v_fmac_f32_e32 v204, v152, v114
	v_fmac_f32_e32 v205, v153, v114
	v_fmac_f32_e32 v202, v138, v115
	v_fmac_f32_e32 v203, v139, v115
	v_fmac_f32_e32 v204, v154, v115
	v_fmac_f32_e32 v205, v155, v115
	s_waitcnt vmcnt(32)
	v_cvt_f32_ubyte0_e32 v124, v80
	v_cvt_f32_ubyte1_e32 v126, v80
	v_cvt_f32_ubyte2_e32 v128, v80
	v_cvt_f32_ubyte3_e32 v130, v80
	v_cvt_f32_ubyte0_e32 v132, v81
	v_cvt_f32_ubyte1_e32 v134, v81
	v_cvt_f32_ubyte2_e32 v136, v81
	v_cvt_f32_ubyte3_e32 v138, v81
	v_readlane_b32 s30, v121, 28
	s_lshl_b32 s30, s30, 12
	s_add_u32 s28, s26, s30
	s_addc_u32 s29, s27, 0
	global_load_dwordx2 v[80:81], v162, s[28:29]
	s_waitcnt vmcnt(32)
	v_cvt_f32_ubyte0_e32 v125, v82
	v_cvt_f32_ubyte1_e32 v127, v82
	v_cvt_f32_ubyte2_e32 v129, v82
	v_cvt_f32_ubyte3_e32 v131, v82
	v_cvt_f32_ubyte0_e32 v133, v83
	v_cvt_f32_ubyte1_e32 v135, v83
	v_cvt_f32_ubyte2_e32 v137, v83
	v_cvt_f32_ubyte3_e32 v139, v83
	v_readlane_b32 s30, v121, 29
	s_lshl_b32 s30, s30, 12
	s_add_u32 s28, s26, s30
	s_addc_u32 s29, s27, 0
	global_load_dwordx2 v[82:83], v162, s[28:29]
	s_waitcnt vmcnt(32)
	v_cvt_f32_ubyte0_e32 v140, v84
	v_cvt_f32_ubyte1_e32 v142, v84
	v_cvt_f32_ubyte2_e32 v144, v84
	v_cvt_f32_ubyte3_e32 v146, v84
	v_cvt_f32_ubyte0_e32 v148, v85
	v_cvt_f32_ubyte1_e32 v150, v85
	v_cvt_f32_ubyte2_e32 v152, v85
	v_cvt_f32_ubyte3_e32 v154, v85
	v_readlane_b32 s30, v121, 30
	s_lshl_b32 s30, s30, 12
	s_add_u32 s28, s26, s30
	s_addc_u32 s29, s27, 0
	global_load_dwordx2 v[84:85], v162, s[28:29]
	s_waitcnt vmcnt(32)
	v_cvt_f32_ubyte0_e32 v141, v86
	v_cvt_f32_ubyte1_e32 v143, v86
	v_cvt_f32_ubyte2_e32 v145, v86
	v_cvt_f32_ubyte3_e32 v147, v86
	v_cvt_f32_ubyte0_e32 v149, v87
	v_cvt_f32_ubyte1_e32 v151, v87
	v_cvt_f32_ubyte2_e32 v153, v87
	v_cvt_f32_ubyte3_e32 v155, v87
	v_readlane_b32 s30, v121, 31
	s_lshl_b32 s30, s30, 12
	s_add_u32 s28, s26, s30
	s_addc_u32 s29, s27, 0
	global_load_dwordx2 v[86:87], v162, s[28:29]
	v_mul_f32_e32 v206, v124, v108
	v_mul_f32_e32 v207, v125, v108
	v_mul_f32_e32 v208, v140, v108
	v_mul_f32_e32 v209, v141, v108
	v_fmac_f32_e32 v206, v126, v109
	v_fmac_f32_e32 v207, v127, v109
	v_fmac_f32_e32 v208, v142, v109
	v_fmac_f32_e32 v209, v143, v109
	v_fmac_f32_e32 v206, v128, v110
	v_fmac_f32_e32 v207, v129, v110
	v_fmac_f32_e32 v208, v144, v110
	v_fmac_f32_e32 v209, v145, v110
	v_fmac_f32_e32 v206, v130, v111
	v_fmac_f32_e32 v207, v131, v111
	v_fmac_f32_e32 v208, v146, v111
	v_fmac_f32_e32 v209, v147, v111
	v_fmac_f32_e32 v206, v132, v112
	v_fmac_f32_e32 v207, v133, v112
	v_fmac_f32_e32 v208, v148, v112
	v_fmac_f32_e32 v209, v149, v112
	v_fmac_f32_e32 v206, v134, v113
	v_fmac_f32_e32 v207, v135, v113
	v_fmac_f32_e32 v208, v150, v113
	v_fmac_f32_e32 v209, v151, v113
	v_fmac_f32_e32 v206, v136, v114
	v_fmac_f32_e32 v207, v137, v114
	v_fmac_f32_e32 v208, v152, v114
	v_fmac_f32_e32 v209, v153, v114
	v_fmac_f32_e32 v206, v138, v115
	v_fmac_f32_e32 v207, v139, v115
	v_fmac_f32_e32 v208, v154, v115
	v_fmac_f32_e32 v209, v155, v115
	v_permlane32_swap_b32_e32 v178, v194
	v_permlane32_swap_b32_e32 v179, v195
	v_permlane32_swap_b32_e32 v180, v196
	v_permlane32_swap_b32_e32 v181, v197
	v_permlane32_swap_b32_e32 v182, v198
	v_permlane32_swap_b32_e32 v183, v199
	v_permlane32_swap_b32_e32 v184, v200
	v_permlane32_swap_b32_e32 v185, v201
	v_permlane32_swap_b32_e32 v186, v202
	v_permlane32_swap_b32_e32 v187, v203
	v_permlane32_swap_b32_e32 v188, v204
	v_permlane32_swap_b32_e32 v189, v205
	v_permlane32_swap_b32_e32 v190, v206
	v_permlane32_swap_b32_e32 v191, v207
	v_permlane32_swap_b32_e32 v192, v208
	v_permlane32_swap_b32_e32 v193, v209
	v_add_f32_e32 v178, v178, v194
	v_add_f32_e32 v179, v179, v195
	v_add_f32_e32 v180, v180, v196
	v_add_f32_e32 v181, v181, v197
	v_add_f32_e32 v182, v182, v198
	v_add_f32_e32 v183, v183, v199
	v_add_f32_e32 v184, v184, v200
	v_add_f32_e32 v185, v185, v201
	v_add_f32_e32 v186, v186, v202
	v_add_f32_e32 v187, v187, v203
	v_add_f32_e32 v188, v188, v204
	v_add_f32_e32 v189, v189, v205
	v_add_f32_e32 v190, v190, v206
	v_add_f32_e32 v191, v191, v207
	v_add_f32_e32 v192, v192, v208
	v_add_f32_e32 v193, v193, v209
	v_permlane16_swap_b32_e32 v178, v186
	v_permlane16_swap_b32_e32 v179, v187
	v_permlane16_swap_b32_e32 v180, v188
	v_permlane16_swap_b32_e32 v181, v189
	v_permlane16_swap_b32_e32 v182, v190
	v_permlane16_swap_b32_e32 v183, v191
	v_permlane16_swap_b32_e32 v184, v192
	v_permlane16_swap_b32_e32 v185, v193
	v_add_f32_e32 v178, v178, v186
	v_add_f32_e32 v179, v179, v187
	v_add_f32_e32 v180, v180, v188
	v_add_f32_e32 v181, v181, v189
	v_add_f32_e32 v182, v182, v190
	v_add_f32_e32 v183, v183, v191
	v_add_f32_e32 v184, v184, v192
	v_add_f32_e32 v185, v185, v193
	v_cndmask_b32_e64 v2, v178, v182, s[8:9]
	v_cndmask_b32_e64 v3, v179, v183, s[8:9]
	v_cndmask_b32_e64 v4, v180, v184, s[8:9]
	v_cndmask_b32_e64 v5, v181, v185, s[8:9]
	v_cndmask_b32_e64 v6, v182, v178, s[8:9]
	v_cndmask_b32_e64 v7, v183, v179, s[8:9]
	v_cndmask_b32_e64 v8, v184, v180, s[8:9]
	v_cndmask_b32_e64 v9, v185, v181, s[8:9]
	v_add_f32_dpp v6, v2, v6 row_ror:8 row_mask:0xf bank_mask:0xf
	v_add_f32_dpp v7, v3, v7 row_ror:8 row_mask:0xf bank_mask:0xf
	v_add_f32_dpp v8, v4, v8 row_ror:8 row_mask:0xf bank_mask:0xf
	v_add_f32_dpp v9, v5, v9 row_ror:8 row_mask:0xf bank_mask:0xf
	v_cndmask_b32_e64 v2, v6, v8, s[10:11]
	v_cndmask_b32_e64 v3, v7, v9, s[10:11]
	v_cndmask_b32_e64 v4, v8, v6, s[10:11]
	v_cndmask_b32_e64 v5, v9, v7, s[10:11]
	v_add_f32_dpp v4, v2, v4 row_half_mirror row_mask:0xf bank_mask:0xf
	v_add_f32_dpp v5, v3, v5 row_half_mirror row_mask:0xf bank_mask:0xf
	v_cndmask_b32_e64 v2, v4, v5, s[14:15]
	v_cndmask_b32_e64 v3, v5, v4, s[14:15]
	s_nop 0
	v_add_f32_dpp v3, v2, v3 quad_perm:[2,3,0,1] row_mask:0xf bank_mask:0xf
	s_nop 1
	v_add_f32_dpp v11, v3, v3 quad_perm:[1,0,3,2] row_mask:0xf bank_mask:0xf
	s_mov_b64 exec, s[2:3]
	global_store_dword v[22:23], v11, off offset:128
	s_mov_b64 exec, -1
	s_waitcnt vmcnt(32)
	v_cvt_f32_ubyte0_e32 v124, v24
	v_cvt_f32_ubyte1_e32 v126, v24
	v_cvt_f32_ubyte2_e32 v128, v24
	v_cvt_f32_ubyte3_e32 v130, v24
	v_cvt_f32_ubyte0_e32 v132, v25
	v_cvt_f32_ubyte1_e32 v134, v25
	v_cvt_f32_ubyte2_e32 v136, v25
	v_cvt_f32_ubyte3_e32 v138, v25
	v_readlane_b32 s30, v121, 32
	s_lshl_b32 s30, s30, 12
	s_add_u32 s28, s26, s30
	s_addc_u32 s29, s27, 0
	global_load_dwordx2 v[24:25], v162, s[28:29]
	s_waitcnt vmcnt(32)
	v_cvt_f32_ubyte0_e32 v125, v26
	v_cvt_f32_ubyte1_e32 v127, v26
	v_cvt_f32_ubyte2_e32 v129, v26
	v_cvt_f32_ubyte3_e32 v131, v26
	v_cvt_f32_ubyte0_e32 v133, v27
	v_cvt_f32_ubyte1_e32 v135, v27
	v_cvt_f32_ubyte2_e32 v137, v27
	v_cvt_f32_ubyte3_e32 v139, v27
	v_readlane_b32 s30, v121, 33
	s_lshl_b32 s30, s30, 12
	s_add_u32 s28, s26, s30
	s_addc_u32 s29, s27, 0
	global_load_dwordx2 v[26:27], v162, s[28:29]
	s_waitcnt vmcnt(32)
	v_cvt_f32_ubyte0_e32 v140, v28
	v_cvt_f32_ubyte1_e32 v142, v28
	v_cvt_f32_ubyte2_e32 v144, v28
	v_cvt_f32_ubyte3_e32 v146, v28
	v_cvt_f32_ubyte0_e32 v148, v29
	v_cvt_f32_ubyte1_e32 v150, v29
	v_cvt_f32_ubyte2_e32 v152, v29
	v_cvt_f32_ubyte3_e32 v154, v29
	v_readlane_b32 s30, v121, 34
	s_lshl_b32 s30, s30, 12
	s_add_u32 s28, s26, s30
	s_addc_u32 s29, s27, 0
	global_load_dwordx2 v[28:29], v162, s[28:29]
	s_waitcnt vmcnt(32)
	v_cvt_f32_ubyte0_e32 v141, v30
	v_cvt_f32_ubyte1_e32 v143, v30
	v_cvt_f32_ubyte2_e32 v145, v30
	v_cvt_f32_ubyte3_e32 v147, v30
	v_cvt_f32_ubyte0_e32 v149, v31
	v_cvt_f32_ubyte1_e32 v151, v31
	v_cvt_f32_ubyte2_e32 v153, v31
	v_cvt_f32_ubyte3_e32 v155, v31
	v_readlane_b32 s30, v121, 35
	s_lshl_b32 s30, s30, 12
	s_add_u32 s28, s26, s30
	s_addc_u32 s29, s27, 0
	global_load_dwordx2 v[30:31], v162, s[28:29]
	v_mul_f32_e32 v178, v124, v108
	v_mul_f32_e32 v179, v125, v108
	v_mul_f32_e32 v180, v140, v108
	v_mul_f32_e32 v181, v141, v108
	v_fmac_f32_e32 v178, v126, v109
	v_fmac_f32_e32 v179, v127, v109
	v_fmac_f32_e32 v180, v142, v109
	v_fmac_f32_e32 v181, v143, v109
	v_fmac_f32_e32 v178, v128, v110
	v_fmac_f32_e32 v179, v129, v110
	v_fmac_f32_e32 v180, v144, v110
	v_fmac_f32_e32 v181, v145, v110
	v_fmac_f32_e32 v178, v130, v111
	v_fmac_f32_e32 v179, v131, v111
	v_fmac_f32_e32 v180, v146, v111
	v_fmac_f32_e32 v181, v147, v111
	v_fmac_f32_e32 v178, v132, v112
	v_fmac_f32_e32 v179, v133, v112
	v_fmac_f32_e32 v180, v148, v112
	v_fmac_f32_e32 v181, v149, v112
	v_fmac_f32_e32 v178, v134, v113
	v_fmac_f32_e32 v179, v135, v113
	v_fmac_f32_e32 v180, v150, v113
	v_fmac_f32_e32 v181, v151, v113
	v_fmac_f32_e32 v178, v136, v114
	v_fmac_f32_e32 v179, v137, v114
	v_fmac_f32_e32 v180, v152, v114
	v_fmac_f32_e32 v181, v153, v114
	v_fmac_f32_e32 v178, v138, v115
	v_fmac_f32_e32 v179, v139, v115
	v_fmac_f32_e32 v180, v154, v115
	v_fmac_f32_e32 v181, v155, v115
	s_waitcnt vmcnt(32)
	v_cvt_f32_ubyte0_e32 v124, v32
	v_cvt_f32_ubyte1_e32 v126, v32
	v_cvt_f32_ubyte2_e32 v128, v32
	v_cvt_f32_ubyte3_e32 v130, v32
	v_cvt_f32_ubyte0_e32 v132, v33
	v_cvt_f32_ubyte1_e32 v134, v33
	v_cvt_f32_ubyte2_e32 v136, v33
	v_cvt_f32_ubyte3_e32 v138, v33
	v_readlane_b32 s30, v121, 36
	s_lshl_b32 s30, s30, 12
	s_add_u32 s28, s26, s30
	s_addc_u32 s29, s27, 0
	global_load_dwordx2 v[32:33], v162, s[28:29]
	s_waitcnt vmcnt(32)
	v_cvt_f32_ubyte0_e32 v125, v34
	v_cvt_f32_ubyte1_e32 v127, v34
	v_cvt_f32_ubyte2_e32 v129, v34
	v_cvt_f32_ubyte3_e32 v131, v34
	v_cvt_f32_ubyte0_e32 v133, v35
	v_cvt_f32_ubyte1_e32 v135, v35
	v_cvt_f32_ubyte2_e32 v137, v35
	v_cvt_f32_ubyte3_e32 v139, v35
	v_readlane_b32 s30, v121, 37
	s_lshl_b32 s30, s30, 12
	s_add_u32 s28, s26, s30
	s_addc_u32 s29, s27, 0
	global_load_dwordx2 v[34:35], v162, s[28:29]
	s_waitcnt vmcnt(32)
	v_cvt_f32_ubyte0_e32 v140, v36
	v_cvt_f32_ubyte1_e32 v142, v36
	v_cvt_f32_ubyte2_e32 v144, v36
	v_cvt_f32_ubyte3_e32 v146, v36
	v_cvt_f32_ubyte0_e32 v148, v37
	v_cvt_f32_ubyte1_e32 v150, v37
	v_cvt_f32_ubyte2_e32 v152, v37
	v_cvt_f32_ubyte3_e32 v154, v37
	v_readlane_b32 s30, v121, 38
	s_lshl_b32 s30, s30, 12
	s_add_u32 s28, s26, s30
	s_addc_u32 s29, s27, 0
	global_load_dwordx2 v[36:37], v162, s[28:29]
	s_waitcnt vmcnt(32)
	v_cvt_f32_ubyte0_e32 v141, v38
	v_cvt_f32_ubyte1_e32 v143, v38
	v_cvt_f32_ubyte2_e32 v145, v38
	v_cvt_f32_ubyte3_e32 v147, v38
	v_cvt_f32_ubyte0_e32 v149, v39
	v_cvt_f32_ubyte1_e32 v151, v39
	v_cvt_f32_ubyte2_e32 v153, v39
	v_cvt_f32_ubyte3_e32 v155, v39
	v_readlane_b32 s30, v121, 39
	s_lshl_b32 s30, s30, 12
	s_add_u32 s28, s26, s30
	s_addc_u32 s29, s27, 0
	global_load_dwordx2 v[38:39], v162, s[28:29]
	v_mul_f32_e32 v182, v124, v108
	v_mul_f32_e32 v183, v125, v108
	v_mul_f32_e32 v184, v140, v108
	v_mul_f32_e32 v185, v141, v108
	v_fmac_f32_e32 v182, v126, v109
	v_fmac_f32_e32 v183, v127, v109
	v_fmac_f32_e32 v184, v142, v109
	v_fmac_f32_e32 v185, v143, v109
	v_fmac_f32_e32 v182, v128, v110
	v_fmac_f32_e32 v183, v129, v110
	v_fmac_f32_e32 v184, v144, v110
	v_fmac_f32_e32 v185, v145, v110
	v_fmac_f32_e32 v182, v130, v111
	v_fmac_f32_e32 v183, v131, v111
	v_fmac_f32_e32 v184, v146, v111
	v_fmac_f32_e32 v185, v147, v111
	v_fmac_f32_e32 v182, v132, v112
	v_fmac_f32_e32 v183, v133, v112
	v_fmac_f32_e32 v184, v148, v112
	v_fmac_f32_e32 v185, v149, v112
	v_fmac_f32_e32 v182, v134, v113
	v_fmac_f32_e32 v183, v135, v113
	v_fmac_f32_e32 v184, v150, v113
	v_fmac_f32_e32 v185, v151, v113
	v_fmac_f32_e32 v182, v136, v114
	v_fmac_f32_e32 v183, v137, v114
	v_fmac_f32_e32 v184, v152, v114
	v_fmac_f32_e32 v185, v153, v114
	v_fmac_f32_e32 v182, v138, v115
	v_fmac_f32_e32 v183, v139, v115
	v_fmac_f32_e32 v184, v154, v115
	v_fmac_f32_e32 v185, v155, v115
	s_waitcnt vmcnt(32)
	v_cvt_f32_ubyte0_e32 v124, v40
	v_cvt_f32_ubyte1_e32 v126, v40
	v_cvt_f32_ubyte2_e32 v128, v40
	v_cvt_f32_ubyte3_e32 v130, v40
	v_cvt_f32_ubyte0_e32 v132, v41
	v_cvt_f32_ubyte1_e32 v134, v41
	v_cvt_f32_ubyte2_e32 v136, v41
	v_cvt_f32_ubyte3_e32 v138, v41
	v_readlane_b32 s30, v121, 40
	s_lshl_b32 s30, s30, 12
	s_add_u32 s28, s26, s30
	s_addc_u32 s29, s27, 0
	global_load_dwordx2 v[40:41], v162, s[28:29]
	s_waitcnt vmcnt(32)
	v_cvt_f32_ubyte0_e32 v125, v42
	v_cvt_f32_ubyte1_e32 v127, v42
	v_cvt_f32_ubyte2_e32 v129, v42
	v_cvt_f32_ubyte3_e32 v131, v42
	v_cvt_f32_ubyte0_e32 v133, v43
	v_cvt_f32_ubyte1_e32 v135, v43
	v_cvt_f32_ubyte2_e32 v137, v43
	v_cvt_f32_ubyte3_e32 v139, v43
	v_readlane_b32 s30, v121, 41
	s_lshl_b32 s30, s30, 12
	s_add_u32 s28, s26, s30
	s_addc_u32 s29, s27, 0
	global_load_dwordx2 v[42:43], v162, s[28:29]
	s_waitcnt vmcnt(32)
	v_cvt_f32_ubyte0_e32 v140, v44
	v_cvt_f32_ubyte1_e32 v142, v44
	v_cvt_f32_ubyte2_e32 v144, v44
	v_cvt_f32_ubyte3_e32 v146, v44
	v_cvt_f32_ubyte0_e32 v148, v45
	v_cvt_f32_ubyte1_e32 v150, v45
	v_cvt_f32_ubyte2_e32 v152, v45
	v_cvt_f32_ubyte3_e32 v154, v45
	v_readlane_b32 s30, v121, 42
	s_lshl_b32 s30, s30, 12
	s_add_u32 s28, s26, s30
	s_addc_u32 s29, s27, 0
	global_load_dwordx2 v[44:45], v162, s[28:29]
	s_waitcnt vmcnt(32)
	v_cvt_f32_ubyte0_e32 v141, v46
	v_cvt_f32_ubyte1_e32 v143, v46
	v_cvt_f32_ubyte2_e32 v145, v46
	v_cvt_f32_ubyte3_e32 v147, v46
	v_cvt_f32_ubyte0_e32 v149, v47
	v_cvt_f32_ubyte1_e32 v151, v47
	v_cvt_f32_ubyte2_e32 v153, v47
	v_cvt_f32_ubyte3_e32 v155, v47
	v_readlane_b32 s30, v121, 43
	s_lshl_b32 s30, s30, 12
	s_add_u32 s28, s26, s30
	s_addc_u32 s29, s27, 0
	global_load_dwordx2 v[46:47], v162, s[28:29]
	v_mul_f32_e32 v186, v124, v108
	v_mul_f32_e32 v187, v125, v108
	v_mul_f32_e32 v188, v140, v108
	v_mul_f32_e32 v189, v141, v108
	v_fmac_f32_e32 v186, v126, v109
	v_fmac_f32_e32 v187, v127, v109
	v_fmac_f32_e32 v188, v142, v109
	v_fmac_f32_e32 v189, v143, v109
	v_fmac_f32_e32 v186, v128, v110
	v_fmac_f32_e32 v187, v129, v110
	v_fmac_f32_e32 v188, v144, v110
	v_fmac_f32_e32 v189, v145, v110
	v_fmac_f32_e32 v186, v130, v111
	v_fmac_f32_e32 v187, v131, v111
	v_fmac_f32_e32 v188, v146, v111
	v_fmac_f32_e32 v189, v147, v111
	v_fmac_f32_e32 v186, v132, v112
	v_fmac_f32_e32 v187, v133, v112
	v_fmac_f32_e32 v188, v148, v112
	v_fmac_f32_e32 v189, v149, v112
	v_fmac_f32_e32 v186, v134, v113
	v_fmac_f32_e32 v187, v135, v113
	v_fmac_f32_e32 v188, v150, v113
	v_fmac_f32_e32 v189, v151, v113
	v_fmac_f32_e32 v186, v136, v114
	v_fmac_f32_e32 v187, v137, v114
	v_fmac_f32_e32 v188, v152, v114
	v_fmac_f32_e32 v189, v153, v114
	v_fmac_f32_e32 v186, v138, v115
	v_fmac_f32_e32 v187, v139, v115
	v_fmac_f32_e32 v188, v154, v115
	v_fmac_f32_e32 v189, v155, v115
	s_waitcnt vmcnt(32)
	v_cvt_f32_ubyte0_e32 v124, v48
	v_cvt_f32_ubyte1_e32 v126, v48
	v_cvt_f32_ubyte2_e32 v128, v48
	v_cvt_f32_ubyte3_e32 v130, v48
	v_cvt_f32_ubyte0_e32 v132, v49
	v_cvt_f32_ubyte1_e32 v134, v49
	v_cvt_f32_ubyte2_e32 v136, v49
	v_cvt_f32_ubyte3_e32 v138, v49
	v_readlane_b32 s30, v121, 44
	s_lshl_b32 s30, s30, 12
	s_add_u32 s28, s26, s30
	s_addc_u32 s29, s27, 0
	global_load_dwordx2 v[48:49], v162, s[28:29]
	s_waitcnt vmcnt(32)
	v_cvt_f32_ubyte0_e32 v125, v50
	v_cvt_f32_ubyte1_e32 v127, v50
	v_cvt_f32_ubyte2_e32 v129, v50
	v_cvt_f32_ubyte3_e32 v131, v50
	v_cvt_f32_ubyte0_e32 v133, v51
	v_cvt_f32_ubyte1_e32 v135, v51
	v_cvt_f32_ubyte2_e32 v137, v51
	v_cvt_f32_ubyte3_e32 v139, v51
	v_readlane_b32 s30, v121, 45
	s_lshl_b32 s30, s30, 12
	s_add_u32 s28, s26, s30
	s_addc_u32 s29, s27, 0
	global_load_dwordx2 v[50:51], v162, s[28:29]
	s_waitcnt vmcnt(32)
	v_cvt_f32_ubyte0_e32 v140, v52
	v_cvt_f32_ubyte1_e32 v142, v52
	v_cvt_f32_ubyte2_e32 v144, v52
	v_cvt_f32_ubyte3_e32 v146, v52
	v_cvt_f32_ubyte0_e32 v148, v53
	v_cvt_f32_ubyte1_e32 v150, v53
	v_cvt_f32_ubyte2_e32 v152, v53
	v_cvt_f32_ubyte3_e32 v154, v53
	v_readlane_b32 s30, v121, 46
	s_lshl_b32 s30, s30, 12
	s_add_u32 s28, s26, s30
	s_addc_u32 s29, s27, 0
	global_load_dwordx2 v[52:53], v162, s[28:29]
	s_waitcnt vmcnt(32)
	v_cvt_f32_ubyte0_e32 v141, v54
	v_cvt_f32_ubyte1_e32 v143, v54
	v_cvt_f32_ubyte2_e32 v145, v54
	v_cvt_f32_ubyte3_e32 v147, v54
	v_cvt_f32_ubyte0_e32 v149, v55
	v_cvt_f32_ubyte1_e32 v151, v55
	v_cvt_f32_ubyte2_e32 v153, v55
	v_cvt_f32_ubyte3_e32 v155, v55
	v_readlane_b32 s30, v121, 47
	s_lshl_b32 s30, s30, 12
	s_add_u32 s28, s26, s30
	s_addc_u32 s29, s27, 0
	global_load_dwordx2 v[54:55], v162, s[28:29]
	v_mul_f32_e32 v190, v124, v108
	v_mul_f32_e32 v191, v125, v108
	v_mul_f32_e32 v192, v140, v108
	v_mul_f32_e32 v193, v141, v108
	v_fmac_f32_e32 v190, v126, v109
	v_fmac_f32_e32 v191, v127, v109
	v_fmac_f32_e32 v192, v142, v109
	v_fmac_f32_e32 v193, v143, v109
	v_fmac_f32_e32 v190, v128, v110
	v_fmac_f32_e32 v191, v129, v110
	v_fmac_f32_e32 v192, v144, v110
	v_fmac_f32_e32 v193, v145, v110
	v_fmac_f32_e32 v190, v130, v111
	v_fmac_f32_e32 v191, v131, v111
	v_fmac_f32_e32 v192, v146, v111
	v_fmac_f32_e32 v193, v147, v111
	v_fmac_f32_e32 v190, v132, v112
	v_fmac_f32_e32 v191, v133, v112
	v_fmac_f32_e32 v192, v148, v112
	v_fmac_f32_e32 v193, v149, v112
	v_fmac_f32_e32 v190, v134, v113
	v_fmac_f32_e32 v191, v135, v113
	v_fmac_f32_e32 v192, v150, v113
	v_fmac_f32_e32 v193, v151, v113
	v_fmac_f32_e32 v190, v136, v114
	v_fmac_f32_e32 v191, v137, v114
	v_fmac_f32_e32 v192, v152, v114
	v_fmac_f32_e32 v193, v153, v114
	v_fmac_f32_e32 v190, v138, v115
	v_fmac_f32_e32 v191, v139, v115
	v_fmac_f32_e32 v192, v154, v115
	v_fmac_f32_e32 v193, v155, v115
	s_waitcnt vmcnt(32)
	v_cvt_f32_ubyte0_e32 v124, v56
	v_cvt_f32_ubyte1_e32 v126, v56
	v_cvt_f32_ubyte2_e32 v128, v56
	v_cvt_f32_ubyte3_e32 v130, v56
	v_cvt_f32_ubyte0_e32 v132, v57
	v_cvt_f32_ubyte1_e32 v134, v57
	v_cvt_f32_ubyte2_e32 v136, v57
	v_cvt_f32_ubyte3_e32 v138, v57
	v_readlane_b32 s30, v121, 48
	s_lshl_b32 s30, s30, 12
	s_add_u32 s28, s26, s30
	s_addc_u32 s29, s27, 0
	global_load_dwordx2 v[56:57], v162, s[28:29]
	s_waitcnt vmcnt(32)
	v_cvt_f32_ubyte0_e32 v125, v58
	v_cvt_f32_ubyte1_e32 v127, v58
	v_cvt_f32_ubyte2_e32 v129, v58
	v_cvt_f32_ubyte3_e32 v131, v58
	v_cvt_f32_ubyte0_e32 v133, v59
	v_cvt_f32_ubyte1_e32 v135, v59
	v_cvt_f32_ubyte2_e32 v137, v59
	v_cvt_f32_ubyte3_e32 v139, v59
	v_readlane_b32 s30, v121, 49
	s_lshl_b32 s30, s30, 12
	s_add_u32 s28, s26, s30
	s_addc_u32 s29, s27, 0
	global_load_dwordx2 v[58:59], v162, s[28:29]
	s_waitcnt vmcnt(32)
	v_cvt_f32_ubyte0_e32 v140, v60
	v_cvt_f32_ubyte1_e32 v142, v60
	v_cvt_f32_ubyte2_e32 v144, v60
	v_cvt_f32_ubyte3_e32 v146, v60
	v_cvt_f32_ubyte0_e32 v148, v61
	v_cvt_f32_ubyte1_e32 v150, v61
	v_cvt_f32_ubyte2_e32 v152, v61
	v_cvt_f32_ubyte3_e32 v154, v61
	v_readlane_b32 s30, v121, 50
	s_lshl_b32 s30, s30, 12
	s_add_u32 s28, s26, s30
	s_addc_u32 s29, s27, 0
	global_load_dwordx2 v[60:61], v162, s[28:29]
	s_waitcnt vmcnt(32)
	v_cvt_f32_ubyte0_e32 v141, v62
	v_cvt_f32_ubyte1_e32 v143, v62
	v_cvt_f32_ubyte2_e32 v145, v62
	v_cvt_f32_ubyte3_e32 v147, v62
	v_cvt_f32_ubyte0_e32 v149, v63
	v_cvt_f32_ubyte1_e32 v151, v63
	v_cvt_f32_ubyte2_e32 v153, v63
	v_cvt_f32_ubyte3_e32 v155, v63
	v_readlane_b32 s30, v121, 51
	s_lshl_b32 s30, s30, 12
	s_add_u32 s28, s26, s30
	s_addc_u32 s29, s27, 0
	global_load_dwordx2 v[62:63], v162, s[28:29]
	v_mul_f32_e32 v194, v124, v108
	v_mul_f32_e32 v195, v125, v108
	v_mul_f32_e32 v196, v140, v108
	v_mul_f32_e32 v197, v141, v108
	v_fmac_f32_e32 v194, v126, v109
	v_fmac_f32_e32 v195, v127, v109
	v_fmac_f32_e32 v196, v142, v109
	v_fmac_f32_e32 v197, v143, v109
	v_fmac_f32_e32 v194, v128, v110
	v_fmac_f32_e32 v195, v129, v110
	v_fmac_f32_e32 v196, v144, v110
	v_fmac_f32_e32 v197, v145, v110
	v_fmac_f32_e32 v194, v130, v111
	v_fmac_f32_e32 v195, v131, v111
	v_fmac_f32_e32 v196, v146, v111
	v_fmac_f32_e32 v197, v147, v111
	v_fmac_f32_e32 v194, v132, v112
	v_fmac_f32_e32 v195, v133, v112
	v_fmac_f32_e32 v196, v148, v112
	v_fmac_f32_e32 v197, v149, v112
	v_fmac_f32_e32 v194, v134, v113
	v_fmac_f32_e32 v195, v135, v113
	v_fmac_f32_e32 v196, v150, v113
	v_fmac_f32_e32 v197, v151, v113
	v_fmac_f32_e32 v194, v136, v114
	v_fmac_f32_e32 v195, v137, v114
	v_fmac_f32_e32 v196, v152, v114
	v_fmac_f32_e32 v197, v153, v114
	v_fmac_f32_e32 v194, v138, v115
	v_fmac_f32_e32 v195, v139, v115
	v_fmac_f32_e32 v196, v154, v115
	v_fmac_f32_e32 v197, v155, v115
	s_waitcnt vmcnt(32)
	v_cvt_f32_ubyte0_e32 v124, v64
	v_cvt_f32_ubyte1_e32 v126, v64
	v_cvt_f32_ubyte2_e32 v128, v64
	v_cvt_f32_ubyte3_e32 v130, v64
	v_cvt_f32_ubyte0_e32 v132, v65
	v_cvt_f32_ubyte1_e32 v134, v65
	v_cvt_f32_ubyte2_e32 v136, v65
	v_cvt_f32_ubyte3_e32 v138, v65
	v_readlane_b32 s30, v121, 52
	s_lshl_b32 s30, s30, 12
	s_add_u32 s28, s26, s30
	s_addc_u32 s29, s27, 0
	global_load_dwordx2 v[64:65], v162, s[28:29]
	s_waitcnt vmcnt(32)
	v_cvt_f32_ubyte0_e32 v125, v66
	v_cvt_f32_ubyte1_e32 v127, v66
	v_cvt_f32_ubyte2_e32 v129, v66
	v_cvt_f32_ubyte3_e32 v131, v66
	v_cvt_f32_ubyte0_e32 v133, v67
	v_cvt_f32_ubyte1_e32 v135, v67
	v_cvt_f32_ubyte2_e32 v137, v67
	v_cvt_f32_ubyte3_e32 v139, v67
	v_readlane_b32 s30, v121, 53
	s_lshl_b32 s30, s30, 12
	s_add_u32 s28, s26, s30
	s_addc_u32 s29, s27, 0
	global_load_dwordx2 v[66:67], v162, s[28:29]
	s_waitcnt vmcnt(32)
	v_cvt_f32_ubyte0_e32 v140, v68
	v_cvt_f32_ubyte1_e32 v142, v68
	v_cvt_f32_ubyte2_e32 v144, v68
	v_cvt_f32_ubyte3_e32 v146, v68
	v_cvt_f32_ubyte0_e32 v148, v69
	v_cvt_f32_ubyte1_e32 v150, v69
	v_cvt_f32_ubyte2_e32 v152, v69
	v_cvt_f32_ubyte3_e32 v154, v69
	v_readlane_b32 s30, v121, 54
	s_lshl_b32 s30, s30, 12
	s_add_u32 s28, s26, s30
	s_addc_u32 s29, s27, 0
	global_load_dwordx2 v[68:69], v162, s[28:29]
	s_waitcnt vmcnt(32)
	v_cvt_f32_ubyte0_e32 v141, v70
	v_cvt_f32_ubyte1_e32 v143, v70
	v_cvt_f32_ubyte2_e32 v145, v70
	v_cvt_f32_ubyte3_e32 v147, v70
	v_cvt_f32_ubyte0_e32 v149, v71
	v_cvt_f32_ubyte1_e32 v151, v71
	v_cvt_f32_ubyte2_e32 v153, v71
	v_cvt_f32_ubyte3_e32 v155, v71
	v_readlane_b32 s30, v121, 55
	s_lshl_b32 s30, s30, 12
	s_add_u32 s28, s26, s30
	s_addc_u32 s29, s27, 0
	global_load_dwordx2 v[70:71], v162, s[28:29]
	v_mul_f32_e32 v198, v124, v108
	v_mul_f32_e32 v199, v125, v108
	v_mul_f32_e32 v200, v140, v108
	v_mul_f32_e32 v201, v141, v108
	v_fmac_f32_e32 v198, v126, v109
	v_fmac_f32_e32 v199, v127, v109
	v_fmac_f32_e32 v200, v142, v109
	v_fmac_f32_e32 v201, v143, v109
	v_fmac_f32_e32 v198, v128, v110
	v_fmac_f32_e32 v199, v129, v110
	v_fmac_f32_e32 v200, v144, v110
	v_fmac_f32_e32 v201, v145, v110
	v_fmac_f32_e32 v198, v130, v111
	v_fmac_f32_e32 v199, v131, v111
	v_fmac_f32_e32 v200, v146, v111
	v_fmac_f32_e32 v201, v147, v111
	v_fmac_f32_e32 v198, v132, v112
	v_fmac_f32_e32 v199, v133, v112
	v_fmac_f32_e32 v200, v148, v112
	v_fmac_f32_e32 v201, v149, v112
	v_fmac_f32_e32 v198, v134, v113
	v_fmac_f32_e32 v199, v135, v113
	v_fmac_f32_e32 v200, v150, v113
	v_fmac_f32_e32 v201, v151, v113
	v_fmac_f32_e32 v198, v136, v114
	v_fmac_f32_e32 v199, v137, v114
	v_fmac_f32_e32 v200, v152, v114
	v_fmac_f32_e32 v201, v153, v114
	v_fmac_f32_e32 v198, v138, v115
	v_fmac_f32_e32 v199, v139, v115
	v_fmac_f32_e32 v200, v154, v115
	v_fmac_f32_e32 v201, v155, v115
	s_waitcnt vmcnt(32)
	v_cvt_f32_ubyte0_e32 v124, v72
	v_cvt_f32_ubyte1_e32 v126, v72
	v_cvt_f32_ubyte2_e32 v128, v72
	v_cvt_f32_ubyte3_e32 v130, v72
	v_cvt_f32_ubyte0_e32 v132, v73
	v_cvt_f32_ubyte1_e32 v134, v73
	v_cvt_f32_ubyte2_e32 v136, v73
	v_cvt_f32_ubyte3_e32 v138, v73
	v_readlane_b32 s30, v121, 56
	s_lshl_b32 s30, s30, 12
	s_add_u32 s28, s26, s30
	s_addc_u32 s29, s27, 0
	global_load_dwordx2 v[72:73], v162, s[28:29]
	s_waitcnt vmcnt(32)
	v_cvt_f32_ubyte0_e32 v125, v74
	v_cvt_f32_ubyte1_e32 v127, v74
	v_cvt_f32_ubyte2_e32 v129, v74
	v_cvt_f32_ubyte3_e32 v131, v74
	v_cvt_f32_ubyte0_e32 v133, v75
	v_cvt_f32_ubyte1_e32 v135, v75
	v_cvt_f32_ubyte2_e32 v137, v75
	v_cvt_f32_ubyte3_e32 v139, v75
	v_readlane_b32 s30, v121, 57
	s_lshl_b32 s30, s30, 12
	s_add_u32 s28, s26, s30
	s_addc_u32 s29, s27, 0
	global_load_dwordx2 v[74:75], v162, s[28:29]
	s_waitcnt vmcnt(32)
	v_cvt_f32_ubyte0_e32 v140, v76
	v_cvt_f32_ubyte1_e32 v142, v76
	v_cvt_f32_ubyte2_e32 v144, v76
	v_cvt_f32_ubyte3_e32 v146, v76
	v_cvt_f32_ubyte0_e32 v148, v77
	v_cvt_f32_ubyte1_e32 v150, v77
	v_cvt_f32_ubyte2_e32 v152, v77
	v_cvt_f32_ubyte3_e32 v154, v77
	v_readlane_b32 s30, v121, 58
	s_lshl_b32 s30, s30, 12
	s_add_u32 s28, s26, s30
	s_addc_u32 s29, s27, 0
	global_load_dwordx2 v[76:77], v162, s[28:29]
	s_waitcnt vmcnt(32)
	v_cvt_f32_ubyte0_e32 v141, v78
	v_cvt_f32_ubyte1_e32 v143, v78
	v_cvt_f32_ubyte2_e32 v145, v78
	v_cvt_f32_ubyte3_e32 v147, v78
	v_cvt_f32_ubyte0_e32 v149, v79
	v_cvt_f32_ubyte1_e32 v151, v79
	v_cvt_f32_ubyte2_e32 v153, v79
	v_cvt_f32_ubyte3_e32 v155, v79
	v_readlane_b32 s30, v121, 59
	s_lshl_b32 s30, s30, 12
	s_add_u32 s28, s26, s30
	s_addc_u32 s29, s27, 0
	global_load_dwordx2 v[78:79], v162, s[28:29]
	v_mul_f32_e32 v202, v124, v108
	v_mul_f32_e32 v203, v125, v108
	v_mul_f32_e32 v204, v140, v108
	v_mul_f32_e32 v205, v141, v108
	v_fmac_f32_e32 v202, v126, v109
	v_fmac_f32_e32 v203, v127, v109
	v_fmac_f32_e32 v204, v142, v109
	v_fmac_f32_e32 v205, v143, v109
	v_fmac_f32_e32 v202, v128, v110
	v_fmac_f32_e32 v203, v129, v110
	v_fmac_f32_e32 v204, v144, v110
	v_fmac_f32_e32 v205, v145, v110
	v_fmac_f32_e32 v202, v130, v111
	v_fmac_f32_e32 v203, v131, v111
	v_fmac_f32_e32 v204, v146, v111
	v_fmac_f32_e32 v205, v147, v111
	v_fmac_f32_e32 v202, v132, v112
	v_fmac_f32_e32 v203, v133, v112
	v_fmac_f32_e32 v204, v148, v112
	v_fmac_f32_e32 v205, v149, v112
	v_fmac_f32_e32 v202, v134, v113
	v_fmac_f32_e32 v203, v135, v113
	v_fmac_f32_e32 v204, v150, v113
	v_fmac_f32_e32 v205, v151, v113
	v_fmac_f32_e32 v202, v136, v114
	v_fmac_f32_e32 v203, v137, v114
	v_fmac_f32_e32 v204, v152, v114
	v_fmac_f32_e32 v205, v153, v114
	v_fmac_f32_e32 v202, v138, v115
	v_fmac_f32_e32 v203, v139, v115
	v_fmac_f32_e32 v204, v154, v115
	v_fmac_f32_e32 v205, v155, v115
	s_waitcnt vmcnt(32)
	v_cvt_f32_ubyte0_e32 v124, v80
	v_cvt_f32_ubyte1_e32 v126, v80
	v_cvt_f32_ubyte2_e32 v128, v80
	v_cvt_f32_ubyte3_e32 v130, v80
	v_cvt_f32_ubyte0_e32 v132, v81
	v_cvt_f32_ubyte1_e32 v134, v81
	v_cvt_f32_ubyte2_e32 v136, v81
	v_cvt_f32_ubyte3_e32 v138, v81
	v_readlane_b32 s30, v121, 60
	s_lshl_b32 s30, s30, 12
	s_add_u32 s28, s26, s30
	s_addc_u32 s29, s27, 0
	global_load_dwordx2 v[80:81], v162, s[28:29]
	s_waitcnt vmcnt(32)
	v_cvt_f32_ubyte0_e32 v125, v82
	v_cvt_f32_ubyte1_e32 v127, v82
	v_cvt_f32_ubyte2_e32 v129, v82
	v_cvt_f32_ubyte3_e32 v131, v82
	v_cvt_f32_ubyte0_e32 v133, v83
	v_cvt_f32_ubyte1_e32 v135, v83
	v_cvt_f32_ubyte2_e32 v137, v83
	v_cvt_f32_ubyte3_e32 v139, v83
	v_readlane_b32 s30, v121, 61
	s_lshl_b32 s30, s30, 12
	s_add_u32 s28, s26, s30
	s_addc_u32 s29, s27, 0
	global_load_dwordx2 v[82:83], v162, s[28:29]
	s_waitcnt vmcnt(32)
	v_cvt_f32_ubyte0_e32 v140, v84
	v_cvt_f32_ubyte1_e32 v142, v84
	v_cvt_f32_ubyte2_e32 v144, v84
	v_cvt_f32_ubyte3_e32 v146, v84
	v_cvt_f32_ubyte0_e32 v148, v85
	v_cvt_f32_ubyte1_e32 v150, v85
	v_cvt_f32_ubyte2_e32 v152, v85
	v_cvt_f32_ubyte3_e32 v154, v85
	v_readlane_b32 s30, v121, 62
	s_lshl_b32 s30, s30, 12
	s_add_u32 s28, s26, s30
	s_addc_u32 s29, s27, 0
	global_load_dwordx2 v[84:85], v162, s[28:29]
	s_waitcnt vmcnt(32)
	v_cvt_f32_ubyte0_e32 v141, v86
	v_cvt_f32_ubyte1_e32 v143, v86
	v_cvt_f32_ubyte2_e32 v145, v86
	v_cvt_f32_ubyte3_e32 v147, v86
	v_cvt_f32_ubyte0_e32 v149, v87
	v_cvt_f32_ubyte1_e32 v151, v87
	v_cvt_f32_ubyte2_e32 v153, v87
	v_cvt_f32_ubyte3_e32 v155, v87
	v_readlane_b32 s30, v121, 63
	s_lshl_b32 s30, s30, 12
	s_add_u32 s28, s26, s30
	s_addc_u32 s29, s27, 0
	global_load_dwordx2 v[86:87], v162, s[28:29]
	v_mul_f32_e32 v206, v124, v108
	v_mul_f32_e32 v207, v125, v108
	v_mul_f32_e32 v208, v140, v108
	v_mul_f32_e32 v209, v141, v108
	v_fmac_f32_e32 v206, v126, v109
	v_fmac_f32_e32 v207, v127, v109
	v_fmac_f32_e32 v208, v142, v109
	v_fmac_f32_e32 v209, v143, v109
	v_fmac_f32_e32 v206, v128, v110
	v_fmac_f32_e32 v207, v129, v110
	v_fmac_f32_e32 v208, v144, v110
	v_fmac_f32_e32 v209, v145, v110
	v_fmac_f32_e32 v206, v130, v111
	v_fmac_f32_e32 v207, v131, v111
	v_fmac_f32_e32 v208, v146, v111
	v_fmac_f32_e32 v209, v147, v111
	v_fmac_f32_e32 v206, v132, v112
	v_fmac_f32_e32 v207, v133, v112
	v_fmac_f32_e32 v208, v148, v112
	v_fmac_f32_e32 v209, v149, v112
	v_fmac_f32_e32 v206, v134, v113
	v_fmac_f32_e32 v207, v135, v113
	v_fmac_f32_e32 v208, v150, v113
	v_fmac_f32_e32 v209, v151, v113
	v_fmac_f32_e32 v206, v136, v114
	v_fmac_f32_e32 v207, v137, v114
	v_fmac_f32_e32 v208, v152, v114
	v_fmac_f32_e32 v209, v153, v114
	v_fmac_f32_e32 v206, v138, v115
	v_fmac_f32_e32 v207, v139, v115
	v_fmac_f32_e32 v208, v154, v115
	v_fmac_f32_e32 v209, v155, v115
	v_permlane32_swap_b32_e32 v178, v194
	v_permlane32_swap_b32_e32 v179, v195
	v_permlane32_swap_b32_e32 v180, v196
	v_permlane32_swap_b32_e32 v181, v197
	v_permlane32_swap_b32_e32 v182, v198
	v_permlane32_swap_b32_e32 v183, v199
	v_permlane32_swap_b32_e32 v184, v200
	v_permlane32_swap_b32_e32 v185, v201
	v_permlane32_swap_b32_e32 v186, v202
	v_permlane32_swap_b32_e32 v187, v203
	v_permlane32_swap_b32_e32 v188, v204
	v_permlane32_swap_b32_e32 v189, v205
	v_permlane32_swap_b32_e32 v190, v206
	v_permlane32_swap_b32_e32 v191, v207
	v_permlane32_swap_b32_e32 v192, v208
	v_permlane32_swap_b32_e32 v193, v209
	v_add_f32_e32 v178, v178, v194
	v_add_f32_e32 v179, v179, v195
	v_add_f32_e32 v180, v180, v196
	v_add_f32_e32 v181, v181, v197
	v_add_f32_e32 v182, v182, v198
	v_add_f32_e32 v183, v183, v199
	v_add_f32_e32 v184, v184, v200
	v_add_f32_e32 v185, v185, v201
	v_add_f32_e32 v186, v186, v202
	v_add_f32_e32 v187, v187, v203
	v_add_f32_e32 v188, v188, v204
	v_add_f32_e32 v189, v189, v205
	v_add_f32_e32 v190, v190, v206
	v_add_f32_e32 v191, v191, v207
	v_add_f32_e32 v192, v192, v208
	v_add_f32_e32 v193, v193, v209
	v_permlane16_swap_b32_e32 v178, v186
	v_permlane16_swap_b32_e32 v179, v187
	v_permlane16_swap_b32_e32 v180, v188
	v_permlane16_swap_b32_e32 v181, v189
	v_permlane16_swap_b32_e32 v182, v190
	v_permlane16_swap_b32_e32 v183, v191
	v_permlane16_swap_b32_e32 v184, v192
	v_permlane16_swap_b32_e32 v185, v193
	v_add_f32_e32 v178, v178, v186
	v_add_f32_e32 v179, v179, v187
	v_add_f32_e32 v180, v180, v188
	v_add_f32_e32 v181, v181, v189
	v_add_f32_e32 v182, v182, v190
	v_add_f32_e32 v183, v183, v191
	v_add_f32_e32 v184, v184, v192
	v_add_f32_e32 v185, v185, v193
	v_cndmask_b32_e64 v2, v178, v182, s[8:9]
	v_cndmask_b32_e64 v3, v179, v183, s[8:9]
	v_cndmask_b32_e64 v4, v180, v184, s[8:9]
	v_cndmask_b32_e64 v5, v181, v185, s[8:9]
	v_cndmask_b32_e64 v6, v182, v178, s[8:9]
	v_cndmask_b32_e64 v7, v183, v179, s[8:9]
	v_cndmask_b32_e64 v8, v184, v180, s[8:9]
	v_cndmask_b32_e64 v9, v185, v181, s[8:9]
	v_add_f32_dpp v6, v2, v6 row_ror:8 row_mask:0xf bank_mask:0xf
	v_add_f32_dpp v7, v3, v7 row_ror:8 row_mask:0xf bank_mask:0xf
	v_add_f32_dpp v8, v4, v8 row_ror:8 row_mask:0xf bank_mask:0xf
	v_add_f32_dpp v9, v5, v9 row_ror:8 row_mask:0xf bank_mask:0xf
	v_cndmask_b32_e64 v2, v6, v8, s[10:11]
	v_cndmask_b32_e64 v3, v7, v9, s[10:11]
	v_cndmask_b32_e64 v4, v8, v6, s[10:11]
	v_cndmask_b32_e64 v5, v9, v7, s[10:11]
	v_add_f32_dpp v4, v2, v4 row_half_mirror row_mask:0xf bank_mask:0xf
	v_add_f32_dpp v5, v3, v5 row_half_mirror row_mask:0xf bank_mask:0xf
	v_cndmask_b32_e64 v2, v4, v5, s[14:15]
	v_cndmask_b32_e64 v3, v5, v4, s[14:15]
	s_nop 0
	v_add_f32_dpp v3, v2, v3 quad_perm:[2,3,0,1] row_mask:0xf bank_mask:0xf
	s_nop 1
	v_add_f32_dpp v11, v3, v3 quad_perm:[1,0,3,2] row_mask:0xf bank_mask:0xf
	s_mov_b64 exec, s[2:3]
	global_store_dword v[22:23], v11, off offset:256
	s_mov_b64 exec, -1
	s_waitcnt vmcnt(32)
	v_cvt_f32_ubyte0_e32 v124, v24
	v_cvt_f32_ubyte1_e32 v126, v24
	v_cvt_f32_ubyte2_e32 v128, v24
	v_cvt_f32_ubyte3_e32 v130, v24
	v_cvt_f32_ubyte0_e32 v132, v25
	v_cvt_f32_ubyte1_e32 v134, v25
	v_cvt_f32_ubyte2_e32 v136, v25
	v_cvt_f32_ubyte3_e32 v138, v25
	s_waitcnt vmcnt(31)
	v_cvt_f32_ubyte0_e32 v125, v26
	v_cvt_f32_ubyte1_e32 v127, v26
	v_cvt_f32_ubyte2_e32 v129, v26
	v_cvt_f32_ubyte3_e32 v131, v26
	v_cvt_f32_ubyte0_e32 v133, v27
	v_cvt_f32_ubyte1_e32 v135, v27
	v_cvt_f32_ubyte2_e32 v137, v27
	v_cvt_f32_ubyte3_e32 v139, v27
	s_waitcnt vmcnt(30)
	v_cvt_f32_ubyte0_e32 v140, v28
	v_cvt_f32_ubyte1_e32 v142, v28
	v_cvt_f32_ubyte2_e32 v144, v28
	v_cvt_f32_ubyte3_e32 v146, v28
	v_cvt_f32_ubyte0_e32 v148, v29
	v_cvt_f32_ubyte1_e32 v150, v29
	v_cvt_f32_ubyte2_e32 v152, v29
	v_cvt_f32_ubyte3_e32 v154, v29
	s_waitcnt vmcnt(29)
	v_cvt_f32_ubyte0_e32 v141, v30
	v_cvt_f32_ubyte1_e32 v143, v30
	v_cvt_f32_ubyte2_e32 v145, v30
	v_cvt_f32_ubyte3_e32 v147, v30
	v_cvt_f32_ubyte0_e32 v149, v31
	v_cvt_f32_ubyte1_e32 v151, v31
	v_cvt_f32_ubyte2_e32 v153, v31
	v_cvt_f32_ubyte3_e32 v155, v31
	v_mul_f32_e32 v178, v124, v108
	v_mul_f32_e32 v179, v125, v108
	v_mul_f32_e32 v180, v140, v108
	v_mul_f32_e32 v181, v141, v108
	v_fmac_f32_e32 v178, v126, v109
	v_fmac_f32_e32 v179, v127, v109
	v_fmac_f32_e32 v180, v142, v109
	v_fmac_f32_e32 v181, v143, v109
	v_fmac_f32_e32 v178, v128, v110
	v_fmac_f32_e32 v179, v129, v110
	v_fmac_f32_e32 v180, v144, v110
	v_fmac_f32_e32 v181, v145, v110
	v_fmac_f32_e32 v178, v130, v111
	v_fmac_f32_e32 v179, v131, v111
	v_fmac_f32_e32 v180, v146, v111
	v_fmac_f32_e32 v181, v147, v111
	v_fmac_f32_e32 v178, v132, v112
	v_fmac_f32_e32 v179, v133, v112
	v_fmac_f32_e32 v180, v148, v112
	v_fmac_f32_e32 v181, v149, v112
	v_fmac_f32_e32 v178, v134, v113
	v_fmac_f32_e32 v179, v135, v113
	v_fmac_f32_e32 v180, v150, v113
	v_fmac_f32_e32 v181, v151, v113
	v_fmac_f32_e32 v178, v136, v114
	v_fmac_f32_e32 v179, v137, v114
	v_fmac_f32_e32 v180, v152, v114
	v_fmac_f32_e32 v181, v153, v114
	v_fmac_f32_e32 v178, v138, v115
	v_fmac_f32_e32 v179, v139, v115
	v_fmac_f32_e32 v180, v154, v115
	v_fmac_f32_e32 v181, v155, v115
	s_waitcnt vmcnt(28)
	v_cvt_f32_ubyte0_e32 v124, v32
	v_cvt_f32_ubyte1_e32 v126, v32
	v_cvt_f32_ubyte2_e32 v128, v32
	v_cvt_f32_ubyte3_e32 v130, v32
	v_cvt_f32_ubyte0_e32 v132, v33
	v_cvt_f32_ubyte1_e32 v134, v33
	v_cvt_f32_ubyte2_e32 v136, v33
	v_cvt_f32_ubyte3_e32 v138, v33
	s_waitcnt vmcnt(27)
	v_cvt_f32_ubyte0_e32 v125, v34
	v_cvt_f32_ubyte1_e32 v127, v34
	v_cvt_f32_ubyte2_e32 v129, v34
	v_cvt_f32_ubyte3_e32 v131, v34
	v_cvt_f32_ubyte0_e32 v133, v35
	v_cvt_f32_ubyte1_e32 v135, v35
	v_cvt_f32_ubyte2_e32 v137, v35
	v_cvt_f32_ubyte3_e32 v139, v35
	s_waitcnt vmcnt(26)
	v_cvt_f32_ubyte0_e32 v140, v36
	v_cvt_f32_ubyte1_e32 v142, v36
	v_cvt_f32_ubyte2_e32 v144, v36
	v_cvt_f32_ubyte3_e32 v146, v36
	v_cvt_f32_ubyte0_e32 v148, v37
	v_cvt_f32_ubyte1_e32 v150, v37
	v_cvt_f32_ubyte2_e32 v152, v37
	v_cvt_f32_ubyte3_e32 v154, v37
	s_waitcnt vmcnt(25)
	v_cvt_f32_ubyte0_e32 v141, v38
	v_cvt_f32_ubyte1_e32 v143, v38
	v_cvt_f32_ubyte2_e32 v145, v38
	v_cvt_f32_ubyte3_e32 v147, v38
	v_cvt_f32_ubyte0_e32 v149, v39
	v_cvt_f32_ubyte1_e32 v151, v39
	v_cvt_f32_ubyte2_e32 v153, v39
	v_cvt_f32_ubyte3_e32 v155, v39
	v_mul_f32_e32 v182, v124, v108
	v_mul_f32_e32 v183, v125, v108
	v_mul_f32_e32 v184, v140, v108
	v_mul_f32_e32 v185, v141, v108
	v_fmac_f32_e32 v182, v126, v109
	v_fmac_f32_e32 v183, v127, v109
	v_fmac_f32_e32 v184, v142, v109
	v_fmac_f32_e32 v185, v143, v109
	v_fmac_f32_e32 v182, v128, v110
	v_fmac_f32_e32 v183, v129, v110
	v_fmac_f32_e32 v184, v144, v110
	v_fmac_f32_e32 v185, v145, v110
	v_fmac_f32_e32 v182, v130, v111
	v_fmac_f32_e32 v183, v131, v111
	v_fmac_f32_e32 v184, v146, v111
	v_fmac_f32_e32 v185, v147, v111
	v_fmac_f32_e32 v182, v132, v112
	v_fmac_f32_e32 v183, v133, v112
	v_fmac_f32_e32 v184, v148, v112
	v_fmac_f32_e32 v185, v149, v112
	v_fmac_f32_e32 v182, v134, v113
	v_fmac_f32_e32 v183, v135, v113
	v_fmac_f32_e32 v184, v150, v113
	v_fmac_f32_e32 v185, v151, v113
	v_fmac_f32_e32 v182, v136, v114
	v_fmac_f32_e32 v183, v137, v114
	v_fmac_f32_e32 v184, v152, v114
	v_fmac_f32_e32 v185, v153, v114
	v_fmac_f32_e32 v182, v138, v115
	v_fmac_f32_e32 v183, v139, v115
	v_fmac_f32_e32 v184, v154, v115
	v_fmac_f32_e32 v185, v155, v115
	s_waitcnt vmcnt(24)
	v_cvt_f32_ubyte0_e32 v124, v40
	v_cvt_f32_ubyte1_e32 v126, v40
	v_cvt_f32_ubyte2_e32 v128, v40
	v_cvt_f32_ubyte3_e32 v130, v40
	v_cvt_f32_ubyte0_e32 v132, v41
	v_cvt_f32_ubyte1_e32 v134, v41
	v_cvt_f32_ubyte2_e32 v136, v41
	v_cvt_f32_ubyte3_e32 v138, v41
	s_waitcnt vmcnt(23)
	v_cvt_f32_ubyte0_e32 v125, v42
	v_cvt_f32_ubyte1_e32 v127, v42
	v_cvt_f32_ubyte2_e32 v129, v42
	v_cvt_f32_ubyte3_e32 v131, v42
	v_cvt_f32_ubyte0_e32 v133, v43
	v_cvt_f32_ubyte1_e32 v135, v43
	v_cvt_f32_ubyte2_e32 v137, v43
	v_cvt_f32_ubyte3_e32 v139, v43
	s_waitcnt vmcnt(22)
	v_cvt_f32_ubyte0_e32 v140, v44
	v_cvt_f32_ubyte1_e32 v142, v44
	v_cvt_f32_ubyte2_e32 v144, v44
	v_cvt_f32_ubyte3_e32 v146, v44
	v_cvt_f32_ubyte0_e32 v148, v45
	v_cvt_f32_ubyte1_e32 v150, v45
	v_cvt_f32_ubyte2_e32 v152, v45
	v_cvt_f32_ubyte3_e32 v154, v45
	s_waitcnt vmcnt(21)
	v_cvt_f32_ubyte0_e32 v141, v46
	v_cvt_f32_ubyte1_e32 v143, v46
	v_cvt_f32_ubyte2_e32 v145, v46
	v_cvt_f32_ubyte3_e32 v147, v46
	v_cvt_f32_ubyte0_e32 v149, v47
	v_cvt_f32_ubyte1_e32 v151, v47
	v_cvt_f32_ubyte2_e32 v153, v47
	v_cvt_f32_ubyte3_e32 v155, v47
	v_mul_f32_e32 v186, v124, v108
	v_mul_f32_e32 v187, v125, v108
	v_mul_f32_e32 v188, v140, v108
	v_mul_f32_e32 v189, v141, v108
	v_fmac_f32_e32 v186, v126, v109
	v_fmac_f32_e32 v187, v127, v109
	v_fmac_f32_e32 v188, v142, v109
	v_fmac_f32_e32 v189, v143, v109
	v_fmac_f32_e32 v186, v128, v110
	v_fmac_f32_e32 v187, v129, v110
	v_fmac_f32_e32 v188, v144, v110
	v_fmac_f32_e32 v189, v145, v110
	v_fmac_f32_e32 v186, v130, v111
	v_fmac_f32_e32 v187, v131, v111
	v_fmac_f32_e32 v188, v146, v111
	v_fmac_f32_e32 v189, v147, v111
	v_fmac_f32_e32 v186, v132, v112
	v_fmac_f32_e32 v187, v133, v112
	v_fmac_f32_e32 v188, v148, v112
	v_fmac_f32_e32 v189, v149, v112
	v_fmac_f32_e32 v186, v134, v113
	v_fmac_f32_e32 v187, v135, v113
	v_fmac_f32_e32 v188, v150, v113
	v_fmac_f32_e32 v189, v151, v113
	v_fmac_f32_e32 v186, v136, v114
	v_fmac_f32_e32 v187, v137, v114
	v_fmac_f32_e32 v188, v152, v114
	v_fmac_f32_e32 v189, v153, v114
	v_fmac_f32_e32 v186, v138, v115
	v_fmac_f32_e32 v187, v139, v115
	v_fmac_f32_e32 v188, v154, v115
	v_fmac_f32_e32 v189, v155, v115
	s_waitcnt vmcnt(20)
	v_cvt_f32_ubyte0_e32 v124, v48
	v_cvt_f32_ubyte1_e32 v126, v48
	v_cvt_f32_ubyte2_e32 v128, v48
	v_cvt_f32_ubyte3_e32 v130, v48
	v_cvt_f32_ubyte0_e32 v132, v49
	v_cvt_f32_ubyte1_e32 v134, v49
	v_cvt_f32_ubyte2_e32 v136, v49
	v_cvt_f32_ubyte3_e32 v138, v49
	s_waitcnt vmcnt(19)
	v_cvt_f32_ubyte0_e32 v125, v50
	v_cvt_f32_ubyte1_e32 v127, v50
	v_cvt_f32_ubyte2_e32 v129, v50
	v_cvt_f32_ubyte3_e32 v131, v50
	v_cvt_f32_ubyte0_e32 v133, v51
	v_cvt_f32_ubyte1_e32 v135, v51
	v_cvt_f32_ubyte2_e32 v137, v51
	v_cvt_f32_ubyte3_e32 v139, v51
	s_waitcnt vmcnt(18)
	v_cvt_f32_ubyte0_e32 v140, v52
	v_cvt_f32_ubyte1_e32 v142, v52
	v_cvt_f32_ubyte2_e32 v144, v52
	v_cvt_f32_ubyte3_e32 v146, v52
	v_cvt_f32_ubyte0_e32 v148, v53
	v_cvt_f32_ubyte1_e32 v150, v53
	v_cvt_f32_ubyte2_e32 v152, v53
	v_cvt_f32_ubyte3_e32 v154, v53
	s_waitcnt vmcnt(17)
	v_cvt_f32_ubyte0_e32 v141, v54
	v_cvt_f32_ubyte1_e32 v143, v54
	v_cvt_f32_ubyte2_e32 v145, v54
	v_cvt_f32_ubyte3_e32 v147, v54
	v_cvt_f32_ubyte0_e32 v149, v55
	v_cvt_f32_ubyte1_e32 v151, v55
	v_cvt_f32_ubyte2_e32 v153, v55
	v_cvt_f32_ubyte3_e32 v155, v55
	v_mul_f32_e32 v190, v124, v108
	v_mul_f32_e32 v191, v125, v108
	v_mul_f32_e32 v192, v140, v108
	v_mul_f32_e32 v193, v141, v108
	v_fmac_f32_e32 v190, v126, v109
	v_fmac_f32_e32 v191, v127, v109
	v_fmac_f32_e32 v192, v142, v109
	v_fmac_f32_e32 v193, v143, v109
	v_fmac_f32_e32 v190, v128, v110
	v_fmac_f32_e32 v191, v129, v110
	v_fmac_f32_e32 v192, v144, v110
	v_fmac_f32_e32 v193, v145, v110
	v_fmac_f32_e32 v190, v130, v111
	v_fmac_f32_e32 v191, v131, v111
	v_fmac_f32_e32 v192, v146, v111
	v_fmac_f32_e32 v193, v147, v111
	v_fmac_f32_e32 v190, v132, v112
	v_fmac_f32_e32 v191, v133, v112
	v_fmac_f32_e32 v192, v148, v112
	v_fmac_f32_e32 v193, v149, v112
	v_fmac_f32_e32 v190, v134, v113
	v_fmac_f32_e32 v191, v135, v113
	v_fmac_f32_e32 v192, v150, v113
	v_fmac_f32_e32 v193, v151, v113
	v_fmac_f32_e32 v190, v136, v114
	v_fmac_f32_e32 v191, v137, v114
	v_fmac_f32_e32 v192, v152, v114
	v_fmac_f32_e32 v193, v153, v114
	v_fmac_f32_e32 v190, v138, v115
	v_fmac_f32_e32 v191, v139, v115
	v_fmac_f32_e32 v192, v154, v115
	v_fmac_f32_e32 v193, v155, v115
	s_waitcnt vmcnt(16)
	v_cvt_f32_ubyte0_e32 v124, v56
	v_cvt_f32_ubyte1_e32 v126, v56
	v_cvt_f32_ubyte2_e32 v128, v56
	v_cvt_f32_ubyte3_e32 v130, v56
	v_cvt_f32_ubyte0_e32 v132, v57
	v_cvt_f32_ubyte1_e32 v134, v57
	v_cvt_f32_ubyte2_e32 v136, v57
	v_cvt_f32_ubyte3_e32 v138, v57
	s_waitcnt vmcnt(15)
	v_cvt_f32_ubyte0_e32 v125, v58
	v_cvt_f32_ubyte1_e32 v127, v58
	v_cvt_f32_ubyte2_e32 v129, v58
	v_cvt_f32_ubyte3_e32 v131, v58
	v_cvt_f32_ubyte0_e32 v133, v59
	v_cvt_f32_ubyte1_e32 v135, v59
	v_cvt_f32_ubyte2_e32 v137, v59
	v_cvt_f32_ubyte3_e32 v139, v59
	s_waitcnt vmcnt(14)
	v_cvt_f32_ubyte0_e32 v140, v60
	v_cvt_f32_ubyte1_e32 v142, v60
	v_cvt_f32_ubyte2_e32 v144, v60
	v_cvt_f32_ubyte3_e32 v146, v60
	v_cvt_f32_ubyte0_e32 v148, v61
	v_cvt_f32_ubyte1_e32 v150, v61
	v_cvt_f32_ubyte2_e32 v152, v61
	v_cvt_f32_ubyte3_e32 v154, v61
	s_waitcnt vmcnt(13)
	v_cvt_f32_ubyte0_e32 v141, v62
	v_cvt_f32_ubyte1_e32 v143, v62
	v_cvt_f32_ubyte2_e32 v145, v62
	v_cvt_f32_ubyte3_e32 v147, v62
	v_cvt_f32_ubyte0_e32 v149, v63
	v_cvt_f32_ubyte1_e32 v151, v63
	v_cvt_f32_ubyte2_e32 v153, v63
	v_cvt_f32_ubyte3_e32 v155, v63
	v_mul_f32_e32 v194, v124, v108
	v_mul_f32_e32 v195, v125, v108
	v_mul_f32_e32 v196, v140, v108
	v_mul_f32_e32 v197, v141, v108
	v_fmac_f32_e32 v194, v126, v109
	v_fmac_f32_e32 v195, v127, v109
	v_fmac_f32_e32 v196, v142, v109
	v_fmac_f32_e32 v197, v143, v109
	v_fmac_f32_e32 v194, v128, v110
	v_fmac_f32_e32 v195, v129, v110
	v_fmac_f32_e32 v196, v144, v110
	v_fmac_f32_e32 v197, v145, v110
	v_fmac_f32_e32 v194, v130, v111
	v_fmac_f32_e32 v195, v131, v111
	v_fmac_f32_e32 v196, v146, v111
	v_fmac_f32_e32 v197, v147, v111
	v_fmac_f32_e32 v194, v132, v112
	v_fmac_f32_e32 v195, v133, v112
	v_fmac_f32_e32 v196, v148, v112
	v_fmac_f32_e32 v197, v149, v112
	v_fmac_f32_e32 v194, v134, v113
	v_fmac_f32_e32 v195, v135, v113
	v_fmac_f32_e32 v196, v150, v113
	v_fmac_f32_e32 v197, v151, v113
	v_fmac_f32_e32 v194, v136, v114
	v_fmac_f32_e32 v195, v137, v114
	v_fmac_f32_e32 v196, v152, v114
	v_fmac_f32_e32 v197, v153, v114
	v_fmac_f32_e32 v194, v138, v115
	v_fmac_f32_e32 v195, v139, v115
	v_fmac_f32_e32 v196, v154, v115
	v_fmac_f32_e32 v197, v155, v115
	s_waitcnt vmcnt(12)
	v_cvt_f32_ubyte0_e32 v124, v64
	v_cvt_f32_ubyte1_e32 v126, v64
	v_cvt_f32_ubyte2_e32 v128, v64
	v_cvt_f32_ubyte3_e32 v130, v64
	v_cvt_f32_ubyte0_e32 v132, v65
	v_cvt_f32_ubyte1_e32 v134, v65
	v_cvt_f32_ubyte2_e32 v136, v65
	v_cvt_f32_ubyte3_e32 v138, v65
	s_waitcnt vmcnt(11)
	v_cvt_f32_ubyte0_e32 v125, v66
	v_cvt_f32_ubyte1_e32 v127, v66
	v_cvt_f32_ubyte2_e32 v129, v66
	v_cvt_f32_ubyte3_e32 v131, v66
	v_cvt_f32_ubyte0_e32 v133, v67
	v_cvt_f32_ubyte1_e32 v135, v67
	v_cvt_f32_ubyte2_e32 v137, v67
	v_cvt_f32_ubyte3_e32 v139, v67
	s_waitcnt vmcnt(10)
	v_cvt_f32_ubyte0_e32 v140, v68
	v_cvt_f32_ubyte1_e32 v142, v68
	v_cvt_f32_ubyte2_e32 v144, v68
	v_cvt_f32_ubyte3_e32 v146, v68
	v_cvt_f32_ubyte0_e32 v148, v69
	v_cvt_f32_ubyte1_e32 v150, v69
	v_cvt_f32_ubyte2_e32 v152, v69
	v_cvt_f32_ubyte3_e32 v154, v69
	s_waitcnt vmcnt(9)
	v_cvt_f32_ubyte0_e32 v141, v70
	v_cvt_f32_ubyte1_e32 v143, v70
	v_cvt_f32_ubyte2_e32 v145, v70
	v_cvt_f32_ubyte3_e32 v147, v70
	v_cvt_f32_ubyte0_e32 v149, v71
	v_cvt_f32_ubyte1_e32 v151, v71
	v_cvt_f32_ubyte2_e32 v153, v71
	v_cvt_f32_ubyte3_e32 v155, v71
	v_mul_f32_e32 v198, v124, v108
	v_mul_f32_e32 v199, v125, v108
	v_mul_f32_e32 v200, v140, v108
	v_mul_f32_e32 v201, v141, v108
	v_fmac_f32_e32 v198, v126, v109
	v_fmac_f32_e32 v199, v127, v109
	v_fmac_f32_e32 v200, v142, v109
	v_fmac_f32_e32 v201, v143, v109
	v_fmac_f32_e32 v198, v128, v110
	v_fmac_f32_e32 v199, v129, v110
	v_fmac_f32_e32 v200, v144, v110
	v_fmac_f32_e32 v201, v145, v110
	v_fmac_f32_e32 v198, v130, v111
	v_fmac_f32_e32 v199, v131, v111
	v_fmac_f32_e32 v200, v146, v111
	v_fmac_f32_e32 v201, v147, v111
	v_fmac_f32_e32 v198, v132, v112
	v_fmac_f32_e32 v199, v133, v112
	v_fmac_f32_e32 v200, v148, v112
	v_fmac_f32_e32 v201, v149, v112
	v_fmac_f32_e32 v198, v134, v113
	v_fmac_f32_e32 v199, v135, v113
	v_fmac_f32_e32 v200, v150, v113
	v_fmac_f32_e32 v201, v151, v113
	v_fmac_f32_e32 v198, v136, v114
	v_fmac_f32_e32 v199, v137, v114
	v_fmac_f32_e32 v200, v152, v114
	v_fmac_f32_e32 v201, v153, v114
	v_fmac_f32_e32 v198, v138, v115
	v_fmac_f32_e32 v199, v139, v115
	v_fmac_f32_e32 v200, v154, v115
	v_fmac_f32_e32 v201, v155, v115
	s_waitcnt vmcnt(8)
	v_cvt_f32_ubyte0_e32 v124, v72
	v_cvt_f32_ubyte1_e32 v126, v72
	v_cvt_f32_ubyte2_e32 v128, v72
	v_cvt_f32_ubyte3_e32 v130, v72
	v_cvt_f32_ubyte0_e32 v132, v73
	v_cvt_f32_ubyte1_e32 v134, v73
	v_cvt_f32_ubyte2_e32 v136, v73
	v_cvt_f32_ubyte3_e32 v138, v73
	s_waitcnt vmcnt(7)
	v_cvt_f32_ubyte0_e32 v125, v74
	v_cvt_f32_ubyte1_e32 v127, v74
	v_cvt_f32_ubyte2_e32 v129, v74
	v_cvt_f32_ubyte3_e32 v131, v74
	v_cvt_f32_ubyte0_e32 v133, v75
	v_cvt_f32_ubyte1_e32 v135, v75
	v_cvt_f32_ubyte2_e32 v137, v75
	v_cvt_f32_ubyte3_e32 v139, v75
	s_waitcnt vmcnt(6)
	v_cvt_f32_ubyte0_e32 v140, v76
	v_cvt_f32_ubyte1_e32 v142, v76
	v_cvt_f32_ubyte2_e32 v144, v76
	v_cvt_f32_ubyte3_e32 v146, v76
	v_cvt_f32_ubyte0_e32 v148, v77
	v_cvt_f32_ubyte1_e32 v150, v77
	v_cvt_f32_ubyte2_e32 v152, v77
	v_cvt_f32_ubyte3_e32 v154, v77
	s_waitcnt vmcnt(5)
	v_cvt_f32_ubyte0_e32 v141, v78
	v_cvt_f32_ubyte1_e32 v143, v78
	v_cvt_f32_ubyte2_e32 v145, v78
	v_cvt_f32_ubyte3_e32 v147, v78
	v_cvt_f32_ubyte0_e32 v149, v79
	v_cvt_f32_ubyte1_e32 v151, v79
	v_cvt_f32_ubyte2_e32 v153, v79
	v_cvt_f32_ubyte3_e32 v155, v79
	v_mul_f32_e32 v202, v124, v108
	v_mul_f32_e32 v203, v125, v108
	v_mul_f32_e32 v204, v140, v108
	v_mul_f32_e32 v205, v141, v108
	v_fmac_f32_e32 v202, v126, v109
	v_fmac_f32_e32 v203, v127, v109
	v_fmac_f32_e32 v204, v142, v109
	v_fmac_f32_e32 v205, v143, v109
	v_fmac_f32_e32 v202, v128, v110
	v_fmac_f32_e32 v203, v129, v110
	v_fmac_f32_e32 v204, v144, v110
	v_fmac_f32_e32 v205, v145, v110
	v_fmac_f32_e32 v202, v130, v111
	v_fmac_f32_e32 v203, v131, v111
	v_fmac_f32_e32 v204, v146, v111
	v_fmac_f32_e32 v205, v147, v111
	v_fmac_f32_e32 v202, v132, v112
	v_fmac_f32_e32 v203, v133, v112
	v_fmac_f32_e32 v204, v148, v112
	v_fmac_f32_e32 v205, v149, v112
	v_fmac_f32_e32 v202, v134, v113
	v_fmac_f32_e32 v203, v135, v113
	v_fmac_f32_e32 v204, v150, v113
	v_fmac_f32_e32 v205, v151, v113
	v_fmac_f32_e32 v202, v136, v114
	v_fmac_f32_e32 v203, v137, v114
	v_fmac_f32_e32 v204, v152, v114
	v_fmac_f32_e32 v205, v153, v114
	v_fmac_f32_e32 v202, v138, v115
	v_fmac_f32_e32 v203, v139, v115
	v_fmac_f32_e32 v204, v154, v115
	v_fmac_f32_e32 v205, v155, v115
	s_waitcnt vmcnt(4)
	v_cvt_f32_ubyte0_e32 v124, v80
	v_cvt_f32_ubyte1_e32 v126, v80
	v_cvt_f32_ubyte2_e32 v128, v80
	v_cvt_f32_ubyte3_e32 v130, v80
	v_cvt_f32_ubyte0_e32 v132, v81
	v_cvt_f32_ubyte1_e32 v134, v81
	v_cvt_f32_ubyte2_e32 v136, v81
	v_cvt_f32_ubyte3_e32 v138, v81
	s_waitcnt vmcnt(3)
	v_cvt_f32_ubyte0_e32 v125, v82
	v_cvt_f32_ubyte1_e32 v127, v82
	v_cvt_f32_ubyte2_e32 v129, v82
	v_cvt_f32_ubyte3_e32 v131, v82
	v_cvt_f32_ubyte0_e32 v133, v83
	v_cvt_f32_ubyte1_e32 v135, v83
	v_cvt_f32_ubyte2_e32 v137, v83
	v_cvt_f32_ubyte3_e32 v139, v83
	s_waitcnt vmcnt(2)
	v_cvt_f32_ubyte0_e32 v140, v84
	v_cvt_f32_ubyte1_e32 v142, v84
	v_cvt_f32_ubyte2_e32 v144, v84
	v_cvt_f32_ubyte3_e32 v146, v84
	v_cvt_f32_ubyte0_e32 v148, v85
	v_cvt_f32_ubyte1_e32 v150, v85
	v_cvt_f32_ubyte2_e32 v152, v85
	v_cvt_f32_ubyte3_e32 v154, v85
	s_waitcnt vmcnt(1)
	v_cvt_f32_ubyte0_e32 v141, v86
	v_cvt_f32_ubyte1_e32 v143, v86
	v_cvt_f32_ubyte2_e32 v145, v86
	v_cvt_f32_ubyte3_e32 v147, v86
	v_cvt_f32_ubyte0_e32 v149, v87
	v_cvt_f32_ubyte1_e32 v151, v87
	v_cvt_f32_ubyte2_e32 v153, v87
	v_cvt_f32_ubyte3_e32 v155, v87
	v_mul_f32_e32 v206, v124, v108
	v_mul_f32_e32 v207, v125, v108
	v_mul_f32_e32 v208, v140, v108
	v_mul_f32_e32 v209, v141, v108
	v_fmac_f32_e32 v206, v126, v109
	v_fmac_f32_e32 v207, v127, v109
	v_fmac_f32_e32 v208, v142, v109
	v_fmac_f32_e32 v209, v143, v109
	v_fmac_f32_e32 v206, v128, v110
	v_fmac_f32_e32 v207, v129, v110
	v_fmac_f32_e32 v208, v144, v110
	v_fmac_f32_e32 v209, v145, v110
	v_fmac_f32_e32 v206, v130, v111
	v_fmac_f32_e32 v207, v131, v111
	v_fmac_f32_e32 v208, v146, v111
	v_fmac_f32_e32 v209, v147, v111
	v_fmac_f32_e32 v206, v132, v112
	v_fmac_f32_e32 v207, v133, v112
	v_fmac_f32_e32 v208, v148, v112
	v_fmac_f32_e32 v209, v149, v112
	v_fmac_f32_e32 v206, v134, v113
	v_fmac_f32_e32 v207, v135, v113
	v_fmac_f32_e32 v208, v150, v113
	v_fmac_f32_e32 v209, v151, v113
	v_fmac_f32_e32 v206, v136, v114
	v_fmac_f32_e32 v207, v137, v114
	v_fmac_f32_e32 v208, v152, v114
	v_fmac_f32_e32 v209, v153, v114
	v_fmac_f32_e32 v206, v138, v115
	v_fmac_f32_e32 v207, v139, v115
	v_fmac_f32_e32 v208, v154, v115
	v_fmac_f32_e32 v209, v155, v115
	v_readlane_b32 s30, v122, 0
	s_lshl_b32 s30, s30, 12
	s_add_u32 s28, s26, s30
	s_addc_u32 s29, s27, 0
	global_load_dwordx2 v[24:25], v162, s[28:29]
	v_readlane_b32 s30, v122, 1
	s_lshl_b32 s30, s30, 12
	s_add_u32 s28, s26, s30
	s_addc_u32 s29, s27, 0
	global_load_dwordx2 v[26:27], v162, s[28:29]
	v_readlane_b32 s30, v122, 2
	s_lshl_b32 s30, s30, 12
	s_add_u32 s28, s26, s30
	s_addc_u32 s29, s27, 0
	global_load_dwordx2 v[28:29], v162, s[28:29]
	v_readlane_b32 s30, v122, 3
	s_lshl_b32 s30, s30, 12
	s_add_u32 s28, s26, s30
	s_addc_u32 s29, s27, 0
	global_load_dwordx2 v[30:31], v162, s[28:29]
	v_readlane_b32 s30, v122, 4
	s_lshl_b32 s30, s30, 12
	s_add_u32 s28, s26, s30
	s_addc_u32 s29, s27, 0
	global_load_dwordx2 v[32:33], v162, s[28:29]
	v_readlane_b32 s30, v122, 5
	s_lshl_b32 s30, s30, 12
	s_add_u32 s28, s26, s30
	s_addc_u32 s29, s27, 0
	global_load_dwordx2 v[34:35], v162, s[28:29]
	v_readlane_b32 s30, v122, 6
	s_lshl_b32 s30, s30, 12
	s_add_u32 s28, s26, s30
	s_addc_u32 s29, s27, 0
	global_load_dwordx2 v[36:37], v162, s[28:29]
	v_readlane_b32 s30, v122, 7
	s_lshl_b32 s30, s30, 12
	s_add_u32 s28, s26, s30
	s_addc_u32 s29, s27, 0
	global_load_dwordx2 v[38:39], v162, s[28:29]
	v_readlane_b32 s30, v122, 8
	s_lshl_b32 s30, s30, 12
	s_add_u32 s28, s26, s30
	s_addc_u32 s29, s27, 0
	global_load_dwordx2 v[40:41], v162, s[28:29]
	v_readlane_b32 s30, v122, 9
	s_lshl_b32 s30, s30, 12
	s_add_u32 s28, s26, s30
	s_addc_u32 s29, s27, 0
	global_load_dwordx2 v[42:43], v162, s[28:29]
	v_readlane_b32 s30, v122, 10
	s_lshl_b32 s30, s30, 12
	s_add_u32 s28, s26, s30
	s_addc_u32 s29, s27, 0
	global_load_dwordx2 v[44:45], v162, s[28:29]
	v_readlane_b32 s30, v122, 11
	s_lshl_b32 s30, s30, 12
	s_add_u32 s28, s26, s30
	s_addc_u32 s29, s27, 0
	global_load_dwordx2 v[46:47], v162, s[28:29]
	v_readlane_b32 s30, v122, 12
	s_lshl_b32 s30, s30, 12
	s_add_u32 s28, s26, s30
	s_addc_u32 s29, s27, 0
	global_load_dwordx2 v[48:49], v162, s[28:29]
	v_readlane_b32 s30, v122, 13
	s_lshl_b32 s30, s30, 12
	s_add_u32 s28, s26, s30
	s_addc_u32 s29, s27, 0
	global_load_dwordx2 v[50:51], v162, s[28:29]
	v_readlane_b32 s30, v122, 14
	s_lshl_b32 s30, s30, 12
	s_add_u32 s28, s26, s30
	s_addc_u32 s29, s27, 0
	global_load_dwordx2 v[52:53], v162, s[28:29]
	v_readlane_b32 s30, v122, 15
	s_lshl_b32 s30, s30, 12
	s_add_u32 s28, s26, s30
	s_addc_u32 s29, s27, 0
	global_load_dwordx2 v[54:55], v162, s[28:29]
	v_readlane_b32 s30, v122, 16
	s_lshl_b32 s30, s30, 12
	s_add_u32 s28, s26, s30
	s_addc_u32 s29, s27, 0
	global_load_dwordx2 v[56:57], v162, s[28:29]
	v_readlane_b32 s30, v122, 17
	s_lshl_b32 s30, s30, 12
	s_add_u32 s28, s26, s30
	s_addc_u32 s29, s27, 0
	global_load_dwordx2 v[58:59], v162, s[28:29]
	v_readlane_b32 s30, v122, 18
	s_lshl_b32 s30, s30, 12
	s_add_u32 s28, s26, s30
	s_addc_u32 s29, s27, 0
	global_load_dwordx2 v[60:61], v162, s[28:29]
	v_readlane_b32 s30, v122, 19
	s_lshl_b32 s30, s30, 12
	s_add_u32 s28, s26, s30
	s_addc_u32 s29, s27, 0
	global_load_dwordx2 v[62:63], v162, s[28:29]
	v_readlane_b32 s30, v122, 20
	s_lshl_b32 s30, s30, 12
	s_add_u32 s28, s26, s30
	s_addc_u32 s29, s27, 0
	global_load_dwordx2 v[64:65], v162, s[28:29]
	v_readlane_b32 s30, v122, 21
	s_lshl_b32 s30, s30, 12
	s_add_u32 s28, s26, s30
	s_addc_u32 s29, s27, 0
	global_load_dwordx2 v[66:67], v162, s[28:29]
	v_readlane_b32 s30, v122, 22
	s_lshl_b32 s30, s30, 12
	s_add_u32 s28, s26, s30
	s_addc_u32 s29, s27, 0
	global_load_dwordx2 v[68:69], v162, s[28:29]
	v_readlane_b32 s30, v122, 23
	s_lshl_b32 s30, s30, 12
	s_add_u32 s28, s26, s30
	s_addc_u32 s29, s27, 0
	global_load_dwordx2 v[70:71], v162, s[28:29]
	v_readlane_b32 s30, v122, 24
	s_lshl_b32 s30, s30, 12
	s_add_u32 s28, s26, s30
	s_addc_u32 s29, s27, 0
	global_load_dwordx2 v[72:73], v162, s[28:29]
	v_readlane_b32 s30, v122, 25
	s_lshl_b32 s30, s30, 12
	s_add_u32 s28, s26, s30
	s_addc_u32 s29, s27, 0
	global_load_dwordx2 v[74:75], v162, s[28:29]
	v_readlane_b32 s30, v122, 26
	s_lshl_b32 s30, s30, 12
	s_add_u32 s28, s26, s30
	s_addc_u32 s29, s27, 0
	global_load_dwordx2 v[76:77], v162, s[28:29]
	v_readlane_b32 s30, v122, 27
	s_lshl_b32 s30, s30, 12
	s_add_u32 s28, s26, s30
	s_addc_u32 s29, s27, 0
	global_load_dwordx2 v[78:79], v162, s[28:29]
	v_readlane_b32 s30, v122, 28
	s_lshl_b32 s30, s30, 12
	s_add_u32 s28, s26, s30
	s_addc_u32 s29, s27, 0
	global_load_dwordx2 v[80:81], v162, s[28:29]
	v_readlane_b32 s30, v122, 29
	s_lshl_b32 s30, s30, 12
	s_add_u32 s28, s26, s30
	s_addc_u32 s29, s27, 0
	global_load_dwordx2 v[82:83], v162, s[28:29]
	v_readlane_b32 s30, v122, 30
	s_lshl_b32 s30, s30, 12
	s_add_u32 s28, s26, s30
	s_addc_u32 s29, s27, 0
	global_load_dwordx2 v[84:85], v162, s[28:29]
	v_readlane_b32 s30, v122, 31
	s_lshl_b32 s30, s30, 12
	s_add_u32 s28, s26, s30
	s_addc_u32 s29, s27, 0
	global_load_dwordx2 v[86:87], v162, s[28:29]
	v_permlane32_swap_b32_e32 v178, v194
	v_permlane32_swap_b32_e32 v179, v195
	v_permlane32_swap_b32_e32 v180, v196
	v_permlane32_swap_b32_e32 v181, v197
	v_permlane32_swap_b32_e32 v182, v198
	v_permlane32_swap_b32_e32 v183, v199
	v_permlane32_swap_b32_e32 v184, v200
	v_permlane32_swap_b32_e32 v185, v201
	v_permlane32_swap_b32_e32 v186, v202
	v_permlane32_swap_b32_e32 v187, v203
	v_permlane32_swap_b32_e32 v188, v204
	v_permlane32_swap_b32_e32 v189, v205
	v_permlane32_swap_b32_e32 v190, v206
	v_permlane32_swap_b32_e32 v191, v207
	v_permlane32_swap_b32_e32 v192, v208
	v_permlane32_swap_b32_e32 v193, v209
	v_add_f32_e32 v178, v178, v194
	v_add_f32_e32 v179, v179, v195
	v_add_f32_e32 v180, v180, v196
	v_add_f32_e32 v181, v181, v197
	v_add_f32_e32 v182, v182, v198
	v_add_f32_e32 v183, v183, v199
	v_add_f32_e32 v184, v184, v200
	v_add_f32_e32 v185, v185, v201
	v_add_f32_e32 v186, v186, v202
	v_add_f32_e32 v187, v187, v203
	v_add_f32_e32 v188, v188, v204
	v_add_f32_e32 v189, v189, v205
	v_add_f32_e32 v190, v190, v206
	v_add_f32_e32 v191, v191, v207
	v_add_f32_e32 v192, v192, v208
	v_add_f32_e32 v193, v193, v209
	v_permlane16_swap_b32_e32 v178, v186
	v_permlane16_swap_b32_e32 v179, v187
	v_permlane16_swap_b32_e32 v180, v188
	v_permlane16_swap_b32_e32 v181, v189
	v_permlane16_swap_b32_e32 v182, v190
	v_permlane16_swap_b32_e32 v183, v191
	v_permlane16_swap_b32_e32 v184, v192
	v_permlane16_swap_b32_e32 v185, v193
	v_add_f32_e32 v178, v178, v186
	v_add_f32_e32 v179, v179, v187
	v_add_f32_e32 v180, v180, v188
	v_add_f32_e32 v181, v181, v189
	v_add_f32_e32 v182, v182, v190
	v_add_f32_e32 v183, v183, v191
	v_add_f32_e32 v184, v184, v192
	v_add_f32_e32 v185, v185, v193
	v_cndmask_b32_e64 v2, v178, v182, s[8:9]
	v_cndmask_b32_e64 v3, v179, v183, s[8:9]
	v_cndmask_b32_e64 v4, v180, v184, s[8:9]
	v_cndmask_b32_e64 v5, v181, v185, s[8:9]
	v_cndmask_b32_e64 v6, v182, v178, s[8:9]
	v_cndmask_b32_e64 v7, v183, v179, s[8:9]
	v_cndmask_b32_e64 v8, v184, v180, s[8:9]
	v_cndmask_b32_e64 v9, v185, v181, s[8:9]
	v_add_f32_dpp v6, v2, v6 row_ror:8 row_mask:0xf bank_mask:0xf
	v_add_f32_dpp v7, v3, v7 row_ror:8 row_mask:0xf bank_mask:0xf
	v_add_f32_dpp v8, v4, v8 row_ror:8 row_mask:0xf bank_mask:0xf
	v_add_f32_dpp v9, v5, v9 row_ror:8 row_mask:0xf bank_mask:0xf
	v_cndmask_b32_e64 v2, v6, v8, s[10:11]
	v_cndmask_b32_e64 v3, v7, v9, s[10:11]
	v_cndmask_b32_e64 v4, v8, v6, s[10:11]
	v_cndmask_b32_e64 v5, v9, v7, s[10:11]
	v_add_f32_dpp v4, v2, v4 row_half_mirror row_mask:0xf bank_mask:0xf
	v_add_f32_dpp v5, v3, v5 row_half_mirror row_mask:0xf bank_mask:0xf
	v_cndmask_b32_e64 v2, v4, v5, s[14:15]
	v_cndmask_b32_e64 v3, v5, v4, s[14:15]
	s_nop 0
	v_add_f32_dpp v3, v2, v3 quad_perm:[2,3,0,1] row_mask:0xf bank_mask:0xf
	s_nop 1
	v_add_f32_dpp v11, v3, v3 quad_perm:[1,0,3,2] row_mask:0xf bank_mask:0xf
	s_mov_b64 exec, s[2:3]
	global_store_dword v[22:23], v11, off offset:384
	s_mov_b64 exec, -1
	s_add_i32 s16, s16, 1
	s_cmp_lt_i32 s16, s17
	s_cbranch_scc1 .Lpa_tok
	s_waitcnt vmcnt(0)
	s_waitcnt vmcnt(0)
	v_cmp_eq_u32_e32 vcc, 0, v0
	s_waitcnt vmcnt(0) lgkmcnt(0)
	s_barrier
	s_and_saveexec_b64 s[2:3], vcc
	s_cbranch_execz .Lgbb_1444
	v_readlane_b32 s4, v237, 5
	s_waitcnt vmcnt(0) expcnt(0) lgkmcnt(0)
	s_nop 0
	v_mov_b32_e32 v1, s4
	ds_read_b32 v3, v1
	ds_read_b32 v1, v1 offset:4
	s_waitcnt lgkmcnt(1)
	v_cmp_ne_u32_e32 vcc, 0, v3
	s_branch .Lgbb_1412
	v_readlane_b32 s4, v237, 2
	v_readlane_b32 s5, v237, 3
	s_load_dwordx2 s[8:9], s[6:7], 0x4
	s_lshl_b64 s[4:5], s[4:5], 2
	v_readlane_b32 s6, v237, 0
	s_add_u32 s4, s6, s4
	v_readlane_b32 s6, v237, 1
	s_addc_u32 s5, s6, s5
	s_add_u32 s6, s4, 0x1000
	s_addc_u32 s7, s5, 0
	s_waitcnt lgkmcnt(0)
	s_mul_i32 s20, s8, s38
	s_add_u32 s8, s4, 0x1100
	s_mul_i32 s20, s20, s9
	s_addc_u32 s9, s5, 0
	s_add_u32 s10, s4, 0x1200
	s_addc_u32 s11, s5, 0
	s_add_u32 s12, s4, 0x1300
	s_addc_u32 s13, s5, 0
	s_mov_b32 s21, 1
	v_mov_b32_e32 v17, 0
	s_branch .Lgbb_1400

.Lgbb_1444:
	s_or_b64 exec, exec, s[2:3]
	s_waitcnt lgkmcnt(0)
	s_barrier
	s_mov_b64 exec, -1
	v_and_b32_e32 v1, 63, v0
	v_readfirstlane_b32 s16, v0
	s_load_dwordx2 s[12:13], s[0:1], 0xc0
	s_lshr_b32 s16, s16, 6
	s_and_b32 s18, s33, 7
	s_lshr_b32 s19, s33, 3
	s_lshl_b32 s19, s19, 8
	s_lshl_b32 s16, s16, 5
	s_add_i32 s16, s16, s19
	s_add_i32 s17, s16, 32
	s_add_i32 s24, s17, -1
	s_lshl_b32 s19, s18, 9
	v_lshl_add_u32 v162, v1, 3, s19
	v_mov_b32_e32 v163, 0
	s_mov_b32 s31, 0
	v_mov_b32_e32 v4, v1
	v_mov_b32_e32 v5, 0
	s_mov_b32 s69, 0
	s_mov_b32 s68, 0x400000
	s_mov_b32 s41, 0x378e98ab
	s_mov_b32 s42, 0x3b7cd369
	s_mov_b32 s43, 0xbcc618b2
	s_mov_b32 s44, 0x3dda74e4
	s_mov_b32 s45, 0x3f228afd
	s_mov_b32 s46, 0x3e03c728
	s_mov_b32 s47, 0xbfb8aa3b
	s_mov_b32 s48, 0x42ce8ed0
	s_mov_b32 s49, 0xc2b17218
	s_mov_b32 s50, 0x7fffffff
	v_mov_b32_e32 v97, 0x43000000
	v_mov_b32_e32 v250, 0x3ba10414
	v_mov_b32_e32 v251, 0xb9c68948
	v_mov_b32_e32 v252, 0x7f800000
	s_load_dwordx2 s[4:5], s[0:1], 0xb8
	s_waitcnt lgkmcnt(0)
	s_add_u32 s26, s12, 0x17c00000
	s_addc_u32 s27, s13, 0
	s_add_u32 s20, s12, 0x100000
	s_addc_u32 s21, s13, 0
	v_lshl_add_u64 v[172:173], v[162:163], 1, s[20:21]
	s_add_u32 s20, s12, 0x4da00000
	s_addc_u32 s21, s13, 0
	v_lshl_add_u64 v[174:175], v[4:5], 2, s[20:21]
	s_add_u32 s20, s12, 0x4de00000
	s_addc_u32 s21, s13, 0
	v_lshl_add_u64 v[176:177], v[4:5], 2, s[20:21]
	s_add_u32 s20, s12, 0x23c00000
	s_addc_u32 s21, s13, 0
	v_lshl_add_u64 v[210:211], v[4:5], 2, s[20:21]
	s_add_u32 s20, s12, 0x25c00000
	s_addc_u32 s21, s13, 0
	v_and_b32_e32 v6, 7, v1
	v_mov_b32_e32 v7, 0
	v_lshlrev_b32_e32 v6, 20, v6
	v_lshl_add_u64 v[212:213], v[6:7], 0, s[20:21]
	s_add_u32 s4, s12, 0x27c00000
	s_addc_u32 s5, s13, 0
	v_lshl_add_u64 v[214:215], v[162:163], 2, s[4:5]
	s_add_u32 s66, s12, 0x1fe00000
	s_addc_u32 s67, s13, 0
	s_add_u32 s64, s12, 0x38d80000
	s_addc_u32 s65, s13, 0
	s_add_u32 s60, s12, 0x38d90000
	s_addc_u32 s61, s13, 0
	s_lshl_b32 s19, s18, 20
	s_add_u32 s62, s12, 0x26c00000
	s_addc_u32 s63, s13, 0
	s_add_u32 s62, s62, s19
	s_addc_u32 s63, s63, 0
	v_mov_b32_e32 v19, 0
	s_mov_b32 s2, 0x55555555
	s_mov_b32 s3, 0x55555555
	s_lshl_b32 s30, s16, 13
	v_lshl_add_u64 v[160:161], v[172:173], 0, s[30:31]
	global_load_dwordx4 v[116:119], v[160:161], off
	s_lshl_b32 s30, s16, 9
	v_lshl_add_u64 v[160:161], v[174:175], 0, s[30:31]
	global_load_dword v122, v[160:161], off
	global_load_dword v123, v[160:161], off offset:256
	v_lshl_add_u64 v[160:161], v[176:177], 0, s[30:31]
	global_load_dword v216, v[160:161], off
	global_load_dword v217, v[160:161], off offset:256
	v_lshl_add_u64 v[160:161], v[210:211], 0, s[30:31]
	global_load_dword v218, v[160:161], off
	global_load_dword v226, v[160:161], off offset:256
	v_lshl_add_u64 v[160:161], v[160:161], 0, s[68:69]
	global_load_dword v219, v[160:161], off
	global_load_dword v227, v[160:161], off offset:256
	v_lshl_add_u64 v[160:161], v[160:161], 0, s[68:69]
	global_load_dword v220, v[160:161], off
	global_load_dword v228, v[160:161], off offset:256
	v_lshl_add_u64 v[160:161], v[160:161], 0, s[68:69]
	global_load_dword v221, v[160:161], off
	global_load_dword v229, v[160:161], off offset:256
	v_lshl_add_u64 v[160:161], v[160:161], 0, s[68:69]
	global_load_dword v222, v[160:161], off
	global_load_dword v230, v[160:161], off offset:256
	v_lshl_add_u64 v[160:161], v[160:161], 0, s[68:69]
	global_load_dword v223, v[160:161], off
	global_load_dword v231, v[160:161], off offset:256
	v_lshl_add_u64 v[160:161], v[160:161], 0, s[68:69]
	global_load_dword v224, v[160:161], off
	global_load_dword v232, v[160:161], off offset:256
	v_lshl_add_u64 v[160:161], v[160:161], 0, s[68:69]
	global_load_dword v225, v[160:161], off
	global_load_dword v233, v[160:161], off offset:256
	s_lshl_b32 s30, s16, 7
	v_lshl_add_u64 v[160:161], v[212:213], 0, s[30:31]
	global_load_dword v234, v[160:161], off
	s_lshl_b32 s30, s16, 2
	s_add_u32 s28, s66, s30
	s_addc_u32 s29, s67, 0
	global_load_dword v235, v19, s[28:29]
	s_waitcnt vmcnt(0)
	v_lshlrev_b32_e32 v16, 2, v122
	v_lshlrev_b32_e32 v17, 2, v123
	global_load_dword v238, v16, s[64:65]
	global_load_dword v240, v16, s[60:61]
	global_load_dword v239, v17, s[64:65]
	global_load_dword v241, v17, s[60:61]
	s_waitcnt vmcnt(0)
	v_readlane_b32 s30, v122, 0
	s_lshl_b32 s30, s30, 12
	s_add_u32 s28, s26, s30
	s_addc_u32 s29, s27, 0
	global_load_dwordx2 v[24:25], v162, s[28:29]
	v_readlane_b32 s30, v122, 1
	s_lshl_b32 s30, s30, 12
	s_add_u32 s28, s26, s30
	s_addc_u32 s29, s27, 0
	global_load_dwordx2 v[26:27], v162, s[28:29]
	v_readlane_b32 s30, v122, 2
	s_lshl_b32 s30, s30, 12
	s_add_u32 s28, s26, s30
	s_addc_u32 s29, s27, 0
	global_load_dwordx2 v[28:29], v162, s[28:29]
	v_readlane_b32 s30, v122, 3
	s_lshl_b32 s30, s30, 12
	s_add_u32 s28, s26, s30
	s_addc_u32 s29, s27, 0
	global_load_dwordx2 v[30:31], v162, s[28:29]
	v_readlane_b32 s30, v122, 4
	s_lshl_b32 s30, s30, 12
	s_add_u32 s28, s26, s30
	s_addc_u32 s29, s27, 0
	global_load_dwordx2 v[32:33], v162, s[28:29]
	v_readlane_b32 s30, v122, 5
	s_lshl_b32 s30, s30, 12
	s_add_u32 s28, s26, s30
	s_addc_u32 s29, s27, 0
	global_load_dwordx2 v[34:35], v162, s[28:29]
	v_readlane_b32 s30, v122, 6
	s_lshl_b32 s30, s30, 12
	s_add_u32 s28, s26, s30
	s_addc_u32 s29, s27, 0
	global_load_dwordx2 v[36:37], v162, s[28:29]
	v_readlane_b32 s30, v122, 7
	s_lshl_b32 s30, s30, 12
	s_add_u32 s28, s26, s30
	s_addc_u32 s29, s27, 0
	global_load_dwordx2 v[38:39], v162, s[28:29]
	v_readlane_b32 s30, v122, 8
	s_lshl_b32 s30, s30, 12
	s_add_u32 s28, s26, s30
	s_addc_u32 s29, s27, 0
	global_load_dwordx2 v[40:41], v162, s[28:29]
	v_readlane_b32 s30, v122, 9
	s_lshl_b32 s30, s30, 12
	s_add_u32 s28, s26, s30
	s_addc_u32 s29, s27, 0
	global_load_dwordx2 v[42:43], v162, s[28:29]
	v_readlane_b32 s30, v122, 10
	s_lshl_b32 s30, s30, 12
	s_add_u32 s28, s26, s30
	s_addc_u32 s29, s27, 0
	global_load_dwordx2 v[44:45], v162, s[28:29]
	v_readlane_b32 s30, v122, 11
	s_lshl_b32 s30, s30, 12
	s_add_u32 s28, s26, s30
	s_addc_u32 s29, s27, 0
	global_load_dwordx2 v[46:47], v162, s[28:29]
	v_readlane_b32 s30, v122, 12
	s_lshl_b32 s30, s30, 12
	s_add_u32 s28, s26, s30
	s_addc_u32 s29, s27, 0
	global_load_dwordx2 v[48:49], v162, s[28:29]
	v_readlane_b32 s30, v122, 13
	s_lshl_b32 s30, s30, 12
	s_add_u32 s28, s26, s30
	s_addc_u32 s29, s27, 0
	global_load_dwordx2 v[50:51], v162, s[28:29]
	v_readlane_b32 s30, v122, 14
	s_lshl_b32 s30, s30, 12
	s_add_u32 s28, s26, s30
	s_addc_u32 s29, s27, 0
	global_load_dwordx2 v[52:53], v162, s[28:29]
	v_readlane_b32 s30, v122, 15
	s_lshl_b32 s30, s30, 12
	s_add_u32 s28, s26, s30
	s_addc_u32 s29, s27, 0
	global_load_dwordx2 v[54:55], v162, s[28:29]
	v_readlane_b32 s30, v122, 16
	s_lshl_b32 s30, s30, 12
	s_add_u32 s28, s26, s30
	s_addc_u32 s29, s27, 0
	global_load_dwordx2 v[56:57], v162, s[28:29]
	v_readlane_b32 s30, v122, 17
	s_lshl_b32 s30, s30, 12
	s_add_u32 s28, s26, s30
	s_addc_u32 s29, s27, 0
	global_load_dwordx2 v[58:59], v162, s[28:29]
	v_readlane_b32 s30, v122, 18
	s_lshl_b32 s30, s30, 12
	s_add_u32 s28, s26, s30
	s_addc_u32 s29, s27, 0
	global_load_dwordx2 v[60:61], v162, s[28:29]
	v_readlane_b32 s30, v122, 19
	s_lshl_b32 s30, s30, 12
	s_add_u32 s28, s26, s30
	s_addc_u32 s29, s27, 0
	global_load_dwordx2 v[62:63], v162, s[28:29]
	v_readlane_b32 s30, v122, 20
	s_lshl_b32 s30, s30, 12
	s_add_u32 s28, s26, s30
	s_addc_u32 s29, s27, 0
	global_load_dwordx2 v[64:65], v162, s[28:29]
	v_readlane_b32 s30, v122, 21
	s_lshl_b32 s30, s30, 12
	s_add_u32 s28, s26, s30
	s_addc_u32 s29, s27, 0
	global_load_dwordx2 v[66:67], v162, s[28:29]
	v_readlane_b32 s30, v122, 22
	s_lshl_b32 s30, s30, 12
	s_add_u32 s28, s26, s30
	s_addc_u32 s29, s27, 0
	global_load_dwordx2 v[68:69], v162, s[28:29]
	v_readlane_b32 s30, v122, 23
	s_lshl_b32 s30, s30, 12
	s_add_u32 s28, s26, s30
	s_addc_u32 s29, s27, 0
	global_load_dwordx2 v[70:71], v162, s[28:29]
	v_readlane_b32 s30, v122, 24
	s_lshl_b32 s30, s30, 12
	s_add_u32 s28, s26, s30
	s_addc_u32 s29, s27, 0
	global_load_dwordx2 v[72:73], v162, s[28:29]
	v_readlane_b32 s30, v122, 25
	s_lshl_b32 s30, s30, 12
	s_add_u32 s28, s26, s30
	s_addc_u32 s29, s27, 0
	global_load_dwordx2 v[74:75], v162, s[28:29]
	v_readlane_b32 s30, v122, 26
	s_lshl_b32 s30, s30, 12
	s_add_u32 s28, s26, s30
	s_addc_u32 s29, s27, 0
	global_load_dwordx2 v[76:77], v162, s[28:29]
	v_readlane_b32 s30, v122, 27
	s_lshl_b32 s30, s30, 12
	s_add_u32 s28, s26, s30
	s_addc_u32 s29, s27, 0
	global_load_dwordx2 v[78:79], v162, s[28:29]
	v_readlane_b32 s30, v122, 28
	s_lshl_b32 s30, s30, 12
	s_add_u32 s28, s26, s30
	s_addc_u32 s29, s27, 0
	global_load_dwordx2 v[80:81], v162, s[28:29]
	v_readlane_b32 s30, v122, 29
	s_lshl_b32 s30, s30, 12
	s_add_u32 s28, s26, s30
	s_addc_u32 s29, s27, 0
	global_load_dwordx2 v[82:83], v162, s[28:29]
	v_readlane_b32 s30, v122, 30
	s_lshl_b32 s30, s30, 12
	s_add_u32 s28, s26, s30
	s_addc_u32 s29, s27, 0
	global_load_dwordx2 v[84:85], v162, s[28:29]
	v_readlane_b32 s30, v122, 31
	s_lshl_b32 s30, s30, 12
	s_add_u32 s28, s26, s30
	s_addc_u32 s29, s27, 0
	global_load_dwordx2 v[86:87], v162, s[28:29]
.Lpb_tok:
	v_mov_b32_e32 v99, v234
	s_nop 1
	v_add_f32_dpp v16, v99, v99 quad_perm:[1,0,3,2] row_mask:0xf bank_mask:0xf
	s_nop 1
	v_add_f32_dpp v99, v16, v16 quad_perm:[2,3,0,1] row_mask:0xf bank_mask:0xf
	s_nop 1
	v_add_f32_dpp v99, v99, v99 row_half_mirror row_mask:0xf bank_mask:0xf
	v_mov_b32_e32 v98, v235
	v_mul_f32_e32 v15, v99, v97
	v_add_f32_e32 v10, v218, v219
	v_add_f32_e32 v12, v220, v221
	v_add_f32_e32 v13, v222, v223
	v_add_f32_e32 v14, v224, v225
	v_add_f32_e32 v10, v10, v12
	v_add_f32_e32 v13, v13, v14
	v_add_f32_e32 v11, v10, v13
	v_mov_b32_e32 v96, v238
	v_mov_b32_e32 v249, v240
	v_mov_b32_e32 v164, v216
	v_mul_f32_e32 v12, v98, v96
	v_mul_f32_e32 v13, v99, v97
	v_sub_f32_e32 v10, v11, v13
	v_mul_f32_e32 v10, v12, v10
	v_mul_f32_e32 v11, 0x3f3504f3, v10
	v_cmp_nlt_f32_e64 s[34:35], |v11|, 1.0
	s_and_saveexec_b64 s[52:53], s[34:35]
	s_xor_b64 s[34:35], exec, s[52:53]
	s_cbranch_execz .Lerfa0_1476
	v_fma_f32 v12, |v11|, s41, v251
	v_fma_f32 v12, |v11|, v12, s42
	v_fma_f32 v12, |v11|, v12, s43
	v_fma_f32 v12, |v11|, v12, s44
	v_fma_f32 v12, |v11|, v12, s45
	v_fma_f32 v12, |v11|, v12, s46
	v_fma_f32 v12, |v11|, v12, |v11|
	v_mul_f32_e32 v13, 0xbfb8aa3b, v12
	v_fma_f32 v14, v12, s47, -v13
	v_rndne_f32_e32 v15, v13
	v_fmac_f32_e32 v14, 0xb2a5705f, v12
	v_sub_f32_e32 v13, v13, v15
	v_add_f32_e32 v13, v13, v14
	v_cvt_i32_f32_e32 v14, v15
	v_exp_f32_e32 v13, v13
	v_cmp_nlt_f32_e32 vcc, s48, v12
	v_ldexp_f32 v13, v13, v14
	s_nop 0
	v_cndmask_b32_e32 v13, 0, v13, vcc
	v_cmp_ngt_f32_e32 vcc, s49, v12
	s_nop 1
	v_cndmask_b32_e32 v12, v252, v13, vcc
	v_sub_f32_e32 v12, 1.0, v12
.Lerfa0_1476:
	s_andn2_saveexec_b64 s[34:35], s[34:35]
	v_mul_f32_e32 v12, v11, v11
	v_fmamk_f32 v13, v12, 0xba1345e1, v250
	v_fmaak_f32 v13, v12, v13, 0xbcdac9b8
	v_fmaak_f32 v13, v12, v13, 0x3de703be
	v_fmaak_f32 v13, v12, v13, 0xbec09330
	v_fmaak_f32 v12, v12, v13, 0x3e0375d0
	v_fma_f32 v12, |v11|, v12, |v11|
	s_or_b64 exec, exec, s[34:35]
	v_bfi_b32 v11, s50, v12, v11
	v_mul_f32_e32 v10, 0.5, v10
	v_add_f32_e32 v11, 1.0, v11
	v_mul_f32_e32 v10, v10, v11
	v_mul_f32_e32 v10, v164, v10
	v_mul_f32_e32 v10, v249, v10
	v_mov_b32_e32 v246, v10
	v_add_f32_e32 v10, v226, v227
	v_add_f32_e32 v12, v228, v229
	v_add_f32_e32 v13, v230, v231
	v_add_f32_e32 v14, v232, v233
	v_add_f32_e32 v10, v10, v12
	v_add_f32_e32 v13, v13, v14
	v_add_f32_e32 v11, v10, v13
	v_mov_b32_e32 v96, v239
	v_mov_b32_e32 v249, v241
	v_mov_b32_e32 v164, v217
	v_mul_f32_e32 v12, v98, v96
	v_mul_f32_e32 v13, v99, v97
	v_sub_f32_e32 v10, v11, v13
	v_mul_f32_e32 v10, v12, v10
	v_mul_f32_e32 v11, 0x3f3504f3, v10
	v_cmp_nlt_f32_e64 s[34:35], |v11|, 1.0
	s_and_saveexec_b64 s[52:53], s[34:35]
	s_xor_b64 s[34:35], exec, s[52:53]
	s_cbranch_execz .Lerfa1_1476
	v_fma_f32 v12, |v11|, s41, v251
	v_fma_f32 v12, |v11|, v12, s42
	v_fma_f32 v12, |v11|, v12, s43
	v_fma_f32 v12, |v11|, v12, s44
	v_fma_f32 v12, |v11|, v12, s45
	v_fma_f32 v12, |v11|, v12, s46
	v_fma_f32 v12, |v11|, v12, |v11|
	v_mul_f32_e32 v13, 0xbfb8aa3b, v12
	v_fma_f32 v14, v12, s47, -v13
	v_rndne_f32_e32 v15, v13
	v_fmac_f32_e32 v14, 0xb2a5705f, v12
	v_sub_f32_e32 v13, v13, v15
	v_add_f32_e32 v13, v13, v14
	v_cvt_i32_f32_e32 v14, v15
	v_exp_f32_e32 v13, v13
	v_cmp_nlt_f32_e32 vcc, s48, v12
	v_ldexp_f32 v13, v13, v14
	s_nop 0
	v_cndmask_b32_e32 v13, 0, v13, vcc
	v_cmp_ngt_f32_e32 vcc, s49, v12
	s_nop 1
	v_cndmask_b32_e32 v12, v252, v13, vcc
	v_sub_f32_e32 v12, 1.0, v12
.Lerfa1_1476:
	s_andn2_saveexec_b64 s[34:35], s[34:35]
	v_mul_f32_e32 v12, v11, v11
	v_fmamk_f32 v13, v12, 0xba1345e1, v250
	v_fmaak_f32 v13, v12, v13, 0xbcdac9b8
	v_fmaak_f32 v13, v12, v13, 0x3de703be
	v_fmaak_f32 v13, v12, v13, 0xbec09330
	v_fmaak_f32 v12, v12, v13, 0x3e0375d0
	v_fma_f32 v12, |v11|, v12, |v11|
	s_or_b64 exec, exec, s[34:35]
	v_bfi_b32 v11, s50, v12, v11
	v_mul_f32_e32 v10, 0.5, v10
	v_add_f32_e32 v11, 1.0, v11
	v_mul_f32_e32 v10, v10, v11
	v_mul_f32_e32 v10, v164, v10
	v_mul_f32_e32 v10, v249, v10
	v_mov_b32_e32 v247, v10
	v_add_f32_e32 v16, v246, v247
	s_nop 1
	v_add_f32_dpp v17, v16, v16 quad_perm:[1,0,3,2] row_mask:0xf bank_mask:0xf
	s_nop 1
	v_add_f32_dpp v16, v17, v17 quad_perm:[2,3,0,1] row_mask:0xf bank_mask:0xf
	s_nop 1
	v_add_f32_dpp v17, v16, v16 row_half_mirror row_mask:0xf bank_mask:0xf
	s_nop 1
	v_add_f32_dpp v16, v17, v17 row_ror:8 row_mask:0xf bank_mask:0xf
	v_mov_b32_e32 v17, v16
	s_nop 1
	v_permlane16_swap_b32_e32 v16, v17
	v_add_f32_e32 v16, v16, v17
	v_mov_b32_e32 v17, v16
	s_nop 1
	v_permlane32_swap_b32_e32 v16, v17
	v_add_f32_e32 v16, v16, v17
	v_mul_f32_e32 v248, 0xc3000000, v16
	v_mov_b32_e32 v242, v116
	v_mov_b32_e32 v243, v117
	v_mov_b32_e32 v244, v118
	v_mov_b32_e32 v245, v119
	v_mov_b32_e32 v120, v122
	v_mov_b32_e32 v121, v123
	s_lshl_b32 s30, s16, 14
	v_lshl_add_u64 v[20:21], v[214:215], 0, s[30:31]
	s_add_i32 s18, s16, 1
	s_min_i32 s18, s18, s24
	s_lshl_b32 s30, s18, 13
	v_lshl_add_u64 v[160:161], v[172:173], 0, s[30:31]
	global_load_dwordx4 v[116:119], v[160:161], off
	s_lshl_b32 s30, s18, 9
	v_lshl_add_u64 v[160:161], v[174:175], 0, s[30:31]
	global_load_dword v122, v[160:161], off
	global_load_dword v123, v[160:161], off offset:256
	v_lshl_add_u64 v[160:161], v[176:177], 0, s[30:31]
	global_load_dword v216, v[160:161], off
	global_load_dword v217, v[160:161], off offset:256
	v_lshl_add_u64 v[160:161], v[210:211], 0, s[30:31]
	global_load_dword v218, v[160:161], off
	global_load_dword v226, v[160:161], off offset:256
	v_lshl_add_u64 v[160:161], v[160:161], 0, s[68:69]
	global_load_dword v219, v[160:161], off
	global_load_dword v227, v[160:161], off offset:256
	v_lshl_add_u64 v[160:161], v[160:161], 0, s[68:69]
	global_load_dword v220, v[160:161], off
	global_load_dword v228, v[160:161], off offset:256
	v_lshl_add_u64 v[160:161], v[160:161], 0, s[68:69]
	global_load_dword v221, v[160:161], off
	global_load_dword v229, v[160:161], off offset:256
	v_lshl_add_u64 v[160:161], v[160:161], 0, s[68:69]
	global_load_dword v222, v[160:161], off
	global_load_dword v230, v[160:161], off offset:256
	v_lshl_add_u64 v[160:161], v[160:161], 0, s[68:69]
	global_load_dword v223, v[160:161], off
	global_load_dword v231, v[160:161], off offset:256
	v_lshl_add_u64 v[160:161], v[160:161], 0, s[68:69]
	global_load_dword v224, v[160:161], off
	global_load_dword v232, v[160:161], off offset:256
	v_lshl_add_u64 v[160:161], v[160:161], 0, s[68:69]
	global_load_dword v225, v[160:161], off
	global_load_dword v233, v[160:161], off offset:256
	s_lshl_b32 s30, s18, 7
	v_lshl_add_u64 v[160:161], v[212:213], 0, s[30:31]
	global_load_dword v234, v[160:161], off
	s_lshl_b32 s30, s18, 2
	s_add_u32 s28, s66, s30
	s_addc_u32 s29, s67, 0
	global_load_dword v235, v19, s[28:29]
	v_mov_b32_e32 v178, 0
	v_mov_b32_e32 v179, 0
	v_mov_b32_e32 v180, 0
	v_mov_b32_e32 v181, 0
	v_mov_b32_e32 v182, 0
	v_mov_b32_e32 v183, 0
	v_mov_b32_e32 v184, 0
	v_mov_b32_e32 v185, 0
	s_waitcnt vmcnt(54)
	v_readlane_b32 s25, v246, 0
	v_cvt_f32_ubyte0_e32 v124, v24
	v_cvt_f32_ubyte1_e32 v125, v24
	v_cvt_f32_ubyte2_e32 v126, v24
	v_cvt_f32_ubyte3_e32 v127, v24
	v_cvt_f32_ubyte0_e32 v128, v25
	v_cvt_f32_ubyte1_e32 v129, v25
	v_cvt_f32_ubyte2_e32 v130, v25
	v_cvt_f32_ubyte3_e32 v131, v25
	v_readlane_b32 s30, v120, 32
	s_lshl_b32 s30, s30, 12
	s_add_u32 s28, s26, s30
	s_addc_u32 s29, s27, 0
	global_load_dwordx2 v[24:25], v162, s[28:29]
	v_fmac_f32_e32 v178, s25, v124
	v_fmac_f32_e32 v179, s25, v125
	v_fmac_f32_e32 v180, s25, v126
	v_fmac_f32_e32 v181, s25, v127
	v_fmac_f32_e32 v182, s25, v128
	v_fmac_f32_e32 v183, s25, v129
	v_fmac_f32_e32 v184, s25, v130
	v_fmac_f32_e32 v185, s25, v131
	s_waitcnt vmcnt(54)
	v_readlane_b32 s25, v246, 1
	v_cvt_f32_ubyte0_e32 v132, v26
	v_cvt_f32_ubyte1_e32 v133, v26
	v_cvt_f32_ubyte2_e32 v134, v26
	v_cvt_f32_ubyte3_e32 v135, v26
	v_cvt_f32_ubyte0_e32 v136, v27
	v_cvt_f32_ubyte1_e32 v137, v27
	v_cvt_f32_ubyte2_e32 v138, v27
	v_cvt_f32_ubyte3_e32 v139, v27
	v_readlane_b32 s30, v120, 33
	s_lshl_b32 s30, s30, 12
	s_add_u32 s28, s26, s30
	s_addc_u32 s29, s27, 0
	global_load_dwordx2 v[26:27], v162, s[28:29]
	v_fmac_f32_e32 v178, s25, v132
	v_fmac_f32_e32 v179, s25, v133
	v_fmac_f32_e32 v180, s25, v134
	v_fmac_f32_e32 v181, s25, v135
	v_fmac_f32_e32 v182, s25, v136
	v_fmac_f32_e32 v183, s25, v137
	v_fmac_f32_e32 v184, s25, v138
	v_fmac_f32_e32 v185, s25, v139
	s_waitcnt vmcnt(54)
	v_readlane_b32 s25, v246, 2
	v_cvt_f32_ubyte0_e32 v124, v28
	v_cvt_f32_ubyte1_e32 v125, v28
	v_cvt_f32_ubyte2_e32 v126, v28
	v_cvt_f32_ubyte3_e32 v127, v28
	v_cvt_f32_ubyte0_e32 v128, v29
	v_cvt_f32_ubyte1_e32 v129, v29
	v_cvt_f32_ubyte2_e32 v130, v29
	v_cvt_f32_ubyte3_e32 v131, v29
	v_readlane_b32 s30, v120, 34
	s_lshl_b32 s30, s30, 12
	s_add_u32 s28, s26, s30
	s_addc_u32 s29, s27, 0
	global_load_dwordx2 v[28:29], v162, s[28:29]
	v_fmac_f32_e32 v178, s25, v124
	v_fmac_f32_e32 v179, s25, v125
	v_fmac_f32_e32 v180, s25, v126
	v_fmac_f32_e32 v181, s25, v127
	v_fmac_f32_e32 v182, s25, v128
	v_fmac_f32_e32 v183, s25, v129
	v_fmac_f32_e32 v184, s25, v130
	v_fmac_f32_e32 v185, s25, v131
	s_waitcnt vmcnt(54)
	v_readlane_b32 s25, v246, 3
	v_cvt_f32_ubyte0_e32 v132, v30
	v_cvt_f32_ubyte1_e32 v133, v30
	v_cvt_f32_ubyte2_e32 v134, v30
	v_cvt_f32_ubyte3_e32 v135, v30
	v_cvt_f32_ubyte0_e32 v136, v31
	v_cvt_f32_ubyte1_e32 v137, v31
	v_cvt_f32_ubyte2_e32 v138, v31
	v_cvt_f32_ubyte3_e32 v139, v31
	v_readlane_b32 s30, v120, 35
	s_lshl_b32 s30, s30, 12
	s_add_u32 s28, s26, s30
	s_addc_u32 s29, s27, 0
	global_load_dwordx2 v[30:31], v162, s[28:29]
	v_fmac_f32_e32 v178, s25, v132
	v_fmac_f32_e32 v179, s25, v133
	v_fmac_f32_e32 v180, s25, v134
	v_fmac_f32_e32 v181, s25, v135
	v_fmac_f32_e32 v182, s25, v136
	v_fmac_f32_e32 v183, s25, v137
	v_fmac_f32_e32 v184, s25, v138
	v_fmac_f32_e32 v185, s25, v139
	s_waitcnt vmcnt(54)
	v_readlane_b32 s25, v246, 4
	v_cvt_f32_ubyte0_e32 v124, v32
	v_cvt_f32_ubyte1_e32 v125, v32
	v_cvt_f32_ubyte2_e32 v126, v32
	v_cvt_f32_ubyte3_e32 v127, v32
	v_cvt_f32_ubyte0_e32 v128, v33
	v_cvt_f32_ubyte1_e32 v129, v33
	v_cvt_f32_ubyte2_e32 v130, v33
	v_cvt_f32_ubyte3_e32 v131, v33
	v_readlane_b32 s30, v120, 36
	s_lshl_b32 s30, s30, 12
	s_add_u32 s28, s26, s30
	s_addc_u32 s29, s27, 0
	global_load_dwordx2 v[32:33], v162, s[28:29]
	v_fmac_f32_e32 v178, s25, v124
	v_fmac_f32_e32 v179, s25, v125
	v_fmac_f32_e32 v180, s25, v126
	v_fmac_f32_e32 v181, s25, v127
	v_fmac_f32_e32 v182, s25, v128
	v_fmac_f32_e32 v183, s25, v129
	v_fmac_f32_e32 v184, s25, v130
	v_fmac_f32_e32 v185, s25, v131
	s_waitcnt vmcnt(54)
	v_readlane_b32 s25, v246, 5
	v_cvt_f32_ubyte0_e32 v132, v34
	v_cvt_f32_ubyte1_e32 v133, v34
	v_cvt_f32_ubyte2_e32 v134, v34
	v_cvt_f32_ubyte3_e32 v135, v34
	v_cvt_f32_ubyte0_e32 v136, v35
	v_cvt_f32_ubyte1_e32 v137, v35
	v_cvt_f32_ubyte2_e32 v138, v35
	v_cvt_f32_ubyte3_e32 v139, v35
	v_readlane_b32 s30, v120, 37
	s_lshl_b32 s30, s30, 12
	s_add_u32 s28, s26, s30
	s_addc_u32 s29, s27, 0
	global_load_dwordx2 v[34:35], v162, s[28:29]
	v_fmac_f32_e32 v178, s25, v132
	v_fmac_f32_e32 v179, s25, v133
	v_fmac_f32_e32 v180, s25, v134
	v_fmac_f32_e32 v181, s25, v135
	v_fmac_f32_e32 v182, s25, v136
	v_fmac_f32_e32 v183, s25, v137
	v_fmac_f32_e32 v184, s25, v138
	v_fmac_f32_e32 v185, s25, v139
	s_waitcnt vmcnt(54)
	v_readlane_b32 s25, v246, 6
	v_cvt_f32_ubyte0_e32 v124, v36
	v_cvt_f32_ubyte1_e32 v125, v36
	v_cvt_f32_ubyte2_e32 v126, v36
	v_cvt_f32_ubyte3_e32 v127, v36
	v_cvt_f32_ubyte0_e32 v128, v37
	v_cvt_f32_ubyte1_e32 v129, v37
	v_cvt_f32_ubyte2_e32 v130, v37
	v_cvt_f32_ubyte3_e32 v131, v37
	v_readlane_b32 s30, v120, 38
	s_lshl_b32 s30, s30, 12
	s_add_u32 s28, s26, s30
	s_addc_u32 s29, s27, 0
	global_load_dwordx2 v[36:37], v162, s[28:29]
	v_fmac_f32_e32 v178, s25, v124
	v_fmac_f32_e32 v179, s25, v125
	v_fmac_f32_e32 v180, s25, v126
	v_fmac_f32_e32 v181, s25, v127
	v_fmac_f32_e32 v182, s25, v128
	v_fmac_f32_e32 v183, s25, v129
	v_fmac_f32_e32 v184, s25, v130
	v_fmac_f32_e32 v185, s25, v131
	s_waitcnt vmcnt(54)
	v_readlane_b32 s25, v246, 7
	v_cvt_f32_ubyte0_e32 v132, v38
	v_cvt_f32_ubyte1_e32 v133, v38
	v_cvt_f32_ubyte2_e32 v134, v38
	v_cvt_f32_ubyte3_e32 v135, v38
	v_cvt_f32_ubyte0_e32 v136, v39
	v_cvt_f32_ubyte1_e32 v137, v39
	v_cvt_f32_ubyte2_e32 v138, v39
	v_cvt_f32_ubyte3_e32 v139, v39
	v_readlane_b32 s30, v120, 39
	s_lshl_b32 s30, s30, 12
	s_add_u32 s28, s26, s30
	s_addc_u32 s29, s27, 0
	global_load_dwordx2 v[38:39], v162, s[28:29]
	v_fmac_f32_e32 v178, s25, v132
	v_fmac_f32_e32 v179, s25, v133
	v_fmac_f32_e32 v180, s25, v134
	v_fmac_f32_e32 v181, s25, v135
	v_fmac_f32_e32 v182, s25, v136
	v_fmac_f32_e32 v183, s25, v137
	v_fmac_f32_e32 v184, s25, v138
	v_fmac_f32_e32 v185, s25, v139
	s_waitcnt vmcnt(54)
	v_readlane_b32 s25, v246, 8
	v_cvt_f32_ubyte0_e32 v124, v40
	v_cvt_f32_ubyte1_e32 v125, v40
	v_cvt_f32_ubyte2_e32 v126, v40
	v_cvt_f32_ubyte3_e32 v127, v40
	v_cvt_f32_ubyte0_e32 v128, v41
	v_cvt_f32_ubyte1_e32 v129, v41
	v_cvt_f32_ubyte2_e32 v130, v41
	v_cvt_f32_ubyte3_e32 v131, v41
	v_readlane_b32 s30, v120, 40
	s_lshl_b32 s30, s30, 12
	s_add_u32 s28, s26, s30
	s_addc_u32 s29, s27, 0
	global_load_dwordx2 v[40:41], v162, s[28:29]
	v_fmac_f32_e32 v178, s25, v124
	v_fmac_f32_e32 v179, s25, v125
	v_fmac_f32_e32 v180, s25, v126
	v_fmac_f32_e32 v181, s25, v127
	v_fmac_f32_e32 v182, s25, v128
	v_fmac_f32_e32 v183, s25, v129
	v_fmac_f32_e32 v184, s25, v130
	v_fmac_f32_e32 v185, s25, v131
	s_waitcnt vmcnt(54)
	v_readlane_b32 s25, v246, 9
	v_cvt_f32_ubyte0_e32 v132, v42
	v_cvt_f32_ubyte1_e32 v133, v42
	v_cvt_f32_ubyte2_e32 v134, v42
	v_cvt_f32_ubyte3_e32 v135, v42
	v_cvt_f32_ubyte0_e32 v136, v43
	v_cvt_f32_ubyte1_e32 v137, v43
	v_cvt_f32_ubyte2_e32 v138, v43
	v_cvt_f32_ubyte3_e32 v139, v43
	v_readlane_b32 s30, v120, 41
	s_lshl_b32 s30, s30, 12
	s_add_u32 s28, s26, s30
	s_addc_u32 s29, s27, 0
	global_load_dwordx2 v[42:43], v162, s[28:29]
	v_fmac_f32_e32 v178, s25, v132
	v_fmac_f32_e32 v179, s25, v133
	v_fmac_f32_e32 v180, s25, v134
	v_fmac_f32_e32 v181, s25, v135
	v_fmac_f32_e32 v182, s25, v136
	v_fmac_f32_e32 v183, s25, v137
	v_fmac_f32_e32 v184, s25, v138
	v_fmac_f32_e32 v185, s25, v139
	s_waitcnt vmcnt(54)
	v_readlane_b32 s25, v246, 10
	v_cvt_f32_ubyte0_e32 v124, v44
	v_cvt_f32_ubyte1_e32 v125, v44
	v_cvt_f32_ubyte2_e32 v126, v44
	v_cvt_f32_ubyte3_e32 v127, v44
	v_cvt_f32_ubyte0_e32 v128, v45
	v_cvt_f32_ubyte1_e32 v129, v45
	v_cvt_f32_ubyte2_e32 v130, v45
	v_cvt_f32_ubyte3_e32 v131, v45
	v_readlane_b32 s30, v120, 42
	s_lshl_b32 s30, s30, 12
	s_add_u32 s28, s26, s30
	s_addc_u32 s29, s27, 0
	global_load_dwordx2 v[44:45], v162, s[28:29]
	v_fmac_f32_e32 v178, s25, v124
	v_fmac_f32_e32 v179, s25, v125
	v_fmac_f32_e32 v180, s25, v126
	v_fmac_f32_e32 v181, s25, v127
	v_fmac_f32_e32 v182, s25, v128
	v_fmac_f32_e32 v183, s25, v129
	v_fmac_f32_e32 v184, s25, v130
	v_fmac_f32_e32 v185, s25, v131
	s_waitcnt vmcnt(54)
	v_readlane_b32 s25, v246, 11
	v_cvt_f32_ubyte0_e32 v132, v46
	v_cvt_f32_ubyte1_e32 v133, v46
	v_cvt_f32_ubyte2_e32 v134, v46
	v_cvt_f32_ubyte3_e32 v135, v46
	v_cvt_f32_ubyte0_e32 v136, v47
	v_cvt_f32_ubyte1_e32 v137, v47
	v_cvt_f32_ubyte2_e32 v138, v47
	v_cvt_f32_ubyte3_e32 v139, v47
	v_readlane_b32 s30, v120, 43
	s_lshl_b32 s30, s30, 12
	s_add_u32 s28, s26, s30
	s_addc_u32 s29, s27, 0
	global_load_dwordx2 v[46:47], v162, s[28:29]
	v_fmac_f32_e32 v178, s25, v132
	v_fmac_f32_e32 v179, s25, v133
	v_fmac_f32_e32 v180, s25, v134
	v_fmac_f32_e32 v181, s25, v135
	v_fmac_f32_e32 v182, s25, v136
	v_fmac_f32_e32 v183, s25, v137
	v_fmac_f32_e32 v184, s25, v138
	v_fmac_f32_e32 v185, s25, v139
	s_waitcnt vmcnt(54)
	v_readlane_b32 s25, v246, 12
	v_cvt_f32_ubyte0_e32 v124, v48
	v_cvt_f32_ubyte1_e32 v125, v48
	v_cvt_f32_ubyte2_e32 v126, v48
	v_cvt_f32_ubyte3_e32 v127, v48
	v_cvt_f32_ubyte0_e32 v128, v49
	v_cvt_f32_ubyte1_e32 v129, v49
	v_cvt_f32_ubyte2_e32 v130, v49
	v_cvt_f32_ubyte3_e32 v131, v49
	v_readlane_b32 s30, v120, 44
	s_lshl_b32 s30, s30, 12
	s_add_u32 s28, s26, s30
	s_addc_u32 s29, s27, 0
	global_load_dwordx2 v[48:49], v162, s[28:29]
	v_fmac_f32_e32 v178, s25, v124
	v_fmac_f32_e32 v179, s25, v125
	v_fmac_f32_e32 v180, s25, v126
	v_fmac_f32_e32 v181, s25, v127
	v_fmac_f32_e32 v182, s25, v128
	v_fmac_f32_e32 v183, s25, v129
	v_fmac_f32_e32 v184, s25, v130
	v_fmac_f32_e32 v185, s25, v131
	s_waitcnt vmcnt(54)
	v_readlane_b32 s25, v246, 13
	v_cvt_f32_ubyte0_e32 v132, v50
	v_cvt_f32_ubyte1_e32 v133, v50
	v_cvt_f32_ubyte2_e32 v134, v50
	v_cvt_f32_ubyte3_e32 v135, v50
	v_cvt_f32_ubyte0_e32 v136, v51
	v_cvt_f32_ubyte1_e32 v137, v51
	v_cvt_f32_ubyte2_e32 v138, v51
	v_cvt_f32_ubyte3_e32 v139, v51
	v_readlane_b32 s30, v120, 45
	s_lshl_b32 s30, s30, 12
	s_add_u32 s28, s26, s30
	s_addc_u32 s29, s27, 0
	global_load_dwordx2 v[50:51], v162, s[28:29]
	v_fmac_f32_e32 v178, s25, v132
	v_fmac_f32_e32 v179, s25, v133
	v_fmac_f32_e32 v180, s25, v134
	v_fmac_f32_e32 v181, s25, v135
	v_fmac_f32_e32 v182, s25, v136
	v_fmac_f32_e32 v183, s25, v137
	v_fmac_f32_e32 v184, s25, v138
	v_fmac_f32_e32 v185, s25, v139
	s_waitcnt vmcnt(54)
	v_readlane_b32 s25, v246, 14
	v_cvt_f32_ubyte0_e32 v124, v52
	v_cvt_f32_ubyte1_e32 v125, v52
	v_cvt_f32_ubyte2_e32 v126, v52
	v_cvt_f32_ubyte3_e32 v127, v52
	v_cvt_f32_ubyte0_e32 v128, v53
	v_cvt_f32_ubyte1_e32 v129, v53
	v_cvt_f32_ubyte2_e32 v130, v53
	v_cvt_f32_ubyte3_e32 v131, v53
	v_readlane_b32 s30, v120, 46
	s_lshl_b32 s30, s30, 12
	s_add_u32 s28, s26, s30
	s_addc_u32 s29, s27, 0
	global_load_dwordx2 v[52:53], v162, s[28:29]
	v_fmac_f32_e32 v178, s25, v124
	v_fmac_f32_e32 v179, s25, v125
	v_fmac_f32_e32 v180, s25, v126
	v_fmac_f32_e32 v181, s25, v127
	v_fmac_f32_e32 v182, s25, v128
	v_fmac_f32_e32 v183, s25, v129
	v_fmac_f32_e32 v184, s25, v130
	v_fmac_f32_e32 v185, s25, v131
	s_waitcnt vmcnt(54)
	v_readlane_b32 s25, v246, 15
	v_cvt_f32_ubyte0_e32 v132, v54
	v_cvt_f32_ubyte1_e32 v133, v54
	v_cvt_f32_ubyte2_e32 v134, v54
	v_cvt_f32_ubyte3_e32 v135, v54
	v_cvt_f32_ubyte0_e32 v136, v55
	v_cvt_f32_ubyte1_e32 v137, v55
	v_cvt_f32_ubyte2_e32 v138, v55
	v_cvt_f32_ubyte3_e32 v139, v55
	v_readlane_b32 s30, v120, 47
	s_lshl_b32 s30, s30, 12
	s_add_u32 s28, s26, s30
	s_addc_u32 s29, s27, 0
	global_load_dwordx2 v[54:55], v162, s[28:29]
	v_fmac_f32_e32 v178, s25, v132
	v_fmac_f32_e32 v179, s25, v133
	v_fmac_f32_e32 v180, s25, v134
	v_fmac_f32_e32 v181, s25, v135
	v_fmac_f32_e32 v182, s25, v136
	v_fmac_f32_e32 v183, s25, v137
	v_fmac_f32_e32 v184, s25, v138
	v_fmac_f32_e32 v185, s25, v139
	s_waitcnt vmcnt(54)
	v_readlane_b32 s25, v246, 16
	v_cvt_f32_ubyte0_e32 v124, v56
	v_cvt_f32_ubyte1_e32 v125, v56
	v_cvt_f32_ubyte2_e32 v126, v56
	v_cvt_f32_ubyte3_e32 v127, v56
	v_cvt_f32_ubyte0_e32 v128, v57
	v_cvt_f32_ubyte1_e32 v129, v57
	v_cvt_f32_ubyte2_e32 v130, v57
	v_cvt_f32_ubyte3_e32 v131, v57
	v_readlane_b32 s30, v120, 48
	s_lshl_b32 s30, s30, 12
	s_add_u32 s28, s26, s30
	s_addc_u32 s29, s27, 0
	global_load_dwordx2 v[56:57], v162, s[28:29]
	v_fmac_f32_e32 v178, s25, v124
	v_fmac_f32_e32 v179, s25, v125
	v_fmac_f32_e32 v180, s25, v126
	v_fmac_f32_e32 v181, s25, v127
	v_fmac_f32_e32 v182, s25, v128
	v_fmac_f32_e32 v183, s25, v129
	v_fmac_f32_e32 v184, s25, v130
	v_fmac_f32_e32 v185, s25, v131
	s_waitcnt vmcnt(54)
	v_readlane_b32 s25, v246, 17
	v_cvt_f32_ubyte0_e32 v132, v58
	v_cvt_f32_ubyte1_e32 v133, v58
	v_cvt_f32_ubyte2_e32 v134, v58
	v_cvt_f32_ubyte3_e32 v135, v58
	v_cvt_f32_ubyte0_e32 v136, v59
	v_cvt_f32_ubyte1_e32 v137, v59
	v_cvt_f32_ubyte2_e32 v138, v59
	v_cvt_f32_ubyte3_e32 v139, v59
	v_readlane_b32 s30, v120, 49
	s_lshl_b32 s30, s30, 12
	s_add_u32 s28, s26, s30
	s_addc_u32 s29, s27, 0
	global_load_dwordx2 v[58:59], v162, s[28:29]
	v_fmac_f32_e32 v178, s25, v132
	v_fmac_f32_e32 v179, s25, v133
	v_fmac_f32_e32 v180, s25, v134
	v_fmac_f32_e32 v181, s25, v135
	v_fmac_f32_e32 v182, s25, v136
	v_fmac_f32_e32 v183, s25, v137
	v_fmac_f32_e32 v184, s25, v138
	v_fmac_f32_e32 v185, s25, v139
	s_waitcnt vmcnt(54)
	v_readlane_b32 s25, v246, 18
	v_cvt_f32_ubyte0_e32 v124, v60
	v_cvt_f32_ubyte1_e32 v125, v60
	v_cvt_f32_ubyte2_e32 v126, v60
	v_cvt_f32_ubyte3_e32 v127, v60
	v_cvt_f32_ubyte0_e32 v128, v61
	v_cvt_f32_ubyte1_e32 v129, v61
	v_cvt_f32_ubyte2_e32 v130, v61
	v_cvt_f32_ubyte3_e32 v131, v61
	v_readlane_b32 s30, v120, 50
	s_lshl_b32 s30, s30, 12
	s_add_u32 s28, s26, s30
	s_addc_u32 s29, s27, 0
	global_load_dwordx2 v[60:61], v162, s[28:29]
	v_fmac_f32_e32 v178, s25, v124
	v_fmac_f32_e32 v179, s25, v125
	v_fmac_f32_e32 v180, s25, v126
	v_fmac_f32_e32 v181, s25, v127
	v_fmac_f32_e32 v182, s25, v128
	v_fmac_f32_e32 v183, s25, v129
	v_fmac_f32_e32 v184, s25, v130
	v_fmac_f32_e32 v185, s25, v131
	s_waitcnt vmcnt(54)
	v_readlane_b32 s25, v246, 19
	v_cvt_f32_ubyte0_e32 v132, v62
	v_cvt_f32_ubyte1_e32 v133, v62
	v_cvt_f32_ubyte2_e32 v134, v62
	v_cvt_f32_ubyte3_e32 v135, v62
	v_cvt_f32_ubyte0_e32 v136, v63
	v_cvt_f32_ubyte1_e32 v137, v63
	v_cvt_f32_ubyte2_e32 v138, v63
	v_cvt_f32_ubyte3_e32 v139, v63
	v_readlane_b32 s30, v120, 51
	s_lshl_b32 s30, s30, 12
	s_add_u32 s28, s26, s30
	s_addc_u32 s29, s27, 0
	global_load_dwordx2 v[62:63], v162, s[28:29]
	v_fmac_f32_e32 v178, s25, v132
	v_fmac_f32_e32 v179, s25, v133
	v_fmac_f32_e32 v180, s25, v134
	v_fmac_f32_e32 v181, s25, v135
	v_fmac_f32_e32 v182, s25, v136
	v_fmac_f32_e32 v183, s25, v137
	v_fmac_f32_e32 v184, s25, v138
	v_fmac_f32_e32 v185, s25, v139
	s_waitcnt vmcnt(54)
	v_readlane_b32 s25, v246, 20
	v_cvt_f32_ubyte0_e32 v124, v64
	v_cvt_f32_ubyte1_e32 v125, v64
	v_cvt_f32_ubyte2_e32 v126, v64
	v_cvt_f32_ubyte3_e32 v127, v64
	v_cvt_f32_ubyte0_e32 v128, v65
	v_cvt_f32_ubyte1_e32 v129, v65
	v_cvt_f32_ubyte2_e32 v130, v65
	v_cvt_f32_ubyte3_e32 v131, v65
	v_readlane_b32 s30, v120, 52
	s_lshl_b32 s30, s30, 12
	s_add_u32 s28, s26, s30
	s_addc_u32 s29, s27, 0
	global_load_dwordx2 v[64:65], v162, s[28:29]
	v_fmac_f32_e32 v178, s25, v124
	v_fmac_f32_e32 v179, s25, v125
	v_fmac_f32_e32 v180, s25, v126
	v_fmac_f32_e32 v181, s25, v127
	v_fmac_f32_e32 v182, s25, v128
	v_fmac_f32_e32 v183, s25, v129
	v_fmac_f32_e32 v184, s25, v130
	v_fmac_f32_e32 v185, s25, v131
	s_waitcnt vmcnt(54)
	v_readlane_b32 s25, v246, 21
	v_cvt_f32_ubyte0_e32 v132, v66
	v_cvt_f32_ubyte1_e32 v133, v66
	v_cvt_f32_ubyte2_e32 v134, v66
	v_cvt_f32_ubyte3_e32 v135, v66
	v_cvt_f32_ubyte0_e32 v136, v67
	v_cvt_f32_ubyte1_e32 v137, v67
	v_cvt_f32_ubyte2_e32 v138, v67
	v_cvt_f32_ubyte3_e32 v139, v67
	v_readlane_b32 s30, v120, 53
	s_lshl_b32 s30, s30, 12
	s_add_u32 s28, s26, s30
	s_addc_u32 s29, s27, 0
	global_load_dwordx2 v[66:67], v162, s[28:29]
	v_fmac_f32_e32 v178, s25, v132
	v_fmac_f32_e32 v179, s25, v133
	v_fmac_f32_e32 v180, s25, v134
	v_fmac_f32_e32 v181, s25, v135
	v_fmac_f32_e32 v182, s25, v136
	v_fmac_f32_e32 v183, s25, v137
	v_fmac_f32_e32 v184, s25, v138
	v_fmac_f32_e32 v185, s25, v139
	s_waitcnt vmcnt(54)
	v_readlane_b32 s25, v246, 22
	v_cvt_f32_ubyte0_e32 v124, v68
	v_cvt_f32_ubyte1_e32 v125, v68
	v_cvt_f32_ubyte2_e32 v126, v68
	v_cvt_f32_ubyte3_e32 v127, v68
	v_cvt_f32_ubyte0_e32 v128, v69
	v_cvt_f32_ubyte1_e32 v129, v69
	v_cvt_f32_ubyte2_e32 v130, v69
	v_cvt_f32_ubyte3_e32 v131, v69
	v_readlane_b32 s30, v120, 54
	s_lshl_b32 s30, s30, 12
	s_add_u32 s28, s26, s30
	s_addc_u32 s29, s27, 0
	global_load_dwordx2 v[68:69], v162, s[28:29]
	v_fmac_f32_e32 v178, s25, v124
	v_fmac_f32_e32 v179, s25, v125
	v_fmac_f32_e32 v180, s25, v126
	v_fmac_f32_e32 v181, s25, v127
	v_fmac_f32_e32 v182, s25, v128
	v_fmac_f32_e32 v183, s25, v129
	v_fmac_f32_e32 v184, s25, v130
	v_fmac_f32_e32 v185, s25, v131
	s_waitcnt vmcnt(54)
	v_readlane_b32 s25, v246, 23
	v_cvt_f32_ubyte0_e32 v132, v70
	v_cvt_f32_ubyte1_e32 v133, v70
	v_cvt_f32_ubyte2_e32 v134, v70
	v_cvt_f32_ubyte3_e32 v135, v70
	v_cvt_f32_ubyte0_e32 v136, v71
	v_cvt_f32_ubyte1_e32 v137, v71
	v_cvt_f32_ubyte2_e32 v138, v71
	v_cvt_f32_ubyte3_e32 v139, v71
	v_readlane_b32 s30, v120, 55
	s_lshl_b32 s30, s30, 12
	s_add_u32 s28, s26, s30
	s_addc_u32 s29, s27, 0
	global_load_dwordx2 v[70:71], v162, s[28:29]
	v_fmac_f32_e32 v178, s25, v132
	v_fmac_f32_e32 v179, s25, v133
	v_fmac_f32_e32 v180, s25, v134
	v_fmac_f32_e32 v181, s25, v135
	v_fmac_f32_e32 v182, s25, v136
	v_fmac_f32_e32 v183, s25, v137
	v_fmac_f32_e32 v184, s25, v138
	v_fmac_f32_e32 v185, s25, v139
	s_waitcnt vmcnt(54)
	v_readlane_b32 s25, v246, 24
	v_cvt_f32_ubyte0_e32 v124, v72
	v_cvt_f32_ubyte1_e32 v125, v72
	v_cvt_f32_ubyte2_e32 v126, v72
	v_cvt_f32_ubyte3_e32 v127, v72
	v_cvt_f32_ubyte0_e32 v128, v73
	v_cvt_f32_ubyte1_e32 v129, v73
	v_cvt_f32_ubyte2_e32 v130, v73
	v_cvt_f32_ubyte3_e32 v131, v73
	v_readlane_b32 s30, v120, 56
	s_lshl_b32 s30, s30, 12
	s_add_u32 s28, s26, s30
	s_addc_u32 s29, s27, 0
	global_load_dwordx2 v[72:73], v162, s[28:29]
	v_fmac_f32_e32 v178, s25, v124
	v_fmac_f32_e32 v179, s25, v125
	v_fmac_f32_e32 v180, s25, v126
	v_fmac_f32_e32 v181, s25, v127
	v_fmac_f32_e32 v182, s25, v128
	v_fmac_f32_e32 v183, s25, v129
	v_fmac_f32_e32 v184, s25, v130
	v_fmac_f32_e32 v185, s25, v131
	s_waitcnt vmcnt(54)
	v_readlane_b32 s25, v246, 25
	v_cvt_f32_ubyte0_e32 v132, v74
	v_cvt_f32_ubyte1_e32 v133, v74
	v_cvt_f32_ubyte2_e32 v134, v74
	v_cvt_f32_ubyte3_e32 v135, v74
	v_cvt_f32_ubyte0_e32 v136, v75
	v_cvt_f32_ubyte1_e32 v137, v75
	v_cvt_f32_ubyte2_e32 v138, v75
	v_cvt_f32_ubyte3_e32 v139, v75
	v_readlane_b32 s30, v120, 57
	s_lshl_b32 s30, s30, 12
	s_add_u32 s28, s26, s30
	s_addc_u32 s29, s27, 0
	global_load_dwordx2 v[74:75], v162, s[28:29]
	v_fmac_f32_e32 v178, s25, v132
	v_fmac_f32_e32 v179, s25, v133
	v_fmac_f32_e32 v180, s25, v134
	v_fmac_f32_e32 v181, s25, v135
	v_fmac_f32_e32 v182, s25, v136
	v_fmac_f32_e32 v183, s25, v137
	v_fmac_f32_e32 v184, s25, v138
	v_fmac_f32_e32 v185, s25, v139
	s_waitcnt vmcnt(54)
	v_readlane_b32 s25, v246, 26
	v_cvt_f32_ubyte0_e32 v124, v76
	v_cvt_f32_ubyte1_e32 v125, v76
	v_cvt_f32_ubyte2_e32 v126, v76
	v_cvt_f32_ubyte3_e32 v127, v76
	v_cvt_f32_ubyte0_e32 v128, v77
	v_cvt_f32_ubyte1_e32 v129, v77
	v_cvt_f32_ubyte2_e32 v130, v77
	v_cvt_f32_ubyte3_e32 v131, v77
	v_readlane_b32 s30, v120, 58
	s_lshl_b32 s30, s30, 12
	s_add_u32 s28, s26, s30
	s_addc_u32 s29, s27, 0
	global_load_dwordx2 v[76:77], v162, s[28:29]
	v_fmac_f32_e32 v178, s25, v124
	v_fmac_f32_e32 v179, s25, v125
	v_fmac_f32_e32 v180, s25, v126
	v_fmac_f32_e32 v181, s25, v127
	v_fmac_f32_e32 v182, s25, v128
	v_fmac_f32_e32 v183, s25, v129
	v_fmac_f32_e32 v184, s25, v130
	v_fmac_f32_e32 v185, s25, v131
	s_waitcnt vmcnt(54)
	v_readlane_b32 s25, v246, 27
	v_cvt_f32_ubyte0_e32 v132, v78
	v_cvt_f32_ubyte1_e32 v133, v78
	v_cvt_f32_ubyte2_e32 v134, v78
	v_cvt_f32_ubyte3_e32 v135, v78
	v_cvt_f32_ubyte0_e32 v136, v79
	v_cvt_f32_ubyte1_e32 v137, v79
	v_cvt_f32_ubyte2_e32 v138, v79
	v_cvt_f32_ubyte3_e32 v139, v79
	v_readlane_b32 s30, v120, 59
	s_lshl_b32 s30, s30, 12
	s_add_u32 s28, s26, s30
	s_addc_u32 s29, s27, 0
	global_load_dwordx2 v[78:79], v162, s[28:29]
	v_fmac_f32_e32 v178, s25, v132
	v_fmac_f32_e32 v179, s25, v133
	v_fmac_f32_e32 v180, s25, v134
	v_fmac_f32_e32 v181, s25, v135
	v_fmac_f32_e32 v182, s25, v136
	v_fmac_f32_e32 v183, s25, v137
	v_fmac_f32_e32 v184, s25, v138
	v_fmac_f32_e32 v185, s25, v139
	s_waitcnt vmcnt(54)
	v_readlane_b32 s25, v246, 28
	v_cvt_f32_ubyte0_e32 v124, v80
	v_cvt_f32_ubyte1_e32 v125, v80
	v_cvt_f32_ubyte2_e32 v126, v80
	v_cvt_f32_ubyte3_e32 v127, v80
	v_cvt_f32_ubyte0_e32 v128, v81
	v_cvt_f32_ubyte1_e32 v129, v81
	v_cvt_f32_ubyte2_e32 v130, v81
	v_cvt_f32_ubyte3_e32 v131, v81
	v_readlane_b32 s30, v120, 60
	s_lshl_b32 s30, s30, 12
	s_add_u32 s28, s26, s30
	s_addc_u32 s29, s27, 0
	global_load_dwordx2 v[80:81], v162, s[28:29]
	v_fmac_f32_e32 v178, s25, v124
	v_fmac_f32_e32 v179, s25, v125
	v_fmac_f32_e32 v180, s25, v126
	v_fmac_f32_e32 v181, s25, v127
	v_fmac_f32_e32 v182, s25, v128
	v_fmac_f32_e32 v183, s25, v129
	v_fmac_f32_e32 v184, s25, v130
	v_fmac_f32_e32 v185, s25, v131
	s_waitcnt vmcnt(54)
	v_readlane_b32 s25, v246, 29
	v_cvt_f32_ubyte0_e32 v132, v82
	v_cvt_f32_ubyte1_e32 v133, v82
	v_cvt_f32_ubyte2_e32 v134, v82
	v_cvt_f32_ubyte3_e32 v135, v82
	v_cvt_f32_ubyte0_e32 v136, v83
	v_cvt_f32_ubyte1_e32 v137, v83
	v_cvt_f32_ubyte2_e32 v138, v83
	v_cvt_f32_ubyte3_e32 v139, v83
	v_readlane_b32 s30, v120, 61
	s_lshl_b32 s30, s30, 12
	s_add_u32 s28, s26, s30
	s_addc_u32 s29, s27, 0
	global_load_dwordx2 v[82:83], v162, s[28:29]
	v_fmac_f32_e32 v178, s25, v132
	v_fmac_f32_e32 v179, s25, v133
	v_fmac_f32_e32 v180, s25, v134
	v_fmac_f32_e32 v181, s25, v135
	v_fmac_f32_e32 v182, s25, v136
	v_fmac_f32_e32 v183, s25, v137
	v_fmac_f32_e32 v184, s25, v138
	v_fmac_f32_e32 v185, s25, v139
	s_waitcnt vmcnt(54)
	v_readlane_b32 s25, v246, 30
	v_cvt_f32_ubyte0_e32 v124, v84
	v_cvt_f32_ubyte1_e32 v125, v84
	v_cvt_f32_ubyte2_e32 v126, v84
	v_cvt_f32_ubyte3_e32 v127, v84
	v_cvt_f32_ubyte0_e32 v128, v85
	v_cvt_f32_ubyte1_e32 v129, v85
	v_cvt_f32_ubyte2_e32 v130, v85
	v_cvt_f32_ubyte3_e32 v131, v85
	v_readlane_b32 s30, v120, 62
	s_lshl_b32 s30, s30, 12
	s_add_u32 s28, s26, s30
	s_addc_u32 s29, s27, 0
	global_load_dwordx2 v[84:85], v162, s[28:29]
	v_fmac_f32_e32 v178, s25, v124
	v_fmac_f32_e32 v179, s25, v125
	v_fmac_f32_e32 v180, s25, v126
	v_fmac_f32_e32 v181, s25, v127
	v_fmac_f32_e32 v182, s25, v128
	v_fmac_f32_e32 v183, s25, v129
	v_fmac_f32_e32 v184, s25, v130
	v_fmac_f32_e32 v185, s25, v131
	s_waitcnt vmcnt(54)
	v_readlane_b32 s25, v246, 31
	v_cvt_f32_ubyte0_e32 v132, v86
	v_cvt_f32_ubyte1_e32 v133, v86
	v_cvt_f32_ubyte2_e32 v134, v86
	v_cvt_f32_ubyte3_e32 v135, v86
	v_cvt_f32_ubyte0_e32 v136, v87
	v_cvt_f32_ubyte1_e32 v137, v87
	v_cvt_f32_ubyte2_e32 v138, v87
	v_cvt_f32_ubyte3_e32 v139, v87
	v_readlane_b32 s30, v120, 63
	s_lshl_b32 s30, s30, 12
	s_add_u32 s28, s26, s30
	s_addc_u32 s29, s27, 0
	global_load_dwordx2 v[86:87], v162, s[28:29]
	v_fmac_f32_e32 v178, s25, v132
	v_fmac_f32_e32 v179, s25, v133
	v_fmac_f32_e32 v180, s25, v134
	v_fmac_f32_e32 v181, s25, v135
	v_fmac_f32_e32 v182, s25, v136
	v_fmac_f32_e32 v183, s25, v137
	v_fmac_f32_e32 v184, s25, v138
	v_fmac_f32_e32 v185, s25, v139
	s_waitcnt vmcnt(31)
	v_readlane_b32 s25, v246, 32
	v_cvt_f32_ubyte0_e32 v124, v24
	v_cvt_f32_ubyte1_e32 v125, v24
	v_cvt_f32_ubyte2_e32 v126, v24
	v_cvt_f32_ubyte3_e32 v127, v24
	v_cvt_f32_ubyte0_e32 v128, v25
	v_cvt_f32_ubyte1_e32 v129, v25
	v_cvt_f32_ubyte2_e32 v130, v25
	v_cvt_f32_ubyte3_e32 v131, v25
	v_readlane_b32 s30, v121, 0
	s_lshl_b32 s30, s30, 12
	s_add_u32 s28, s26, s30
	s_addc_u32 s29, s27, 0
	global_load_dwordx2 v[24:25], v162, s[28:29]
	v_fmac_f32_e32 v178, s25, v124
	v_fmac_f32_e32 v179, s25, v125
	v_fmac_f32_e32 v180, s25, v126
	v_fmac_f32_e32 v181, s25, v127
	v_fmac_f32_e32 v182, s25, v128
	v_fmac_f32_e32 v183, s25, v129
	v_fmac_f32_e32 v184, s25, v130
	v_fmac_f32_e32 v185, s25, v131
	s_waitcnt vmcnt(31)
	v_readlane_b32 s25, v246, 33
	v_cvt_f32_ubyte0_e32 v132, v26
	v_cvt_f32_ubyte1_e32 v133, v26
	v_cvt_f32_ubyte2_e32 v134, v26
	v_cvt_f32_ubyte3_e32 v135, v26
	v_cvt_f32_ubyte0_e32 v136, v27
	v_cvt_f32_ubyte1_e32 v137, v27
	v_cvt_f32_ubyte2_e32 v138, v27
	v_cvt_f32_ubyte3_e32 v139, v27
	v_readlane_b32 s30, v121, 1
	s_lshl_b32 s30, s30, 12
	s_add_u32 s28, s26, s30
	s_addc_u32 s29, s27, 0
	global_load_dwordx2 v[26:27], v162, s[28:29]
	v_fmac_f32_e32 v178, s25, v132
	v_fmac_f32_e32 v179, s25, v133
	v_fmac_f32_e32 v180, s25, v134
	v_fmac_f32_e32 v181, s25, v135
	v_fmac_f32_e32 v182, s25, v136
	v_fmac_f32_e32 v183, s25, v137
	v_fmac_f32_e32 v184, s25, v138
	v_fmac_f32_e32 v185, s25, v139
	s_waitcnt vmcnt(31)
	v_readlane_b32 s25, v246, 34
	v_cvt_f32_ubyte0_e32 v124, v28
	v_cvt_f32_ubyte1_e32 v125, v28
	v_cvt_f32_ubyte2_e32 v126, v28
	v_cvt_f32_ubyte3_e32 v127, v28
	v_cvt_f32_ubyte0_e32 v128, v29
	v_cvt_f32_ubyte1_e32 v129, v29
	v_cvt_f32_ubyte2_e32 v130, v29
	v_cvt_f32_ubyte3_e32 v131, v29
	v_readlane_b32 s30, v121, 2
	s_lshl_b32 s30, s30, 12
	s_add_u32 s28, s26, s30
	s_addc_u32 s29, s27, 0
	global_load_dwordx2 v[28:29], v162, s[28:29]
	v_fmac_f32_e32 v178, s25, v124
	v_fmac_f32_e32 v179, s25, v125
	v_fmac_f32_e32 v180, s25, v126
	v_fmac_f32_e32 v181, s25, v127
	v_fmac_f32_e32 v182, s25, v128
	v_fmac_f32_e32 v183, s25, v129
	v_fmac_f32_e32 v184, s25, v130
	v_fmac_f32_e32 v185, s25, v131
	s_waitcnt vmcnt(31)
	v_readlane_b32 s25, v246, 35
	v_cvt_f32_ubyte0_e32 v132, v30
	v_cvt_f32_ubyte1_e32 v133, v30
	v_cvt_f32_ubyte2_e32 v134, v30
	v_cvt_f32_ubyte3_e32 v135, v30
	v_cvt_f32_ubyte0_e32 v136, v31
	v_cvt_f32_ubyte1_e32 v137, v31
	v_cvt_f32_ubyte2_e32 v138, v31
	v_cvt_f32_ubyte3_e32 v139, v31
	v_readlane_b32 s30, v121, 3
	s_lshl_b32 s30, s30, 12
	s_add_u32 s28, s26, s30
	s_addc_u32 s29, s27, 0
	global_load_dwordx2 v[30:31], v162, s[28:29]
	v_fmac_f32_e32 v178, s25, v132
	v_fmac_f32_e32 v179, s25, v133
	v_fmac_f32_e32 v180, s25, v134
	v_fmac_f32_e32 v181, s25, v135
	v_fmac_f32_e32 v182, s25, v136
	v_fmac_f32_e32 v183, s25, v137
	v_fmac_f32_e32 v184, s25, v138
	v_fmac_f32_e32 v185, s25, v139
	s_waitcnt vmcnt(31)
	v_readlane_b32 s25, v246, 36
	v_cvt_f32_ubyte0_e32 v124, v32
	v_cvt_f32_ubyte1_e32 v125, v32
	v_cvt_f32_ubyte2_e32 v126, v32
	v_cvt_f32_ubyte3_e32 v127, v32
	v_cvt_f32_ubyte0_e32 v128, v33
	v_cvt_f32_ubyte1_e32 v129, v33
	v_cvt_f32_ubyte2_e32 v130, v33
	v_cvt_f32_ubyte3_e32 v131, v33
	v_readlane_b32 s30, v121, 4
	s_lshl_b32 s30, s30, 12
	s_add_u32 s28, s26, s30
	s_addc_u32 s29, s27, 0
	global_load_dwordx2 v[32:33], v162, s[28:29]
	v_fmac_f32_e32 v178, s25, v124
	v_fmac_f32_e32 v179, s25, v125
	v_fmac_f32_e32 v180, s25, v126
	v_fmac_f32_e32 v181, s25, v127
	v_fmac_f32_e32 v182, s25, v128
	v_fmac_f32_e32 v183, s25, v129
	v_fmac_f32_e32 v184, s25, v130
	v_fmac_f32_e32 v185, s25, v131
	s_waitcnt vmcnt(31)
	v_readlane_b32 s25, v246, 37
	v_cvt_f32_ubyte0_e32 v132, v34
	v_cvt_f32_ubyte1_e32 v133, v34
	v_cvt_f32_ubyte2_e32 v134, v34
	v_cvt_f32_ubyte3_e32 v135, v34
	v_cvt_f32_ubyte0_e32 v136, v35
	v_cvt_f32_ubyte1_e32 v137, v35
	v_cvt_f32_ubyte2_e32 v138, v35
	v_cvt_f32_ubyte3_e32 v139, v35
	v_readlane_b32 s30, v121, 5
	s_lshl_b32 s30, s30, 12
	s_add_u32 s28, s26, s30
	s_addc_u32 s29, s27, 0
	global_load_dwordx2 v[34:35], v162, s[28:29]
	v_fmac_f32_e32 v178, s25, v132
	v_fmac_f32_e32 v179, s25, v133
	v_fmac_f32_e32 v180, s25, v134
	v_fmac_f32_e32 v181, s25, v135
	v_fmac_f32_e32 v182, s25, v136
	v_fmac_f32_e32 v183, s25, v137
	v_fmac_f32_e32 v184, s25, v138
	v_fmac_f32_e32 v185, s25, v139
	s_waitcnt vmcnt(31)
	v_readlane_b32 s25, v246, 38
	v_cvt_f32_ubyte0_e32 v124, v36
	v_cvt_f32_ubyte1_e32 v125, v36
	v_cvt_f32_ubyte2_e32 v126, v36
	v_cvt_f32_ubyte3_e32 v127, v36
	v_cvt_f32_ubyte0_e32 v128, v37
	v_cvt_f32_ubyte1_e32 v129, v37
	v_cvt_f32_ubyte2_e32 v130, v37
	v_cvt_f32_ubyte3_e32 v131, v37
	v_readlane_b32 s30, v121, 6
	s_lshl_b32 s30, s30, 12
	s_add_u32 s28, s26, s30
	s_addc_u32 s29, s27, 0
	global_load_dwordx2 v[36:37], v162, s[28:29]
	v_fmac_f32_e32 v178, s25, v124
	v_fmac_f32_e32 v179, s25, v125
	v_fmac_f32_e32 v180, s25, v126
	v_fmac_f32_e32 v181, s25, v127
	v_fmac_f32_e32 v182, s25, v128
	v_fmac_f32_e32 v183, s25, v129
	v_fmac_f32_e32 v184, s25, v130
	v_fmac_f32_e32 v185, s25, v131
	s_waitcnt vmcnt(31)
	v_readlane_b32 s25, v246, 39
	v_cvt_f32_ubyte0_e32 v132, v38
	v_cvt_f32_ubyte1_e32 v133, v38
	v_cvt_f32_ubyte2_e32 v134, v38
	v_cvt_f32_ubyte3_e32 v135, v38
	v_cvt_f32_ubyte0_e32 v136, v39
	v_cvt_f32_ubyte1_e32 v137, v39
	v_cvt_f32_ubyte2_e32 v138, v39
	v_cvt_f32_ubyte3_e32 v139, v39
	v_readlane_b32 s30, v121, 7
	s_lshl_b32 s30, s30, 12
	s_add_u32 s28, s26, s30
	s_addc_u32 s29, s27, 0
	global_load_dwordx2 v[38:39], v162, s[28:29]
	v_fmac_f32_e32 v178, s25, v132
	v_fmac_f32_e32 v179, s25, v133
	v_fmac_f32_e32 v180, s25, v134
	v_fmac_f32_e32 v181, s25, v135
	v_fmac_f32_e32 v182, s25, v136
	v_fmac_f32_e32 v183, s25, v137
	v_fmac_f32_e32 v184, s25, v138
	v_fmac_f32_e32 v185, s25, v139
	s_waitcnt vmcnt(31)
	v_readlane_b32 s25, v246, 40
	v_cvt_f32_ubyte0_e32 v124, v40
	v_cvt_f32_ubyte1_e32 v125, v40
	v_cvt_f32_ubyte2_e32 v126, v40
	v_cvt_f32_ubyte3_e32 v127, v40
	v_cvt_f32_ubyte0_e32 v128, v41
	v_cvt_f32_ubyte1_e32 v129, v41
	v_cvt_f32_ubyte2_e32 v130, v41
	v_cvt_f32_ubyte3_e32 v131, v41
	v_readlane_b32 s30, v121, 8
	s_lshl_b32 s30, s30, 12
	s_add_u32 s28, s26, s30
	s_addc_u32 s29, s27, 0
	global_load_dwordx2 v[40:41], v162, s[28:29]
	v_fmac_f32_e32 v178, s25, v124
	v_fmac_f32_e32 v179, s25, v125
	v_fmac_f32_e32 v180, s25, v126
	v_fmac_f32_e32 v181, s25, v127
	v_fmac_f32_e32 v182, s25, v128
	v_fmac_f32_e32 v183, s25, v129
	v_fmac_f32_e32 v184, s25, v130
	v_fmac_f32_e32 v185, s25, v131
	s_waitcnt vmcnt(31)
	v_readlane_b32 s25, v246, 41
	v_cvt_f32_ubyte0_e32 v132, v42
	v_cvt_f32_ubyte1_e32 v133, v42
	v_cvt_f32_ubyte2_e32 v134, v42
	v_cvt_f32_ubyte3_e32 v135, v42
	v_cvt_f32_ubyte0_e32 v136, v43
	v_cvt_f32_ubyte1_e32 v137, v43
	v_cvt_f32_ubyte2_e32 v138, v43
	v_cvt_f32_ubyte3_e32 v139, v43
	v_readlane_b32 s30, v121, 9
	s_lshl_b32 s30, s30, 12
	s_add_u32 s28, s26, s30
	s_addc_u32 s29, s27, 0
	global_load_dwordx2 v[42:43], v162, s[28:29]
	v_fmac_f32_e32 v178, s25, v132
	v_fmac_f32_e32 v179, s25, v133
	v_fmac_f32_e32 v180, s25, v134
	v_fmac_f32_e32 v181, s25, v135
	v_fmac_f32_e32 v182, s25, v136
	v_fmac_f32_e32 v183, s25, v137
	v_fmac_f32_e32 v184, s25, v138
	v_fmac_f32_e32 v185, s25, v139
	s_waitcnt vmcnt(31)
	v_readlane_b32 s25, v246, 42
	v_cvt_f32_ubyte0_e32 v124, v44
	v_cvt_f32_ubyte1_e32 v125, v44
	v_cvt_f32_ubyte2_e32 v126, v44
	v_cvt_f32_ubyte3_e32 v127, v44
	v_cvt_f32_ubyte0_e32 v128, v45
	v_cvt_f32_ubyte1_e32 v129, v45
	v_cvt_f32_ubyte2_e32 v130, v45
	v_cvt_f32_ubyte3_e32 v131, v45
	v_readlane_b32 s30, v121, 10
	s_lshl_b32 s30, s30, 12
	s_add_u32 s28, s26, s30
	s_addc_u32 s29, s27, 0
	global_load_dwordx2 v[44:45], v162, s[28:29]
	v_fmac_f32_e32 v178, s25, v124
	v_fmac_f32_e32 v179, s25, v125
	v_fmac_f32_e32 v180, s25, v126
	v_fmac_f32_e32 v181, s25, v127
	v_fmac_f32_e32 v182, s25, v128
	v_fmac_f32_e32 v183, s25, v129
	v_fmac_f32_e32 v184, s25, v130
	v_fmac_f32_e32 v185, s25, v131
	s_waitcnt vmcnt(31)
	v_readlane_b32 s25, v246, 43
	v_cvt_f32_ubyte0_e32 v132, v46
	v_cvt_f32_ubyte1_e32 v133, v46
	v_cvt_f32_ubyte2_e32 v134, v46
	v_cvt_f32_ubyte3_e32 v135, v46
	v_cvt_f32_ubyte0_e32 v136, v47
	v_cvt_f32_ubyte1_e32 v137, v47
	v_cvt_f32_ubyte2_e32 v138, v47
	v_cvt_f32_ubyte3_e32 v139, v47
	v_readlane_b32 s30, v121, 11
	s_lshl_b32 s30, s30, 12
	s_add_u32 s28, s26, s30
	s_addc_u32 s29, s27, 0
	global_load_dwordx2 v[46:47], v162, s[28:29]
	v_fmac_f32_e32 v178, s25, v132
	v_fmac_f32_e32 v179, s25, v133
	v_fmac_f32_e32 v180, s25, v134
	v_fmac_f32_e32 v181, s25, v135
	v_fmac_f32_e32 v182, s25, v136
	v_fmac_f32_e32 v183, s25, v137
	v_fmac_f32_e32 v184, s25, v138
	v_fmac_f32_e32 v185, s25, v139
	s_waitcnt vmcnt(31)
	v_readlane_b32 s25, v246, 44
	v_cvt_f32_ubyte0_e32 v124, v48
	v_cvt_f32_ubyte1_e32 v125, v48
	v_cvt_f32_ubyte2_e32 v126, v48
	v_cvt_f32_ubyte3_e32 v127, v48
	v_cvt_f32_ubyte0_e32 v128, v49
	v_cvt_f32_ubyte1_e32 v129, v49
	v_cvt_f32_ubyte2_e32 v130, v49
	v_cvt_f32_ubyte3_e32 v131, v49
	v_readlane_b32 s30, v121, 12
	s_lshl_b32 s30, s30, 12
	s_add_u32 s28, s26, s30
	s_addc_u32 s29, s27, 0
	global_load_dwordx2 v[48:49], v162, s[28:29]
	v_fmac_f32_e32 v178, s25, v124
	v_fmac_f32_e32 v179, s25, v125
	v_fmac_f32_e32 v180, s25, v126
	v_fmac_f32_e32 v181, s25, v127
	v_fmac_f32_e32 v182, s25, v128
	v_fmac_f32_e32 v183, s25, v129
	v_fmac_f32_e32 v184, s25, v130
	v_fmac_f32_e32 v185, s25, v131
	s_waitcnt vmcnt(31)
	v_readlane_b32 s25, v246, 45
	v_cvt_f32_ubyte0_e32 v132, v50
	v_cvt_f32_ubyte1_e32 v133, v50
	v_cvt_f32_ubyte2_e32 v134, v50
	v_cvt_f32_ubyte3_e32 v135, v50
	v_cvt_f32_ubyte0_e32 v136, v51
	v_cvt_f32_ubyte1_e32 v137, v51
	v_cvt_f32_ubyte2_e32 v138, v51
	v_cvt_f32_ubyte3_e32 v139, v51
	v_readlane_b32 s30, v121, 13
	s_lshl_b32 s30, s30, 12
	s_add_u32 s28, s26, s30
	s_addc_u32 s29, s27, 0
	global_load_dwordx2 v[50:51], v162, s[28:29]
	v_fmac_f32_e32 v178, s25, v132
	v_fmac_f32_e32 v179, s25, v133
	v_fmac_f32_e32 v180, s25, v134
	v_fmac_f32_e32 v181, s25, v135
	v_fmac_f32_e32 v182, s25, v136
	v_fmac_f32_e32 v183, s25, v137
	v_fmac_f32_e32 v184, s25, v138
	v_fmac_f32_e32 v185, s25, v139
	s_waitcnt vmcnt(31)
	v_readlane_b32 s25, v246, 46
	v_cvt_f32_ubyte0_e32 v124, v52
	v_cvt_f32_ubyte1_e32 v125, v52
	v_cvt_f32_ubyte2_e32 v126, v52
	v_cvt_f32_ubyte3_e32 v127, v52
	v_cvt_f32_ubyte0_e32 v128, v53
	v_cvt_f32_ubyte1_e32 v129, v53
	v_cvt_f32_ubyte2_e32 v130, v53
	v_cvt_f32_ubyte3_e32 v131, v53
	v_readlane_b32 s30, v121, 14
	s_lshl_b32 s30, s30, 12
	s_add_u32 s28, s26, s30
	s_addc_u32 s29, s27, 0
	global_load_dwordx2 v[52:53], v162, s[28:29]
	v_fmac_f32_e32 v178, s25, v124
	v_fmac_f32_e32 v179, s25, v125
	v_fmac_f32_e32 v180, s25, v126
	v_fmac_f32_e32 v181, s25, v127
	v_fmac_f32_e32 v182, s25, v128
	v_fmac_f32_e32 v183, s25, v129
	v_fmac_f32_e32 v184, s25, v130
	v_fmac_f32_e32 v185, s25, v131
	s_waitcnt vmcnt(31)
	v_readlane_b32 s25, v246, 47
	v_cvt_f32_ubyte0_e32 v132, v54
	v_cvt_f32_ubyte1_e32 v133, v54
	v_cvt_f32_ubyte2_e32 v134, v54
	v_cvt_f32_ubyte3_e32 v135, v54
	v_cvt_f32_ubyte0_e32 v136, v55
	v_cvt_f32_ubyte1_e32 v137, v55
	v_cvt_f32_ubyte2_e32 v138, v55
	v_cvt_f32_ubyte3_e32 v139, v55
	v_readlane_b32 s30, v121, 15
	s_lshl_b32 s30, s30, 12
	s_add_u32 s28, s26, s30
	s_addc_u32 s29, s27, 0
	global_load_dwordx2 v[54:55], v162, s[28:29]
	v_fmac_f32_e32 v178, s25, v132
	v_fmac_f32_e32 v179, s25, v133
	v_fmac_f32_e32 v180, s25, v134
	v_fmac_f32_e32 v181, s25, v135
	v_fmac_f32_e32 v182, s25, v136
	v_fmac_f32_e32 v183, s25, v137
	v_fmac_f32_e32 v184, s25, v138
	v_fmac_f32_e32 v185, s25, v139
	s_waitcnt vmcnt(31)
	v_readlane_b32 s25, v246, 48
	v_cvt_f32_ubyte0_e32 v124, v56
	v_cvt_f32_ubyte1_e32 v125, v56
	v_cvt_f32_ubyte2_e32 v126, v56
	v_cvt_f32_ubyte3_e32 v127, v56
	v_cvt_f32_ubyte0_e32 v128, v57
	v_cvt_f32_ubyte1_e32 v129, v57
	v_cvt_f32_ubyte2_e32 v130, v57
	v_cvt_f32_ubyte3_e32 v131, v57
	v_readlane_b32 s30, v121, 16
	s_lshl_b32 s30, s30, 12
	s_add_u32 s28, s26, s30
	s_addc_u32 s29, s27, 0
	global_load_dwordx2 v[56:57], v162, s[28:29]
	v_fmac_f32_e32 v178, s25, v124
	v_fmac_f32_e32 v179, s25, v125
	v_fmac_f32_e32 v180, s25, v126
	v_fmac_f32_e32 v181, s25, v127
	v_fmac_f32_e32 v182, s25, v128
	v_fmac_f32_e32 v183, s25, v129
	v_fmac_f32_e32 v184, s25, v130
	v_fmac_f32_e32 v185, s25, v131
	s_waitcnt vmcnt(31)
	v_readlane_b32 s25, v246, 49
	v_cvt_f32_ubyte0_e32 v132, v58
	v_cvt_f32_ubyte1_e32 v133, v58
	v_cvt_f32_ubyte2_e32 v134, v58
	v_cvt_f32_ubyte3_e32 v135, v58
	v_cvt_f32_ubyte0_e32 v136, v59
	v_cvt_f32_ubyte1_e32 v137, v59
	v_cvt_f32_ubyte2_e32 v138, v59
	v_cvt_f32_ubyte3_e32 v139, v59
	v_readlane_b32 s30, v121, 17
	s_lshl_b32 s30, s30, 12
	s_add_u32 s28, s26, s30
	s_addc_u32 s29, s27, 0
	global_load_dwordx2 v[58:59], v162, s[28:29]
	v_fmac_f32_e32 v178, s25, v132
	v_fmac_f32_e32 v179, s25, v133
	v_fmac_f32_e32 v180, s25, v134
	v_fmac_f32_e32 v181, s25, v135
	v_fmac_f32_e32 v182, s25, v136
	v_fmac_f32_e32 v183, s25, v137
	v_fmac_f32_e32 v184, s25, v138
	v_fmac_f32_e32 v185, s25, v139
	s_waitcnt vmcnt(31)
	v_readlane_b32 s25, v246, 50
	v_cvt_f32_ubyte0_e32 v124, v60
	v_cvt_f32_ubyte1_e32 v125, v60
	v_cvt_f32_ubyte2_e32 v126, v60
	v_cvt_f32_ubyte3_e32 v127, v60
	v_cvt_f32_ubyte0_e32 v128, v61
	v_cvt_f32_ubyte1_e32 v129, v61
	v_cvt_f32_ubyte2_e32 v130, v61
	v_cvt_f32_ubyte3_e32 v131, v61
	v_readlane_b32 s30, v121, 18
	s_lshl_b32 s30, s30, 12
	s_add_u32 s28, s26, s30
	s_addc_u32 s29, s27, 0
	global_load_dwordx2 v[60:61], v162, s[28:29]
	v_fmac_f32_e32 v178, s25, v124
	v_fmac_f32_e32 v179, s25, v125
	v_fmac_f32_e32 v180, s25, v126
	v_fmac_f32_e32 v181, s25, v127
	v_fmac_f32_e32 v182, s25, v128
	v_fmac_f32_e32 v183, s25, v129
	v_fmac_f32_e32 v184, s25, v130
	v_fmac_f32_e32 v185, s25, v131
	s_waitcnt vmcnt(31)
	v_readlane_b32 s25, v246, 51
	v_cvt_f32_ubyte0_e32 v132, v62
	v_cvt_f32_ubyte1_e32 v133, v62
	v_cvt_f32_ubyte2_e32 v134, v62
	v_cvt_f32_ubyte3_e32 v135, v62
	v_cvt_f32_ubyte0_e32 v136, v63
	v_cvt_f32_ubyte1_e32 v137, v63
	v_cvt_f32_ubyte2_e32 v138, v63
	v_cvt_f32_ubyte3_e32 v139, v63
	v_readlane_b32 s30, v121, 19
	s_lshl_b32 s30, s30, 12
	s_add_u32 s28, s26, s30
	s_addc_u32 s29, s27, 0
	global_load_dwordx2 v[62:63], v162, s[28:29]
	v_fmac_f32_e32 v178, s25, v132
	v_fmac_f32_e32 v179, s25, v133
	v_fmac_f32_e32 v180, s25, v134
	v_fmac_f32_e32 v181, s25, v135
	v_fmac_f32_e32 v182, s25, v136
	v_fmac_f32_e32 v183, s25, v137
	v_fmac_f32_e32 v184, s25, v138
	v_fmac_f32_e32 v185, s25, v139
	s_waitcnt vmcnt(31)
	v_readlane_b32 s25, v246, 52
	v_cvt_f32_ubyte0_e32 v124, v64
	v_cvt_f32_ubyte1_e32 v125, v64
	v_cvt_f32_ubyte2_e32 v126, v64
	v_cvt_f32_ubyte3_e32 v127, v64
	v_cvt_f32_ubyte0_e32 v128, v65
	v_cvt_f32_ubyte1_e32 v129, v65
	v_cvt_f32_ubyte2_e32 v130, v65
	v_cvt_f32_ubyte3_e32 v131, v65
	v_readlane_b32 s30, v121, 20
	s_lshl_b32 s30, s30, 12
	s_add_u32 s28, s26, s30
	s_addc_u32 s29, s27, 0
	global_load_dwordx2 v[64:65], v162, s[28:29]
	v_fmac_f32_e32 v178, s25, v124
	v_fmac_f32_e32 v179, s25, v125
	v_fmac_f32_e32 v180, s25, v126
	v_fmac_f32_e32 v181, s25, v127
	v_fmac_f32_e32 v182, s25, v128
	v_fmac_f32_e32 v183, s25, v129
	v_fmac_f32_e32 v184, s25, v130
	v_fmac_f32_e32 v185, s25, v131
	s_waitcnt vmcnt(31)
	v_readlane_b32 s25, v246, 53
	v_cvt_f32_ubyte0_e32 v132, v66
	v_cvt_f32_ubyte1_e32 v133, v66
	v_cvt_f32_ubyte2_e32 v134, v66
	v_cvt_f32_ubyte3_e32 v135, v66
	v_cvt_f32_ubyte0_e32 v136, v67
	v_cvt_f32_ubyte1_e32 v137, v67
	v_cvt_f32_ubyte2_e32 v138, v67
	v_cvt_f32_ubyte3_e32 v139, v67
	v_readlane_b32 s30, v121, 21
	s_lshl_b32 s30, s30, 12
	s_add_u32 s28, s26, s30
	s_addc_u32 s29, s27, 0
	global_load_dwordx2 v[66:67], v162, s[28:29]
	v_fmac_f32_e32 v178, s25, v132
	v_fmac_f32_e32 v179, s25, v133
	v_fmac_f32_e32 v180, s25, v134
	v_fmac_f32_e32 v181, s25, v135
	v_fmac_f32_e32 v182, s25, v136
	v_fmac_f32_e32 v183, s25, v137
	v_fmac_f32_e32 v184, s25, v138
	v_fmac_f32_e32 v185, s25, v139
	s_waitcnt vmcnt(31)
	v_readlane_b32 s25, v246, 54
	v_cvt_f32_ubyte0_e32 v124, v68
	v_cvt_f32_ubyte1_e32 v125, v68
	v_cvt_f32_ubyte2_e32 v126, v68
	v_cvt_f32_ubyte3_e32 v127, v68
	v_cvt_f32_ubyte0_e32 v128, v69
	v_cvt_f32_ubyte1_e32 v129, v69
	v_cvt_f32_ubyte2_e32 v130, v69
	v_cvt_f32_ubyte3_e32 v131, v69
	v_readlane_b32 s30, v121, 22
	s_lshl_b32 s30, s30, 12
	s_add_u32 s28, s26, s30
	s_addc_u32 s29, s27, 0
	global_load_dwordx2 v[68:69], v162, s[28:29]
	v_fmac_f32_e32 v178, s25, v124
	v_fmac_f32_e32 v179, s25, v125
	v_fmac_f32_e32 v180, s25, v126
	v_fmac_f32_e32 v181, s25, v127
	v_fmac_f32_e32 v182, s25, v128
	v_fmac_f32_e32 v183, s25, v129
	v_fmac_f32_e32 v184, s25, v130
	v_fmac_f32_e32 v185, s25, v131
	s_waitcnt vmcnt(31)
	v_readlane_b32 s25, v246, 55
	v_cvt_f32_ubyte0_e32 v132, v70
	v_cvt_f32_ubyte1_e32 v133, v70
	v_cvt_f32_ubyte2_e32 v134, v70
	v_cvt_f32_ubyte3_e32 v135, v70
	v_cvt_f32_ubyte0_e32 v136, v71
	v_cvt_f32_ubyte1_e32 v137, v71
	v_cvt_f32_ubyte2_e32 v138, v71
	v_cvt_f32_ubyte3_e32 v139, v71
	v_readlane_b32 s30, v121, 23
	s_lshl_b32 s30, s30, 12
	s_add_u32 s28, s26, s30
	s_addc_u32 s29, s27, 0
	global_load_dwordx2 v[70:71], v162, s[28:29]
	v_fmac_f32_e32 v178, s25, v132
	v_fmac_f32_e32 v179, s25, v133
	v_fmac_f32_e32 v180, s25, v134
	v_fmac_f32_e32 v181, s25, v135
	v_fmac_f32_e32 v182, s25, v136
	v_fmac_f32_e32 v183, s25, v137
	v_fmac_f32_e32 v184, s25, v138
	v_fmac_f32_e32 v185, s25, v139
	s_waitcnt vmcnt(31)
	v_readlane_b32 s25, v246, 56
	v_cvt_f32_ubyte0_e32 v124, v72
	v_cvt_f32_ubyte1_e32 v125, v72
	v_cvt_f32_ubyte2_e32 v126, v72
	v_cvt_f32_ubyte3_e32 v127, v72
	v_cvt_f32_ubyte0_e32 v128, v73
	v_cvt_f32_ubyte1_e32 v129, v73
	v_cvt_f32_ubyte2_e32 v130, v73
	v_cvt_f32_ubyte3_e32 v131, v73
	v_readlane_b32 s30, v121, 24
	s_lshl_b32 s30, s30, 12
	s_add_u32 s28, s26, s30
	s_addc_u32 s29, s27, 0
	global_load_dwordx2 v[72:73], v162, s[28:29]
	v_fmac_f32_e32 v178, s25, v124
	v_fmac_f32_e32 v179, s25, v125
	v_fmac_f32_e32 v180, s25, v126
	v_fmac_f32_e32 v181, s25, v127
	v_fmac_f32_e32 v182, s25, v128
	v_fmac_f32_e32 v183, s25, v129
	v_fmac_f32_e32 v184, s25, v130
	v_fmac_f32_e32 v185, s25, v131
	s_waitcnt vmcnt(31)
	v_readlane_b32 s25, v246, 57
	v_cvt_f32_ubyte0_e32 v132, v74
	v_cvt_f32_ubyte1_e32 v133, v74
	v_cvt_f32_ubyte2_e32 v134, v74
	v_cvt_f32_ubyte3_e32 v135, v74
	v_cvt_f32_ubyte0_e32 v136, v75
	v_cvt_f32_ubyte1_e32 v137, v75
	v_cvt_f32_ubyte2_e32 v138, v75
	v_cvt_f32_ubyte3_e32 v139, v75
	v_readlane_b32 s30, v121, 25
	s_lshl_b32 s30, s30, 12
	s_add_u32 s28, s26, s30
	s_addc_u32 s29, s27, 0
	global_load_dwordx2 v[74:75], v162, s[28:29]
	v_fmac_f32_e32 v178, s25, v132
	v_fmac_f32_e32 v179, s25, v133
	v_fmac_f32_e32 v180, s25, v134
	v_fmac_f32_e32 v181, s25, v135
	v_fmac_f32_e32 v182, s25, v136
	v_fmac_f32_e32 v183, s25, v137
	v_fmac_f32_e32 v184, s25, v138
	v_fmac_f32_e32 v185, s25, v139
	s_waitcnt vmcnt(31)
	v_readlane_b32 s25, v246, 58
	v_cvt_f32_ubyte0_e32 v124, v76
	v_cvt_f32_ubyte1_e32 v125, v76
	v_cvt_f32_ubyte2_e32 v126, v76
	v_cvt_f32_ubyte3_e32 v127, v76
	v_cvt_f32_ubyte0_e32 v128, v77
	v_cvt_f32_ubyte1_e32 v129, v77
	v_cvt_f32_ubyte2_e32 v130, v77
	v_cvt_f32_ubyte3_e32 v131, v77
	v_readlane_b32 s30, v121, 26
	s_lshl_b32 s30, s30, 12
	s_add_u32 s28, s26, s30
	s_addc_u32 s29, s27, 0
	global_load_dwordx2 v[76:77], v162, s[28:29]
	v_fmac_f32_e32 v178, s25, v124
	v_fmac_f32_e32 v179, s25, v125
	v_fmac_f32_e32 v180, s25, v126
	v_fmac_f32_e32 v181, s25, v127
	v_fmac_f32_e32 v182, s25, v128
	v_fmac_f32_e32 v183, s25, v129
	v_fmac_f32_e32 v184, s25, v130
	v_fmac_f32_e32 v185, s25, v131
	s_waitcnt vmcnt(31)
	v_readlane_b32 s25, v246, 59
	v_cvt_f32_ubyte0_e32 v132, v78
	v_cvt_f32_ubyte1_e32 v133, v78
	v_cvt_f32_ubyte2_e32 v134, v78
	v_cvt_f32_ubyte3_e32 v135, v78
	v_cvt_f32_ubyte0_e32 v136, v79
	v_cvt_f32_ubyte1_e32 v137, v79
	v_cvt_f32_ubyte2_e32 v138, v79
	v_cvt_f32_ubyte3_e32 v139, v79
	v_readlane_b32 s30, v121, 27
	s_lshl_b32 s30, s30, 12
	s_add_u32 s28, s26, s30
	s_addc_u32 s29, s27, 0
	global_load_dwordx2 v[78:79], v162, s[28:29]
	v_fmac_f32_e32 v178, s25, v132
	v_fmac_f32_e32 v179, s25, v133
	v_fmac_f32_e32 v180, s25, v134
	v_fmac_f32_e32 v181, s25, v135
	v_fmac_f32_e32 v182, s25, v136
	v_fmac_f32_e32 v183, s25, v137
	v_fmac_f32_e32 v184, s25, v138
	v_fmac_f32_e32 v185, s25, v139
	s_waitcnt vmcnt(31)
	v_readlane_b32 s25, v246, 60
	v_cvt_f32_ubyte0_e32 v124, v80
	v_cvt_f32_ubyte1_e32 v125, v80
	v_cvt_f32_ubyte2_e32 v126, v80
	v_cvt_f32_ubyte3_e32 v127, v80
	v_cvt_f32_ubyte0_e32 v128, v81
	v_cvt_f32_ubyte1_e32 v129, v81
	v_cvt_f32_ubyte2_e32 v130, v81
	v_cvt_f32_ubyte3_e32 v131, v81
	v_readlane_b32 s30, v121, 28
	s_lshl_b32 s30, s30, 12
	s_add_u32 s28, s26, s30
	s_addc_u32 s29, s27, 0
	global_load_dwordx2 v[80:81], v162, s[28:29]
	v_fmac_f32_e32 v178, s25, v124
	v_fmac_f32_e32 v179, s25, v125
	v_fmac_f32_e32 v180, s25, v126
	v_fmac_f32_e32 v181, s25, v127
	v_fmac_f32_e32 v182, s25, v128
	v_fmac_f32_e32 v183, s25, v129
	v_fmac_f32_e32 v184, s25, v130
	v_fmac_f32_e32 v185, s25, v131
	s_waitcnt vmcnt(31)
	v_readlane_b32 s25, v246, 61
	v_cvt_f32_ubyte0_e32 v132, v82
	v_cvt_f32_ubyte1_e32 v133, v82
	v_cvt_f32_ubyte2_e32 v134, v82
	v_cvt_f32_ubyte3_e32 v135, v82
	v_cvt_f32_ubyte0_e32 v136, v83
	v_cvt_f32_ubyte1_e32 v137, v83
	v_cvt_f32_ubyte2_e32 v138, v83
	v_cvt_f32_ubyte3_e32 v139, v83
	v_readlane_b32 s30, v121, 29
	s_lshl_b32 s30, s30, 12
	s_add_u32 s28, s26, s30
	s_addc_u32 s29, s27, 0
	global_load_dwordx2 v[82:83], v162, s[28:29]
	v_fmac_f32_e32 v178, s25, v132
	v_fmac_f32_e32 v179, s25, v133
	v_fmac_f32_e32 v180, s25, v134
	v_fmac_f32_e32 v181, s25, v135
	v_fmac_f32_e32 v182, s25, v136
	v_fmac_f32_e32 v183, s25, v137
	v_fmac_f32_e32 v184, s25, v138
	v_fmac_f32_e32 v185, s25, v139
	s_waitcnt vmcnt(31)
	v_readlane_b32 s25, v246, 62
	v_cvt_f32_ubyte0_e32 v124, v84
	v_cvt_f32_ubyte1_e32 v125, v84
	v_cvt_f32_ubyte2_e32 v126, v84
	v_cvt_f32_ubyte3_e32 v127, v84
	v_cvt_f32_ubyte0_e32 v128, v85
	v_cvt_f32_ubyte1_e32 v129, v85
	v_cvt_f32_ubyte2_e32 v130, v85
	v_cvt_f32_ubyte3_e32 v131, v85
	v_readlane_b32 s30, v121, 30
	s_lshl_b32 s30, s30, 12
	s_add_u32 s28, s26, s30
	s_addc_u32 s29, s27, 0
	global_load_dwordx2 v[84:85], v162, s[28:29]
	v_fmac_f32_e32 v178, s25, v124
	v_fmac_f32_e32 v179, s25, v125
	v_fmac_f32_e32 v180, s25, v126
	v_fmac_f32_e32 v181, s25, v127
	v_fmac_f32_e32 v182, s25, v128
	v_fmac_f32_e32 v183, s25, v129
	v_fmac_f32_e32 v184, s25, v130
	v_fmac_f32_e32 v185, s25, v131
	s_waitcnt vmcnt(31)
	v_readlane_b32 s25, v246, 63
	v_cvt_f32_ubyte0_e32 v132, v86
	v_cvt_f32_ubyte1_e32 v133, v86
	v_cvt_f32_ubyte2_e32 v134, v86
	v_cvt_f32_ubyte3_e32 v135, v86
	v_cvt_f32_ubyte0_e32 v136, v87
	v_cvt_f32_ubyte1_e32 v137, v87
	v_cvt_f32_ubyte2_e32 v138, v87
	v_cvt_f32_ubyte3_e32 v139, v87
	v_readlane_b32 s30, v121, 31
	s_lshl_b32 s30, s30, 12
	s_add_u32 s28, s26, s30
	s_addc_u32 s29, s27, 0
	global_load_dwordx2 v[86:87], v162, s[28:29]
	v_fmac_f32_e32 v178, s25, v132
	v_fmac_f32_e32 v179, s25, v133
	v_fmac_f32_e32 v180, s25, v134
	v_fmac_f32_e32 v181, s25, v135
	v_fmac_f32_e32 v182, s25, v136
	v_fmac_f32_e32 v183, s25, v137
	v_fmac_f32_e32 v184, s25, v138
	v_fmac_f32_e32 v185, s25, v139
	s_waitcnt vmcnt(31)
	v_readlane_b32 s25, v247, 0
	v_cvt_f32_ubyte0_e32 v124, v24
	v_cvt_f32_ubyte1_e32 v125, v24
	v_cvt_f32_ubyte2_e32 v126, v24
	v_cvt_f32_ubyte3_e32 v127, v24
	v_cvt_f32_ubyte0_e32 v128, v25
	v_cvt_f32_ubyte1_e32 v129, v25
	v_cvt_f32_ubyte2_e32 v130, v25
	v_cvt_f32_ubyte3_e32 v131, v25
	v_readlane_b32 s30, v121, 32
	s_lshl_b32 s30, s30, 12
	s_add_u32 s28, s26, s30
	s_addc_u32 s29, s27, 0
	global_load_dwordx2 v[24:25], v162, s[28:29]
	v_lshlrev_b32_e32 v16, 2, v122
	v_lshlrev_b32_e32 v17, 2, v123
	global_load_dword v238, v16, s[64:65]
	global_load_dword v240, v16, s[60:61]
	global_load_dword v239, v17, s[64:65]
	global_load_dword v241, v17, s[60:61]
	v_fmac_f32_e32 v178, s25, v124
	v_fmac_f32_e32 v179, s25, v125
	v_fmac_f32_e32 v180, s25, v126
	v_fmac_f32_e32 v181, s25, v127
	v_fmac_f32_e32 v182, s25, v128
	v_fmac_f32_e32 v183, s25, v129
	v_fmac_f32_e32 v184, s25, v130
	v_fmac_f32_e32 v185, s25, v131
	s_waitcnt vmcnt(35)
	v_readlane_b32 s25, v247, 1
	v_cvt_f32_ubyte0_e32 v132, v26
	v_cvt_f32_ubyte1_e32 v133, v26
	v_cvt_f32_ubyte2_e32 v134, v26
	v_cvt_f32_ubyte3_e32 v135, v26
	v_cvt_f32_ubyte0_e32 v136, v27
	v_cvt_f32_ubyte1_e32 v137, v27
	v_cvt_f32_ubyte2_e32 v138, v27
	v_cvt_f32_ubyte3_e32 v139, v27
	v_readlane_b32 s30, v121, 33
	s_lshl_b32 s30, s30, 12
	s_add_u32 s28, s26, s30
	s_addc_u32 s29, s27, 0
	global_load_dwordx2 v[26:27], v162, s[28:29]
	v_fmac_f32_e32 v178, s25, v132
	v_fmac_f32_e32 v179, s25, v133
	v_fmac_f32_e32 v180, s25, v134
	v_fmac_f32_e32 v181, s25, v135
	v_fmac_f32_e32 v182, s25, v136
	v_fmac_f32_e32 v183, s25, v137
	v_fmac_f32_e32 v184, s25, v138
	v_fmac_f32_e32 v185, s25, v139
	s_waitcnt vmcnt(35)
	v_readlane_b32 s25, v247, 2
	v_cvt_f32_ubyte0_e32 v124, v28
	v_cvt_f32_ubyte1_e32 v125, v28
	v_cvt_f32_ubyte2_e32 v126, v28
	v_cvt_f32_ubyte3_e32 v127, v28
	v_cvt_f32_ubyte0_e32 v128, v29
	v_cvt_f32_ubyte1_e32 v129, v29
	v_cvt_f32_ubyte2_e32 v130, v29
	v_cvt_f32_ubyte3_e32 v131, v29
	v_readlane_b32 s30, v121, 34
	s_lshl_b32 s30, s30, 12
	s_add_u32 s28, s26, s30
	s_addc_u32 s29, s27, 0
	global_load_dwordx2 v[28:29], v162, s[28:29]
	v_fmac_f32_e32 v178, s25, v124
	v_fmac_f32_e32 v179, s25, v125
	v_fmac_f32_e32 v180, s25, v126
	v_fmac_f32_e32 v181, s25, v127
	v_fmac_f32_e32 v182, s25, v128
	v_fmac_f32_e32 v183, s25, v129
	v_fmac_f32_e32 v184, s25, v130
	v_fmac_f32_e32 v185, s25, v131
	s_waitcnt vmcnt(35)
	v_readlane_b32 s25, v247, 3
	v_cvt_f32_ubyte0_e32 v132, v30
	v_cvt_f32_ubyte1_e32 v133, v30
	v_cvt_f32_ubyte2_e32 v134, v30
	v_cvt_f32_ubyte3_e32 v135, v30
	v_cvt_f32_ubyte0_e32 v136, v31
	v_cvt_f32_ubyte1_e32 v137, v31
	v_cvt_f32_ubyte2_e32 v138, v31
	v_cvt_f32_ubyte3_e32 v139, v31
	v_readlane_b32 s30, v121, 35
	s_lshl_b32 s30, s30, 12
	s_add_u32 s28, s26, s30
	s_addc_u32 s29, s27, 0
	global_load_dwordx2 v[30:31], v162, s[28:29]
	v_fmac_f32_e32 v178, s25, v132
	v_fmac_f32_e32 v179, s25, v133
	v_fmac_f32_e32 v180, s25, v134
	v_fmac_f32_e32 v181, s25, v135
	v_fmac_f32_e32 v182, s25, v136
	v_fmac_f32_e32 v183, s25, v137
	v_fmac_f32_e32 v184, s25, v138
	v_fmac_f32_e32 v185, s25, v139
	s_waitcnt vmcnt(35)
	v_readlane_b32 s25, v247, 4
	v_cvt_f32_ubyte0_e32 v124, v32
	v_cvt_f32_ubyte1_e32 v125, v32
	v_cvt_f32_ubyte2_e32 v126, v32
	v_cvt_f32_ubyte3_e32 v127, v32
	v_cvt_f32_ubyte0_e32 v128, v33
	v_cvt_f32_ubyte1_e32 v129, v33
	v_cvt_f32_ubyte2_e32 v130, v33
	v_cvt_f32_ubyte3_e32 v131, v33
	v_readlane_b32 s30, v121, 36
	s_lshl_b32 s30, s30, 12
	s_add_u32 s28, s26, s30
	s_addc_u32 s29, s27, 0
	global_load_dwordx2 v[32:33], v162, s[28:29]
	v_fmac_f32_e32 v178, s25, v124
	v_fmac_f32_e32 v179, s25, v125
	v_fmac_f32_e32 v180, s25, v126
	v_fmac_f32_e32 v181, s25, v127
	v_fmac_f32_e32 v182, s25, v128
	v_fmac_f32_e32 v183, s25, v129
	v_fmac_f32_e32 v184, s25, v130
	v_fmac_f32_e32 v185, s25, v131
	s_waitcnt vmcnt(35)
	v_readlane_b32 s25, v247, 5
	v_cvt_f32_ubyte0_e32 v132, v34
	v_cvt_f32_ubyte1_e32 v133, v34
	v_cvt_f32_ubyte2_e32 v134, v34
	v_cvt_f32_ubyte3_e32 v135, v34
	v_cvt_f32_ubyte0_e32 v136, v35
	v_cvt_f32_ubyte1_e32 v137, v35
	v_cvt_f32_ubyte2_e32 v138, v35
	v_cvt_f32_ubyte3_e32 v139, v35
	v_readlane_b32 s30, v121, 37
	s_lshl_b32 s30, s30, 12
	s_add_u32 s28, s26, s30
	s_addc_u32 s29, s27, 0
	global_load_dwordx2 v[34:35], v162, s[28:29]
	v_fmac_f32_e32 v178, s25, v132
	v_fmac_f32_e32 v179, s25, v133
	v_fmac_f32_e32 v180, s25, v134
	v_fmac_f32_e32 v181, s25, v135
	v_fmac_f32_e32 v182, s25, v136
	v_fmac_f32_e32 v183, s25, v137
	v_fmac_f32_e32 v184, s25, v138
	v_fmac_f32_e32 v185, s25, v139
	s_waitcnt vmcnt(35)
	v_readlane_b32 s25, v247, 6
	v_cvt_f32_ubyte0_e32 v124, v36
	v_cvt_f32_ubyte1_e32 v125, v36
	v_cvt_f32_ubyte2_e32 v126, v36
	v_cvt_f32_ubyte3_e32 v127, v36
	v_cvt_f32_ubyte0_e32 v128, v37
	v_cvt_f32_ubyte1_e32 v129, v37
	v_cvt_f32_ubyte2_e32 v130, v37
	v_cvt_f32_ubyte3_e32 v131, v37
	v_readlane_b32 s30, v121, 38
	s_lshl_b32 s30, s30, 12
	s_add_u32 s28, s26, s30
	s_addc_u32 s29, s27, 0
	global_load_dwordx2 v[36:37], v162, s[28:29]
	v_fmac_f32_e32 v178, s25, v124
	v_fmac_f32_e32 v179, s25, v125
	v_fmac_f32_e32 v180, s25, v126
	v_fmac_f32_e32 v181, s25, v127
	v_fmac_f32_e32 v182, s25, v128
	v_fmac_f32_e32 v183, s25, v129
	v_fmac_f32_e32 v184, s25, v130
	v_fmac_f32_e32 v185, s25, v131
	s_waitcnt vmcnt(35)
	v_readlane_b32 s25, v247, 7
	v_cvt_f32_ubyte0_e32 v132, v38
	v_cvt_f32_ubyte1_e32 v133, v38
	v_cvt_f32_ubyte2_e32 v134, v38
	v_cvt_f32_ubyte3_e32 v135, v38
	v_cvt_f32_ubyte0_e32 v136, v39
	v_cvt_f32_ubyte1_e32 v137, v39
	v_cvt_f32_ubyte2_e32 v138, v39
	v_cvt_f32_ubyte3_e32 v139, v39
	v_readlane_b32 s30, v121, 39
	s_lshl_b32 s30, s30, 12
	s_add_u32 s28, s26, s30
	s_addc_u32 s29, s27, 0
	global_load_dwordx2 v[38:39], v162, s[28:29]
	v_fmac_f32_e32 v178, s25, v132
	v_fmac_f32_e32 v179, s25, v133
	v_fmac_f32_e32 v180, s25, v134
	v_fmac_f32_e32 v181, s25, v135
	v_fmac_f32_e32 v182, s25, v136
	v_fmac_f32_e32 v183, s25, v137
	v_fmac_f32_e32 v184, s25, v138
	v_fmac_f32_e32 v185, s25, v139
	s_waitcnt vmcnt(35)
	v_readlane_b32 s25, v247, 8
	v_cvt_f32_ubyte0_e32 v124, v40
	v_cvt_f32_ubyte1_e32 v125, v40
	v_cvt_f32_ubyte2_e32 v126, v40
	v_cvt_f32_ubyte3_e32 v127, v40
	v_cvt_f32_ubyte0_e32 v128, v41
	v_cvt_f32_ubyte1_e32 v129, v41
	v_cvt_f32_ubyte2_e32 v130, v41
	v_cvt_f32_ubyte3_e32 v131, v41
	v_readlane_b32 s30, v121, 40
	s_lshl_b32 s30, s30, 12
	s_add_u32 s28, s26, s30
	s_addc_u32 s29, s27, 0
	global_load_dwordx2 v[40:41], v162, s[28:29]
	v_fmac_f32_e32 v178, s25, v124
	v_fmac_f32_e32 v179, s25, v125
	v_fmac_f32_e32 v180, s25, v126
	v_fmac_f32_e32 v181, s25, v127
	v_fmac_f32_e32 v182, s25, v128
	v_fmac_f32_e32 v183, s25, v129
	v_fmac_f32_e32 v184, s25, v130
	v_fmac_f32_e32 v185, s25, v131
	s_waitcnt vmcnt(35)
	v_readlane_b32 s25, v247, 9
	v_cvt_f32_ubyte0_e32 v132, v42
	v_cvt_f32_ubyte1_e32 v133, v42
	v_cvt_f32_ubyte2_e32 v134, v42
	v_cvt_f32_ubyte3_e32 v135, v42
	v_cvt_f32_ubyte0_e32 v136, v43
	v_cvt_f32_ubyte1_e32 v137, v43
	v_cvt_f32_ubyte2_e32 v138, v43
	v_cvt_f32_ubyte3_e32 v139, v43
	v_readlane_b32 s30, v121, 41
	s_lshl_b32 s30, s30, 12
	s_add_u32 s28, s26, s30
	s_addc_u32 s29, s27, 0
	global_load_dwordx2 v[42:43], v162, s[28:29]
	v_fmac_f32_e32 v178, s25, v132
	v_fmac_f32_e32 v179, s25, v133
	v_fmac_f32_e32 v180, s25, v134
	v_fmac_f32_e32 v181, s25, v135
	v_fmac_f32_e32 v182, s25, v136
	v_fmac_f32_e32 v183, s25, v137
	v_fmac_f32_e32 v184, s25, v138
	v_fmac_f32_e32 v185, s25, v139
	s_waitcnt vmcnt(35)
	v_readlane_b32 s25, v247, 10
	v_cvt_f32_ubyte0_e32 v124, v44
	v_cvt_f32_ubyte1_e32 v125, v44
	v_cvt_f32_ubyte2_e32 v126, v44
	v_cvt_f32_ubyte3_e32 v127, v44
	v_cvt_f32_ubyte0_e32 v128, v45
	v_cvt_f32_ubyte1_e32 v129, v45
	v_cvt_f32_ubyte2_e32 v130, v45
	v_cvt_f32_ubyte3_e32 v131, v45
	v_readlane_b32 s30, v121, 42
	s_lshl_b32 s30, s30, 12
	s_add_u32 s28, s26, s30
	s_addc_u32 s29, s27, 0
	global_load_dwordx2 v[44:45], v162, s[28:29]
	v_fmac_f32_e32 v178, s25, v124
	v_fmac_f32_e32 v179, s25, v125
	v_fmac_f32_e32 v180, s25, v126
	v_fmac_f32_e32 v181, s25, v127
	v_fmac_f32_e32 v182, s25, v128
	v_fmac_f32_e32 v183, s25, v129
	v_fmac_f32_e32 v184, s25, v130
	v_fmac_f32_e32 v185, s25, v131
	s_waitcnt vmcnt(35)
	v_readlane_b32 s25, v247, 11
	v_cvt_f32_ubyte0_e32 v132, v46
	v_cvt_f32_ubyte1_e32 v133, v46
	v_cvt_f32_ubyte2_e32 v134, v46
	v_cvt_f32_ubyte3_e32 v135, v46
	v_cvt_f32_ubyte0_e32 v136, v47
	v_cvt_f32_ubyte1_e32 v137, v47
	v_cvt_f32_ubyte2_e32 v138, v47
	v_cvt_f32_ubyte3_e32 v139, v47
	v_readlane_b32 s30, v121, 43
	s_lshl_b32 s30, s30, 12
	s_add_u32 s28, s26, s30
	s_addc_u32 s29, s27, 0
	global_load_dwordx2 v[46:47], v162, s[28:29]
	v_fmac_f32_e32 v178, s25, v132
	v_fmac_f32_e32 v179, s25, v133
	v_fmac_f32_e32 v180, s25, v134
	v_fmac_f32_e32 v181, s25, v135
	v_fmac_f32_e32 v182, s25, v136
	v_fmac_f32_e32 v183, s25, v137
	v_fmac_f32_e32 v184, s25, v138
	v_fmac_f32_e32 v185, s25, v139
	s_waitcnt vmcnt(35)
	v_readlane_b32 s25, v247, 12
	v_cvt_f32_ubyte0_e32 v124, v48
	v_cvt_f32_ubyte1_e32 v125, v48
	v_cvt_f32_ubyte2_e32 v126, v48
	v_cvt_f32_ubyte3_e32 v127, v48
	v_cvt_f32_ubyte0_e32 v128, v49
	v_cvt_f32_ubyte1_e32 v129, v49
	v_cvt_f32_ubyte2_e32 v130, v49
	v_cvt_f32_ubyte3_e32 v131, v49
	v_readlane_b32 s30, v121, 44
	s_lshl_b32 s30, s30, 12
	s_add_u32 s28, s26, s30
	s_addc_u32 s29, s27, 0
	global_load_dwordx2 v[48:49], v162, s[28:29]
	v_fmac_f32_e32 v178, s25, v124
	v_fmac_f32_e32 v179, s25, v125
	v_fmac_f32_e32 v180, s25, v126
	v_fmac_f32_e32 v181, s25, v127
	v_fmac_f32_e32 v182, s25, v128
	v_fmac_f32_e32 v183, s25, v129
	v_fmac_f32_e32 v184, s25, v130
	v_fmac_f32_e32 v185, s25, v131
	s_waitcnt vmcnt(35)
	v_readlane_b32 s25, v247, 13
	v_cvt_f32_ubyte0_e32 v132, v50
	v_cvt_f32_ubyte1_e32 v133, v50
	v_cvt_f32_ubyte2_e32 v134, v50
	v_cvt_f32_ubyte3_e32 v135, v50
	v_cvt_f32_ubyte0_e32 v136, v51
	v_cvt_f32_ubyte1_e32 v137, v51
	v_cvt_f32_ubyte2_e32 v138, v51
	v_cvt_f32_ubyte3_e32 v139, v51
	v_readlane_b32 s30, v121, 45
	s_lshl_b32 s30, s30, 12
	s_add_u32 s28, s26, s30
	s_addc_u32 s29, s27, 0
	global_load_dwordx2 v[50:51], v162, s[28:29]
	v_fmac_f32_e32 v178, s25, v132
	v_fmac_f32_e32 v179, s25, v133
	v_fmac_f32_e32 v180, s25, v134
	v_fmac_f32_e32 v181, s25, v135
	v_fmac_f32_e32 v182, s25, v136
	v_fmac_f32_e32 v183, s25, v137
	v_fmac_f32_e32 v184, s25, v138
	v_fmac_f32_e32 v185, s25, v139
	s_waitcnt vmcnt(35)
	v_readlane_b32 s25, v247, 14
	v_cvt_f32_ubyte0_e32 v124, v52
	v_cvt_f32_ubyte1_e32 v125, v52
	v_cvt_f32_ubyte2_e32 v126, v52
	v_cvt_f32_ubyte3_e32 v127, v52
	v_cvt_f32_ubyte0_e32 v128, v53
	v_cvt_f32_ubyte1_e32 v129, v53
	v_cvt_f32_ubyte2_e32 v130, v53
	v_cvt_f32_ubyte3_e32 v131, v53
	v_readlane_b32 s30, v121, 46
	s_lshl_b32 s30, s30, 12
	s_add_u32 s28, s26, s30
	s_addc_u32 s29, s27, 0
	global_load_dwordx2 v[52:53], v162, s[28:29]
	v_fmac_f32_e32 v178, s25, v124
	v_fmac_f32_e32 v179, s25, v125
	v_fmac_f32_e32 v180, s25, v126
	v_fmac_f32_e32 v181, s25, v127
	v_fmac_f32_e32 v182, s25, v128
	v_fmac_f32_e32 v183, s25, v129
	v_fmac_f32_e32 v184, s25, v130
	v_fmac_f32_e32 v185, s25, v131
	s_waitcnt vmcnt(35)
	v_readlane_b32 s25, v247, 15
	v_cvt_f32_ubyte0_e32 v132, v54
	v_cvt_f32_ubyte1_e32 v133, v54
	v_cvt_f32_ubyte2_e32 v134, v54
	v_cvt_f32_ubyte3_e32 v135, v54
	v_cvt_f32_ubyte0_e32 v136, v55
	v_cvt_f32_ubyte1_e32 v137, v55
	v_cvt_f32_ubyte2_e32 v138, v55
	v_cvt_f32_ubyte3_e32 v139, v55
	v_readlane_b32 s30, v121, 47
	s_lshl_b32 s30, s30, 12
	s_add_u32 s28, s26, s30
	s_addc_u32 s29, s27, 0
	global_load_dwordx2 v[54:55], v162, s[28:29]
	v_fmac_f32_e32 v178, s25, v132
	v_fmac_f32_e32 v179, s25, v133
	v_fmac_f32_e32 v180, s25, v134
	v_fmac_f32_e32 v181, s25, v135
	v_fmac_f32_e32 v182, s25, v136
	v_fmac_f32_e32 v183, s25, v137
	v_fmac_f32_e32 v184, s25, v138
	v_fmac_f32_e32 v185, s25, v139
	s_waitcnt vmcnt(35)
	v_readlane_b32 s25, v247, 16
	v_cvt_f32_ubyte0_e32 v124, v56
	v_cvt_f32_ubyte1_e32 v125, v56
	v_cvt_f32_ubyte2_e32 v126, v56
	v_cvt_f32_ubyte3_e32 v127, v56
	v_cvt_f32_ubyte0_e32 v128, v57
	v_cvt_f32_ubyte1_e32 v129, v57
	v_cvt_f32_ubyte2_e32 v130, v57
	v_cvt_f32_ubyte3_e32 v131, v57
	v_readlane_b32 s30, v121, 48
	s_lshl_b32 s30, s30, 12
	s_add_u32 s28, s26, s30
	s_addc_u32 s29, s27, 0
	global_load_dwordx2 v[56:57], v162, s[28:29]
	v_fmac_f32_e32 v178, s25, v124
	v_fmac_f32_e32 v179, s25, v125
	v_fmac_f32_e32 v180, s25, v126
	v_fmac_f32_e32 v181, s25, v127
	v_fmac_f32_e32 v182, s25, v128
	v_fmac_f32_e32 v183, s25, v129
	v_fmac_f32_e32 v184, s25, v130
	v_fmac_f32_e32 v185, s25, v131
	s_waitcnt vmcnt(35)
	v_readlane_b32 s25, v247, 17
	v_cvt_f32_ubyte0_e32 v132, v58
	v_cvt_f32_ubyte1_e32 v133, v58
	v_cvt_f32_ubyte2_e32 v134, v58
	v_cvt_f32_ubyte3_e32 v135, v58
	v_cvt_f32_ubyte0_e32 v136, v59
	v_cvt_f32_ubyte1_e32 v137, v59
	v_cvt_f32_ubyte2_e32 v138, v59
	v_cvt_f32_ubyte3_e32 v139, v59
	v_readlane_b32 s30, v121, 49
	s_lshl_b32 s30, s30, 12
	s_add_u32 s28, s26, s30
	s_addc_u32 s29, s27, 0
	global_load_dwordx2 v[58:59], v162, s[28:29]
	v_fmac_f32_e32 v178, s25, v132
	v_fmac_f32_e32 v179, s25, v133
	v_fmac_f32_e32 v180, s25, v134
	v_fmac_f32_e32 v181, s25, v135
	v_fmac_f32_e32 v182, s25, v136
	v_fmac_f32_e32 v183, s25, v137
	v_fmac_f32_e32 v184, s25, v138
	v_fmac_f32_e32 v185, s25, v139
	s_waitcnt vmcnt(35)
	v_readlane_b32 s25, v247, 18
	v_cvt_f32_ubyte0_e32 v124, v60
	v_cvt_f32_ubyte1_e32 v125, v60
	v_cvt_f32_ubyte2_e32 v126, v60
	v_cvt_f32_ubyte3_e32 v127, v60
	v_cvt_f32_ubyte0_e32 v128, v61
	v_cvt_f32_ubyte1_e32 v129, v61
	v_cvt_f32_ubyte2_e32 v130, v61
	v_cvt_f32_ubyte3_e32 v131, v61
	v_readlane_b32 s30, v121, 50
	s_lshl_b32 s30, s30, 12
	s_add_u32 s28, s26, s30
	s_addc_u32 s29, s27, 0
	global_load_dwordx2 v[60:61], v162, s[28:29]
	v_fmac_f32_e32 v178, s25, v124
	v_fmac_f32_e32 v179, s25, v125
	v_fmac_f32_e32 v180, s25, v126
	v_fmac_f32_e32 v181, s25, v127
	v_fmac_f32_e32 v182, s25, v128
	v_fmac_f32_e32 v183, s25, v129
	v_fmac_f32_e32 v184, s25, v130
	v_fmac_f32_e32 v185, s25, v131
	s_waitcnt vmcnt(35)
	v_readlane_b32 s25, v247, 19
	v_cvt_f32_ubyte0_e32 v132, v62
	v_cvt_f32_ubyte1_e32 v133, v62
	v_cvt_f32_ubyte2_e32 v134, v62
	v_cvt_f32_ubyte3_e32 v135, v62
	v_cvt_f32_ubyte0_e32 v136, v63
	v_cvt_f32_ubyte1_e32 v137, v63
	v_cvt_f32_ubyte2_e32 v138, v63
	v_cvt_f32_ubyte3_e32 v139, v63
	v_readlane_b32 s30, v121, 51
	s_lshl_b32 s30, s30, 12
	s_add_u32 s28, s26, s30
	s_addc_u32 s29, s27, 0
	global_load_dwordx2 v[62:63], v162, s[28:29]
	v_fmac_f32_e32 v178, s25, v132
	v_fmac_f32_e32 v179, s25, v133
	v_fmac_f32_e32 v180, s25, v134
	v_fmac_f32_e32 v181, s25, v135
	v_fmac_f32_e32 v182, s25, v136
	v_fmac_f32_e32 v183, s25, v137
	v_fmac_f32_e32 v184, s25, v138
	v_fmac_f32_e32 v185, s25, v139
	s_waitcnt vmcnt(35)
	v_readlane_b32 s25, v247, 20
	v_cvt_f32_ubyte0_e32 v124, v64
	v_cvt_f32_ubyte1_e32 v125, v64
	v_cvt_f32_ubyte2_e32 v126, v64
	v_cvt_f32_ubyte3_e32 v127, v64
	v_cvt_f32_ubyte0_e32 v128, v65
	v_cvt_f32_ubyte1_e32 v129, v65
	v_cvt_f32_ubyte2_e32 v130, v65
	v_cvt_f32_ubyte3_e32 v131, v65
	v_readlane_b32 s30, v121, 52
	s_lshl_b32 s30, s30, 12
	s_add_u32 s28, s26, s30
	s_addc_u32 s29, s27, 0
	global_load_dwordx2 v[64:65], v162, s[28:29]
	v_fmac_f32_e32 v178, s25, v124
	v_fmac_f32_e32 v179, s25, v125
	v_fmac_f32_e32 v180, s25, v126
	v_fmac_f32_e32 v181, s25, v127
	v_fmac_f32_e32 v182, s25, v128
	v_fmac_f32_e32 v183, s25, v129
	v_fmac_f32_e32 v184, s25, v130
	v_fmac_f32_e32 v185, s25, v131
	s_waitcnt vmcnt(35)
	v_readlane_b32 s25, v247, 21
	v_cvt_f32_ubyte0_e32 v132, v66
	v_cvt_f32_ubyte1_e32 v133, v66
	v_cvt_f32_ubyte2_e32 v134, v66
	v_cvt_f32_ubyte3_e32 v135, v66
	v_cvt_f32_ubyte0_e32 v136, v67
	v_cvt_f32_ubyte1_e32 v137, v67
	v_cvt_f32_ubyte2_e32 v138, v67
	v_cvt_f32_ubyte3_e32 v139, v67
	v_readlane_b32 s30, v121, 53
	s_lshl_b32 s30, s30, 12
	s_add_u32 s28, s26, s30
	s_addc_u32 s29, s27, 0
	global_load_dwordx2 v[66:67], v162, s[28:29]
	v_fmac_f32_e32 v178, s25, v132
	v_fmac_f32_e32 v179, s25, v133
	v_fmac_f32_e32 v180, s25, v134
	v_fmac_f32_e32 v181, s25, v135
	v_fmac_f32_e32 v182, s25, v136
	v_fmac_f32_e32 v183, s25, v137
	v_fmac_f32_e32 v184, s25, v138
	v_fmac_f32_e32 v185, s25, v139
	s_waitcnt vmcnt(35)
	v_readlane_b32 s25, v247, 22
	v_cvt_f32_ubyte0_e32 v124, v68
	v_cvt_f32_ubyte1_e32 v125, v68
	v_cvt_f32_ubyte2_e32 v126, v68
	v_cvt_f32_ubyte3_e32 v127, v68
	v_cvt_f32_ubyte0_e32 v128, v69
	v_cvt_f32_ubyte1_e32 v129, v69
	v_cvt_f32_ubyte2_e32 v130, v69
	v_cvt_f32_ubyte3_e32 v131, v69
	v_readlane_b32 s30, v121, 54
	s_lshl_b32 s30, s30, 12
	s_add_u32 s28, s26, s30
	s_addc_u32 s29, s27, 0
	global_load_dwordx2 v[68:69], v162, s[28:29]
	v_fmac_f32_e32 v178, s25, v124
	v_fmac_f32_e32 v179, s25, v125
	v_fmac_f32_e32 v180, s25, v126
	v_fmac_f32_e32 v181, s25, v127
	v_fmac_f32_e32 v182, s25, v128
	v_fmac_f32_e32 v183, s25, v129
	v_fmac_f32_e32 v184, s25, v130
	v_fmac_f32_e32 v185, s25, v131
	s_waitcnt vmcnt(35)
	v_readlane_b32 s25, v247, 23
	v_cvt_f32_ubyte0_e32 v132, v70
	v_cvt_f32_ubyte1_e32 v133, v70
	v_cvt_f32_ubyte2_e32 v134, v70
	v_cvt_f32_ubyte3_e32 v135, v70
	v_cvt_f32_ubyte0_e32 v136, v71
	v_cvt_f32_ubyte1_e32 v137, v71
	v_cvt_f32_ubyte2_e32 v138, v71
	v_cvt_f32_ubyte3_e32 v139, v71
	v_readlane_b32 s30, v121, 55
	s_lshl_b32 s30, s30, 12
	s_add_u32 s28, s26, s30
	s_addc_u32 s29, s27, 0
	global_load_dwordx2 v[70:71], v162, s[28:29]
	v_fmac_f32_e32 v178, s25, v132
	v_fmac_f32_e32 v179, s25, v133
	v_fmac_f32_e32 v180, s25, v134
	v_fmac_f32_e32 v181, s25, v135
	v_fmac_f32_e32 v182, s25, v136
	v_fmac_f32_e32 v183, s25, v137
	v_fmac_f32_e32 v184, s25, v138
	v_fmac_f32_e32 v185, s25, v139
	s_waitcnt vmcnt(35)
	v_readlane_b32 s25, v247, 24
	v_cvt_f32_ubyte0_e32 v124, v72
	v_cvt_f32_ubyte1_e32 v125, v72
	v_cvt_f32_ubyte2_e32 v126, v72
	v_cvt_f32_ubyte3_e32 v127, v72
	v_cvt_f32_ubyte0_e32 v128, v73
	v_cvt_f32_ubyte1_e32 v129, v73
	v_cvt_f32_ubyte2_e32 v130, v73
	v_cvt_f32_ubyte3_e32 v131, v73
	v_readlane_b32 s30, v121, 56
	s_lshl_b32 s30, s30, 12
	s_add_u32 s28, s26, s30
	s_addc_u32 s29, s27, 0
	global_load_dwordx2 v[72:73], v162, s[28:29]
	v_fmac_f32_e32 v178, s25, v124
	v_fmac_f32_e32 v179, s25, v125
	v_fmac_f32_e32 v180, s25, v126
	v_fmac_f32_e32 v181, s25, v127
	v_fmac_f32_e32 v182, s25, v128
	v_fmac_f32_e32 v183, s25, v129
	v_fmac_f32_e32 v184, s25, v130
	v_fmac_f32_e32 v185, s25, v131
	s_waitcnt vmcnt(35)
	v_readlane_b32 s25, v247, 25
	v_cvt_f32_ubyte0_e32 v132, v74
	v_cvt_f32_ubyte1_e32 v133, v74
	v_cvt_f32_ubyte2_e32 v134, v74
	v_cvt_f32_ubyte3_e32 v135, v74
	v_cvt_f32_ubyte0_e32 v136, v75
	v_cvt_f32_ubyte1_e32 v137, v75
	v_cvt_f32_ubyte2_e32 v138, v75
	v_cvt_f32_ubyte3_e32 v139, v75
	v_readlane_b32 s30, v121, 57
	s_lshl_b32 s30, s30, 12
	s_add_u32 s28, s26, s30
	s_addc_u32 s29, s27, 0
	global_load_dwordx2 v[74:75], v162, s[28:29]
	v_fmac_f32_e32 v178, s25, v132
	v_fmac_f32_e32 v179, s25, v133
	v_fmac_f32_e32 v180, s25, v134
	v_fmac_f32_e32 v181, s25, v135
	v_fmac_f32_e32 v182, s25, v136
	v_fmac_f32_e32 v183, s25, v137
	v_fmac_f32_e32 v184, s25, v138
	v_fmac_f32_e32 v185, s25, v139
	s_waitcnt vmcnt(35)
	v_readlane_b32 s25, v247, 26
	v_cvt_f32_ubyte0_e32 v124, v76
	v_cvt_f32_ubyte1_e32 v125, v76
	v_cvt_f32_ubyte2_e32 v126, v76
	v_cvt_f32_ubyte3_e32 v127, v76
	v_cvt_f32_ubyte0_e32 v128, v77
	v_cvt_f32_ubyte1_e32 v129, v77
	v_cvt_f32_ubyte2_e32 v130, v77
	v_cvt_f32_ubyte3_e32 v131, v77
	v_readlane_b32 s30, v121, 58
	s_lshl_b32 s30, s30, 12
	s_add_u32 s28, s26, s30
	s_addc_u32 s29, s27, 0
	global_load_dwordx2 v[76:77], v162, s[28:29]
	v_fmac_f32_e32 v178, s25, v124
	v_fmac_f32_e32 v179, s25, v125
	v_fmac_f32_e32 v180, s25, v126
	v_fmac_f32_e32 v181, s25, v127
	v_fmac_f32_e32 v182, s25, v128
	v_fmac_f32_e32 v183, s25, v129
	v_fmac_f32_e32 v184, s25, v130
	v_fmac_f32_e32 v185, s25, v131
	s_waitcnt vmcnt(35)
	v_readlane_b32 s25, v247, 27
	v_cvt_f32_ubyte0_e32 v132, v78
	v_cvt_f32_ubyte1_e32 v133, v78
	v_cvt_f32_ubyte2_e32 v134, v78
	v_cvt_f32_ubyte3_e32 v135, v78
	v_cvt_f32_ubyte0_e32 v136, v79
	v_cvt_f32_ubyte1_e32 v137, v79
	v_cvt_f32_ubyte2_e32 v138, v79
	v_cvt_f32_ubyte3_e32 v139, v79
	v_readlane_b32 s30, v121, 59
	s_lshl_b32 s30, s30, 12
	s_add_u32 s28, s26, s30
	s_addc_u32 s29, s27, 0
	global_load_dwordx2 v[78:79], v162, s[28:29]
	v_fmac_f32_e32 v178, s25, v132
	v_fmac_f32_e32 v179, s25, v133
	v_fmac_f32_e32 v180, s25, v134
	v_fmac_f32_e32 v181, s25, v135
	v_fmac_f32_e32 v182, s25, v136
	v_fmac_f32_e32 v183, s25, v137
	v_fmac_f32_e32 v184, s25, v138
	v_fmac_f32_e32 v185, s25, v139
	s_waitcnt vmcnt(35)
	v_readlane_b32 s25, v247, 28
	v_cvt_f32_ubyte0_e32 v124, v80
	v_cvt_f32_ubyte1_e32 v125, v80
	v_cvt_f32_ubyte2_e32 v126, v80
	v_cvt_f32_ubyte3_e32 v127, v80
	v_cvt_f32_ubyte0_e32 v128, v81
	v_cvt_f32_ubyte1_e32 v129, v81
	v_cvt_f32_ubyte2_e32 v130, v81
	v_cvt_f32_ubyte3_e32 v131, v81
	v_readlane_b32 s30, v121, 60
	s_lshl_b32 s30, s30, 12
	s_add_u32 s28, s26, s30
	s_addc_u32 s29, s27, 0
	global_load_dwordx2 v[80:81], v162, s[28:29]
	v_fmac_f32_e32 v178, s25, v124
	v_fmac_f32_e32 v179, s25, v125
	v_fmac_f32_e32 v180, s25, v126
	v_fmac_f32_e32 v181, s25, v127
	v_fmac_f32_e32 v182, s25, v128
	v_fmac_f32_e32 v183, s25, v129
	v_fmac_f32_e32 v184, s25, v130
	v_fmac_f32_e32 v185, s25, v131
	s_waitcnt vmcnt(35)
	v_readlane_b32 s25, v247, 29
	v_cvt_f32_ubyte0_e32 v132, v82
	v_cvt_f32_ubyte1_e32 v133, v82
	v_cvt_f32_ubyte2_e32 v134, v82
	v_cvt_f32_ubyte3_e32 v135, v82
	v_cvt_f32_ubyte0_e32 v136, v83
	v_cvt_f32_ubyte1_e32 v137, v83
	v_cvt_f32_ubyte2_e32 v138, v83
	v_cvt_f32_ubyte3_e32 v139, v83
	v_readlane_b32 s30, v121, 61
	s_lshl_b32 s30, s30, 12
	s_add_u32 s28, s26, s30
	s_addc_u32 s29, s27, 0
	global_load_dwordx2 v[82:83], v162, s[28:29]
	v_fmac_f32_e32 v178, s25, v132
	v_fmac_f32_e32 v179, s25, v133
	v_fmac_f32_e32 v180, s25, v134
	v_fmac_f32_e32 v181, s25, v135
	v_fmac_f32_e32 v182, s25, v136
	v_fmac_f32_e32 v183, s25, v137
	v_fmac_f32_e32 v184, s25, v138
	v_fmac_f32_e32 v185, s25, v139
	s_waitcnt vmcnt(35)
	v_readlane_b32 s25, v247, 30
	v_cvt_f32_ubyte0_e32 v124, v84
	v_cvt_f32_ubyte1_e32 v125, v84
	v_cvt_f32_ubyte2_e32 v126, v84
	v_cvt_f32_ubyte3_e32 v127, v84
	v_cvt_f32_ubyte0_e32 v128, v85
	v_cvt_f32_ubyte1_e32 v129, v85
	v_cvt_f32_ubyte2_e32 v130, v85
	v_cvt_f32_ubyte3_e32 v131, v85
	v_readlane_b32 s30, v121, 62
	s_lshl_b32 s30, s30, 12
	s_add_u32 s28, s26, s30
	s_addc_u32 s29, s27, 0
	global_load_dwordx2 v[84:85], v162, s[28:29]
	v_fmac_f32_e32 v178, s25, v124
	v_fmac_f32_e32 v179, s25, v125
	v_fmac_f32_e32 v180, s25, v126
	v_fmac_f32_e32 v181, s25, v127
	v_fmac_f32_e32 v182, s25, v128
	v_fmac_f32_e32 v183, s25, v129
	v_fmac_f32_e32 v184, s25, v130
	v_fmac_f32_e32 v185, s25, v131
	s_waitcnt vmcnt(35)
	v_readlane_b32 s25, v247, 31
	v_cvt_f32_ubyte0_e32 v132, v86
	v_cvt_f32_ubyte1_e32 v133, v86
	v_cvt_f32_ubyte2_e32 v134, v86
	v_cvt_f32_ubyte3_e32 v135, v86
	v_cvt_f32_ubyte0_e32 v136, v87
	v_cvt_f32_ubyte1_e32 v137, v87
	v_cvt_f32_ubyte2_e32 v138, v87
	v_cvt_f32_ubyte3_e32 v139, v87
	v_readlane_b32 s30, v121, 63
	s_lshl_b32 s30, s30, 12
	s_add_u32 s28, s26, s30
	s_addc_u32 s29, s27, 0
	global_load_dwordx2 v[86:87], v162, s[28:29]
	v_fmac_f32_e32 v178, s25, v132
	v_fmac_f32_e32 v179, s25, v133
	v_fmac_f32_e32 v180, s25, v134
	v_fmac_f32_e32 v181, s25, v135
	v_fmac_f32_e32 v182, s25, v136
	v_fmac_f32_e32 v183, s25, v137
	v_fmac_f32_e32 v184, s25, v138
	v_fmac_f32_e32 v185, s25, v139
	s_waitcnt vmcnt(35)
	v_readlane_b32 s25, v247, 32
	v_cvt_f32_ubyte0_e32 v124, v24
	v_cvt_f32_ubyte1_e32 v125, v24
	v_cvt_f32_ubyte2_e32 v126, v24
	v_cvt_f32_ubyte3_e32 v127, v24
	v_cvt_f32_ubyte0_e32 v128, v25
	v_cvt_f32_ubyte1_e32 v129, v25
	v_cvt_f32_ubyte2_e32 v130, v25
	v_cvt_f32_ubyte3_e32 v131, v25
	v_fmac_f32_e32 v178, s25, v124
	v_fmac_f32_e32 v179, s25, v125
	v_fmac_f32_e32 v180, s25, v126
	v_fmac_f32_e32 v181, s25, v127
	v_fmac_f32_e32 v182, s25, v128
	v_fmac_f32_e32 v183, s25, v129
	v_fmac_f32_e32 v184, s25, v130
	v_fmac_f32_e32 v185, s25, v131
	s_waitcnt vmcnt(30)
	v_readlane_b32 s25, v247, 33
	v_cvt_f32_ubyte0_e32 v132, v26
	v_cvt_f32_ubyte1_e32 v133, v26
	v_cvt_f32_ubyte2_e32 v134, v26
	v_cvt_f32_ubyte3_e32 v135, v26
	v_cvt_f32_ubyte0_e32 v136, v27
	v_cvt_f32_ubyte1_e32 v137, v27
	v_cvt_f32_ubyte2_e32 v138, v27
	v_cvt_f32_ubyte3_e32 v139, v27
	v_fmac_f32_e32 v178, s25, v132
	v_fmac_f32_e32 v179, s25, v133
	v_fmac_f32_e32 v180, s25, v134
	v_fmac_f32_e32 v181, s25, v135
	v_fmac_f32_e32 v182, s25, v136
	v_fmac_f32_e32 v183, s25, v137
	v_fmac_f32_e32 v184, s25, v138
	v_fmac_f32_e32 v185, s25, v139
	s_waitcnt vmcnt(29)
	v_readlane_b32 s25, v247, 34
	v_cvt_f32_ubyte0_e32 v124, v28
	v_cvt_f32_ubyte1_e32 v125, v28
	v_cvt_f32_ubyte2_e32 v126, v28
	v_cvt_f32_ubyte3_e32 v127, v28
	v_cvt_f32_ubyte0_e32 v128, v29
	v_cvt_f32_ubyte1_e32 v129, v29
	v_cvt_f32_ubyte2_e32 v130, v29
	v_cvt_f32_ubyte3_e32 v131, v29
	v_fmac_f32_e32 v178, s25, v124
	v_fmac_f32_e32 v179, s25, v125
	v_fmac_f32_e32 v180, s25, v126
	v_fmac_f32_e32 v181, s25, v127
	v_fmac_f32_e32 v182, s25, v128
	v_fmac_f32_e32 v183, s25, v129
	v_fmac_f32_e32 v184, s25, v130
	v_fmac_f32_e32 v185, s25, v131
	s_waitcnt vmcnt(28)
	v_readlane_b32 s25, v247, 35
	v_cvt_f32_ubyte0_e32 v132, v30
	v_cvt_f32_ubyte1_e32 v133, v30
	v_cvt_f32_ubyte2_e32 v134, v30
	v_cvt_f32_ubyte3_e32 v135, v30
	v_cvt_f32_ubyte0_e32 v136, v31
	v_cvt_f32_ubyte1_e32 v137, v31
	v_cvt_f32_ubyte2_e32 v138, v31
	v_cvt_f32_ubyte3_e32 v139, v31
	v_fmac_f32_e32 v178, s25, v132
	v_fmac_f32_e32 v179, s25, v133
	v_fmac_f32_e32 v180, s25, v134
	v_fmac_f32_e32 v181, s25, v135
	v_fmac_f32_e32 v182, s25, v136
	v_fmac_f32_e32 v183, s25, v137
	v_fmac_f32_e32 v184, s25, v138
	v_fmac_f32_e32 v185, s25, v139
	s_waitcnt vmcnt(27)
	v_readlane_b32 s25, v247, 36
	v_cvt_f32_ubyte0_e32 v124, v32
	v_cvt_f32_ubyte1_e32 v125, v32
	v_cvt_f32_ubyte2_e32 v126, v32
	v_cvt_f32_ubyte3_e32 v127, v32
	v_cvt_f32_ubyte0_e32 v128, v33
	v_cvt_f32_ubyte1_e32 v129, v33
	v_cvt_f32_ubyte2_e32 v130, v33
	v_cvt_f32_ubyte3_e32 v131, v33
	v_fmac_f32_e32 v178, s25, v124
	v_fmac_f32_e32 v179, s25, v125
	v_fmac_f32_e32 v180, s25, v126
	v_fmac_f32_e32 v181, s25, v127
	v_fmac_f32_e32 v182, s25, v128
	v_fmac_f32_e32 v183, s25, v129
	v_fmac_f32_e32 v184, s25, v130
	v_fmac_f32_e32 v185, s25, v131
	s_waitcnt vmcnt(26)
	v_readlane_b32 s25, v247, 37
	v_cvt_f32_ubyte0_e32 v132, v34
	v_cvt_f32_ubyte1_e32 v133, v34
	v_cvt_f32_ubyte2_e32 v134, v34
	v_cvt_f32_ubyte3_e32 v135, v34
	v_cvt_f32_ubyte0_e32 v136, v35
	v_cvt_f32_ubyte1_e32 v137, v35
	v_cvt_f32_ubyte2_e32 v138, v35
	v_cvt_f32_ubyte3_e32 v139, v35
	v_fmac_f32_e32 v178, s25, v132
	v_fmac_f32_e32 v179, s25, v133
	v_fmac_f32_e32 v180, s25, v134
	v_fmac_f32_e32 v181, s25, v135
	v_fmac_f32_e32 v182, s25, v136
	v_fmac_f32_e32 v183, s25, v137
	v_fmac_f32_e32 v184, s25, v138
	v_fmac_f32_e32 v185, s25, v139
	s_waitcnt vmcnt(25)
	v_readlane_b32 s25, v247, 38
	v_cvt_f32_ubyte0_e32 v124, v36
	v_cvt_f32_ubyte1_e32 v125, v36
	v_cvt_f32_ubyte2_e32 v126, v36
	v_cvt_f32_ubyte3_e32 v127, v36
	v_cvt_f32_ubyte0_e32 v128, v37
	v_cvt_f32_ubyte1_e32 v129, v37
	v_cvt_f32_ubyte2_e32 v130, v37
	v_cvt_f32_ubyte3_e32 v131, v37
	v_fmac_f32_e32 v178, s25, v124
	v_fmac_f32_e32 v179, s25, v125
	v_fmac_f32_e32 v180, s25, v126
	v_fmac_f32_e32 v181, s25, v127
	v_fmac_f32_e32 v182, s25, v128
	v_fmac_f32_e32 v183, s25, v129
	v_fmac_f32_e32 v184, s25, v130
	v_fmac_f32_e32 v185, s25, v131
	s_waitcnt vmcnt(24)
	v_readlane_b32 s25, v247, 39
	v_cvt_f32_ubyte0_e32 v132, v38
	v_cvt_f32_ubyte1_e32 v133, v38
	v_cvt_f32_ubyte2_e32 v134, v38
	v_cvt_f32_ubyte3_e32 v135, v38
	v_cvt_f32_ubyte0_e32 v136, v39
	v_cvt_f32_ubyte1_e32 v137, v39
	v_cvt_f32_ubyte2_e32 v138, v39
	v_cvt_f32_ubyte3_e32 v139, v39
	v_fmac_f32_e32 v178, s25, v132
	v_fmac_f32_e32 v179, s25, v133
	v_fmac_f32_e32 v180, s25, v134
	v_fmac_f32_e32 v181, s25, v135
	v_fmac_f32_e32 v182, s25, v136
	v_fmac_f32_e32 v183, s25, v137
	v_fmac_f32_e32 v184, s25, v138
	v_fmac_f32_e32 v185, s25, v139
	s_waitcnt vmcnt(23)
	v_readlane_b32 s25, v247, 40
	v_cvt_f32_ubyte0_e32 v124, v40
	v_cvt_f32_ubyte1_e32 v125, v40
	v_cvt_f32_ubyte2_e32 v126, v40
	v_cvt_f32_ubyte3_e32 v127, v40
	v_cvt_f32_ubyte0_e32 v128, v41
	v_cvt_f32_ubyte1_e32 v129, v41
	v_cvt_f32_ubyte2_e32 v130, v41
	v_cvt_f32_ubyte3_e32 v131, v41
	v_fmac_f32_e32 v178, s25, v124
	v_fmac_f32_e32 v179, s25, v125
	v_fmac_f32_e32 v180, s25, v126
	v_fmac_f32_e32 v181, s25, v127
	v_fmac_f32_e32 v182, s25, v128
	v_fmac_f32_e32 v183, s25, v129
	v_fmac_f32_e32 v184, s25, v130
	v_fmac_f32_e32 v185, s25, v131
	s_waitcnt vmcnt(22)
	v_readlane_b32 s25, v247, 41
	v_cvt_f32_ubyte0_e32 v132, v42
	v_cvt_f32_ubyte1_e32 v133, v42
	v_cvt_f32_ubyte2_e32 v134, v42
	v_cvt_f32_ubyte3_e32 v135, v42
	v_cvt_f32_ubyte0_e32 v136, v43
	v_cvt_f32_ubyte1_e32 v137, v43
	v_cvt_f32_ubyte2_e32 v138, v43
	v_cvt_f32_ubyte3_e32 v139, v43
	v_fmac_f32_e32 v178, s25, v132
	v_fmac_f32_e32 v179, s25, v133
	v_fmac_f32_e32 v180, s25, v134
	v_fmac_f32_e32 v181, s25, v135
	v_fmac_f32_e32 v182, s25, v136
	v_fmac_f32_e32 v183, s25, v137
	v_fmac_f32_e32 v184, s25, v138
	v_fmac_f32_e32 v185, s25, v139
	s_waitcnt vmcnt(21)
	v_readlane_b32 s25, v247, 42
	v_cvt_f32_ubyte0_e32 v124, v44
	v_cvt_f32_ubyte1_e32 v125, v44
	v_cvt_f32_ubyte2_e32 v126, v44
	v_cvt_f32_ubyte3_e32 v127, v44
	v_cvt_f32_ubyte0_e32 v128, v45
	v_cvt_f32_ubyte1_e32 v129, v45
	v_cvt_f32_ubyte2_e32 v130, v45
	v_cvt_f32_ubyte3_e32 v131, v45
	v_fmac_f32_e32 v178, s25, v124
	v_fmac_f32_e32 v179, s25, v125
	v_fmac_f32_e32 v180, s25, v126
	v_fmac_f32_e32 v181, s25, v127
	v_fmac_f32_e32 v182, s25, v128
	v_fmac_f32_e32 v183, s25, v129
	v_fmac_f32_e32 v184, s25, v130
	v_fmac_f32_e32 v185, s25, v131
	s_waitcnt vmcnt(20)
	v_readlane_b32 s25, v247, 43
	v_cvt_f32_ubyte0_e32 v132, v46
	v_cvt_f32_ubyte1_e32 v133, v46
	v_cvt_f32_ubyte2_e32 v134, v46
	v_cvt_f32_ubyte3_e32 v135, v46
	v_cvt_f32_ubyte0_e32 v136, v47
	v_cvt_f32_ubyte1_e32 v137, v47
	v_cvt_f32_ubyte2_e32 v138, v47
	v_cvt_f32_ubyte3_e32 v139, v47
	v_fmac_f32_e32 v178, s25, v132
	v_fmac_f32_e32 v179, s25, v133
	v_fmac_f32_e32 v180, s25, v134
	v_fmac_f32_e32 v181, s25, v135
	v_fmac_f32_e32 v182, s25, v136
	v_fmac_f32_e32 v183, s25, v137
	v_fmac_f32_e32 v184, s25, v138
	v_fmac_f32_e32 v185, s25, v139
	s_waitcnt vmcnt(19)
	v_readlane_b32 s25, v247, 44
	v_cvt_f32_ubyte0_e32 v124, v48
	v_cvt_f32_ubyte1_e32 v125, v48
	v_cvt_f32_ubyte2_e32 v126, v48
	v_cvt_f32_ubyte3_e32 v127, v48
	v_cvt_f32_ubyte0_e32 v128, v49
	v_cvt_f32_ubyte1_e32 v129, v49
	v_cvt_f32_ubyte2_e32 v130, v49
	v_cvt_f32_ubyte3_e32 v131, v49
	v_fmac_f32_e32 v178, s25, v124
	v_fmac_f32_e32 v179, s25, v125
	v_fmac_f32_e32 v180, s25, v126
	v_fmac_f32_e32 v181, s25, v127
	v_fmac_f32_e32 v182, s25, v128
	v_fmac_f32_e32 v183, s25, v129
	v_fmac_f32_e32 v184, s25, v130
	v_fmac_f32_e32 v185, s25, v131
	s_waitcnt vmcnt(18)
	v_readlane_b32 s25, v247, 45
	v_cvt_f32_ubyte0_e32 v132, v50
	v_cvt_f32_ubyte1_e32 v133, v50
	v_cvt_f32_ubyte2_e32 v134, v50
	v_cvt_f32_ubyte3_e32 v135, v50
	v_cvt_f32_ubyte0_e32 v136, v51
	v_cvt_f32_ubyte1_e32 v137, v51
	v_cvt_f32_ubyte2_e32 v138, v51
	v_cvt_f32_ubyte3_e32 v139, v51
	v_fmac_f32_e32 v178, s25, v132
	v_fmac_f32_e32 v179, s25, v133
	v_fmac_f32_e32 v180, s25, v134
	v_fmac_f32_e32 v181, s25, v135
	v_fmac_f32_e32 v182, s25, v136
	v_fmac_f32_e32 v183, s25, v137
	v_fmac_f32_e32 v184, s25, v138
	v_fmac_f32_e32 v185, s25, v139
	s_waitcnt vmcnt(17)
	v_readlane_b32 s25, v247, 46
	v_cvt_f32_ubyte0_e32 v124, v52
	v_cvt_f32_ubyte1_e32 v125, v52
	v_cvt_f32_ubyte2_e32 v126, v52
	v_cvt_f32_ubyte3_e32 v127, v52
	v_cvt_f32_ubyte0_e32 v128, v53
	v_cvt_f32_ubyte1_e32 v129, v53
	v_cvt_f32_ubyte2_e32 v130, v53
	v_cvt_f32_ubyte3_e32 v131, v53
	v_fmac_f32_e32 v178, s25, v124
	v_fmac_f32_e32 v179, s25, v125
	v_fmac_f32_e32 v180, s25, v126
	v_fmac_f32_e32 v181, s25, v127
	v_fmac_f32_e32 v182, s25, v128
	v_fmac_f32_e32 v183, s25, v129
	v_fmac_f32_e32 v184, s25, v130
	v_fmac_f32_e32 v185, s25, v131
	s_waitcnt vmcnt(16)
	v_readlane_b32 s25, v247, 47
	v_cvt_f32_ubyte0_e32 v132, v54
	v_cvt_f32_ubyte1_e32 v133, v54
	v_cvt_f32_ubyte2_e32 v134, v54
	v_cvt_f32_ubyte3_e32 v135, v54
	v_cvt_f32_ubyte0_e32 v136, v55
	v_cvt_f32_ubyte1_e32 v137, v55
	v_cvt_f32_ubyte2_e32 v138, v55
	v_cvt_f32_ubyte3_e32 v139, v55
	v_fmac_f32_e32 v178, s25, v132
	v_fmac_f32_e32 v179, s25, v133
	v_fmac_f32_e32 v180, s25, v134
	v_fmac_f32_e32 v181, s25, v135
	v_fmac_f32_e32 v182, s25, v136
	v_fmac_f32_e32 v183, s25, v137
	v_fmac_f32_e32 v184, s25, v138
	v_fmac_f32_e32 v185, s25, v139
	s_waitcnt vmcnt(15)
	v_readlane_b32 s25, v247, 48
	v_cvt_f32_ubyte0_e32 v124, v56
	v_cvt_f32_ubyte1_e32 v125, v56
	v_cvt_f32_ubyte2_e32 v126, v56
	v_cvt_f32_ubyte3_e32 v127, v56
	v_cvt_f32_ubyte0_e32 v128, v57
	v_cvt_f32_ubyte1_e32 v129, v57
	v_cvt_f32_ubyte2_e32 v130, v57
	v_cvt_f32_ubyte3_e32 v131, v57
	v_fmac_f32_e32 v178, s25, v124
	v_fmac_f32_e32 v179, s25, v125
	v_fmac_f32_e32 v180, s25, v126
	v_fmac_f32_e32 v181, s25, v127
	v_fmac_f32_e32 v182, s25, v128
	v_fmac_f32_e32 v183, s25, v129
	v_fmac_f32_e32 v184, s25, v130
	v_fmac_f32_e32 v185, s25, v131
	s_waitcnt vmcnt(14)
	v_readlane_b32 s25, v247, 49
	v_cvt_f32_ubyte0_e32 v132, v58
	v_cvt_f32_ubyte1_e32 v133, v58
	v_cvt_f32_ubyte2_e32 v134, v58
	v_cvt_f32_ubyte3_e32 v135, v58
	v_cvt_f32_ubyte0_e32 v136, v59
	v_cvt_f32_ubyte1_e32 v137, v59
	v_cvt_f32_ubyte2_e32 v138, v59
	v_cvt_f32_ubyte3_e32 v139, v59
	v_fmac_f32_e32 v178, s25, v132
	v_fmac_f32_e32 v179, s25, v133
	v_fmac_f32_e32 v180, s25, v134
	v_fmac_f32_e32 v181, s25, v135
	v_fmac_f32_e32 v182, s25, v136
	v_fmac_f32_e32 v183, s25, v137
	v_fmac_f32_e32 v184, s25, v138
	v_fmac_f32_e32 v185, s25, v139
	s_waitcnt vmcnt(13)
	v_readlane_b32 s25, v247, 50
	v_cvt_f32_ubyte0_e32 v124, v60
	v_cvt_f32_ubyte1_e32 v125, v60
	v_cvt_f32_ubyte2_e32 v126, v60
	v_cvt_f32_ubyte3_e32 v127, v60
	v_cvt_f32_ubyte0_e32 v128, v61
	v_cvt_f32_ubyte1_e32 v129, v61
	v_cvt_f32_ubyte2_e32 v130, v61
	v_cvt_f32_ubyte3_e32 v131, v61
	v_fmac_f32_e32 v178, s25, v124
	v_fmac_f32_e32 v179, s25, v125
	v_fmac_f32_e32 v180, s25, v126
	v_fmac_f32_e32 v181, s25, v127
	v_fmac_f32_e32 v182, s25, v128
	v_fmac_f32_e32 v183, s25, v129
	v_fmac_f32_e32 v184, s25, v130
	v_fmac_f32_e32 v185, s25, v131
	s_waitcnt vmcnt(12)
	v_readlane_b32 s25, v247, 51
	v_cvt_f32_ubyte0_e32 v132, v62
	v_cvt_f32_ubyte1_e32 v133, v62
	v_cvt_f32_ubyte2_e32 v134, v62
	v_cvt_f32_ubyte3_e32 v135, v62
	v_cvt_f32_ubyte0_e32 v136, v63
	v_cvt_f32_ubyte1_e32 v137, v63
	v_cvt_f32_ubyte2_e32 v138, v63
	v_cvt_f32_ubyte3_e32 v139, v63
	v_fmac_f32_e32 v178, s25, v132
	v_fmac_f32_e32 v179, s25, v133
	v_fmac_f32_e32 v180, s25, v134
	v_fmac_f32_e32 v181, s25, v135
	v_fmac_f32_e32 v182, s25, v136
	v_fmac_f32_e32 v183, s25, v137
	v_fmac_f32_e32 v184, s25, v138
	v_fmac_f32_e32 v185, s25, v139
	s_waitcnt vmcnt(11)
	v_readlane_b32 s25, v247, 52
	v_cvt_f32_ubyte0_e32 v124, v64
	v_cvt_f32_ubyte1_e32 v125, v64
	v_cvt_f32_ubyte2_e32 v126, v64
	v_cvt_f32_ubyte3_e32 v127, v64
	v_cvt_f32_ubyte0_e32 v128, v65
	v_cvt_f32_ubyte1_e32 v129, v65
	v_cvt_f32_ubyte2_e32 v130, v65
	v_cvt_f32_ubyte3_e32 v131, v65
	v_fmac_f32_e32 v178, s25, v124
	v_fmac_f32_e32 v179, s25, v125
	v_fmac_f32_e32 v180, s25, v126
	v_fmac_f32_e32 v181, s25, v127
	v_fmac_f32_e32 v182, s25, v128
	v_fmac_f32_e32 v183, s25, v129
	v_fmac_f32_e32 v184, s25, v130
	v_fmac_f32_e32 v185, s25, v131
	s_waitcnt vmcnt(10)
	v_readlane_b32 s25, v247, 53
	v_cvt_f32_ubyte0_e32 v132, v66
	v_cvt_f32_ubyte1_e32 v133, v66
	v_cvt_f32_ubyte2_e32 v134, v66
	v_cvt_f32_ubyte3_e32 v135, v66
	v_cvt_f32_ubyte0_e32 v136, v67
	v_cvt_f32_ubyte1_e32 v137, v67
	v_cvt_f32_ubyte2_e32 v138, v67
	v_cvt_f32_ubyte3_e32 v139, v67
	v_fmac_f32_e32 v178, s25, v132
	v_fmac_f32_e32 v179, s25, v133
	v_fmac_f32_e32 v180, s25, v134
	v_fmac_f32_e32 v181, s25, v135
	v_fmac_f32_e32 v182, s25, v136
	v_fmac_f32_e32 v183, s25, v137
	v_fmac_f32_e32 v184, s25, v138
	v_fmac_f32_e32 v185, s25, v139
	s_waitcnt vmcnt(9)
	v_readlane_b32 s25, v247, 54
	v_cvt_f32_ubyte0_e32 v124, v68
	v_cvt_f32_ubyte1_e32 v125, v68
	v_cvt_f32_ubyte2_e32 v126, v68
	v_cvt_f32_ubyte3_e32 v127, v68
	v_cvt_f32_ubyte0_e32 v128, v69
	v_cvt_f32_ubyte1_e32 v129, v69
	v_cvt_f32_ubyte2_e32 v130, v69
	v_cvt_f32_ubyte3_e32 v131, v69
	v_fmac_f32_e32 v178, s25, v124
	v_fmac_f32_e32 v179, s25, v125
	v_fmac_f32_e32 v180, s25, v126
	v_fmac_f32_e32 v181, s25, v127
	v_fmac_f32_e32 v182, s25, v128
	v_fmac_f32_e32 v183, s25, v129
	v_fmac_f32_e32 v184, s25, v130
	v_fmac_f32_e32 v185, s25, v131
	s_waitcnt vmcnt(8)
	v_readlane_b32 s25, v247, 55
	v_cvt_f32_ubyte0_e32 v132, v70
	v_cvt_f32_ubyte1_e32 v133, v70
	v_cvt_f32_ubyte2_e32 v134, v70
	v_cvt_f32_ubyte3_e32 v135, v70
	v_cvt_f32_ubyte0_e32 v136, v71
	v_cvt_f32_ubyte1_e32 v137, v71
	v_cvt_f32_ubyte2_e32 v138, v71
	v_cvt_f32_ubyte3_e32 v139, v71
	v_fmac_f32_e32 v178, s25, v132
	v_fmac_f32_e32 v179, s25, v133
	v_fmac_f32_e32 v180, s25, v134
	v_fmac_f32_e32 v181, s25, v135
	v_fmac_f32_e32 v182, s25, v136
	v_fmac_f32_e32 v183, s25, v137
	v_fmac_f32_e32 v184, s25, v138
	v_fmac_f32_e32 v185, s25, v139
	s_waitcnt vmcnt(7)
	v_readlane_b32 s25, v247, 56
	v_cvt_f32_ubyte0_e32 v124, v72
	v_cvt_f32_ubyte1_e32 v125, v72
	v_cvt_f32_ubyte2_e32 v126, v72
	v_cvt_f32_ubyte3_e32 v127, v72
	v_cvt_f32_ubyte0_e32 v128, v73
	v_cvt_f32_ubyte1_e32 v129, v73
	v_cvt_f32_ubyte2_e32 v130, v73
	v_cvt_f32_ubyte3_e32 v131, v73
	v_fmac_f32_e32 v178, s25, v124
	v_fmac_f32_e32 v179, s25, v125
	v_fmac_f32_e32 v180, s25, v126
	v_fmac_f32_e32 v181, s25, v127
	v_fmac_f32_e32 v182, s25, v128
	v_fmac_f32_e32 v183, s25, v129
	v_fmac_f32_e32 v184, s25, v130
	v_fmac_f32_e32 v185, s25, v131
	s_waitcnt vmcnt(6)
	v_readlane_b32 s25, v247, 57
	v_cvt_f32_ubyte0_e32 v132, v74
	v_cvt_f32_ubyte1_e32 v133, v74
	v_cvt_f32_ubyte2_e32 v134, v74
	v_cvt_f32_ubyte3_e32 v135, v74
	v_cvt_f32_ubyte0_e32 v136, v75
	v_cvt_f32_ubyte1_e32 v137, v75
	v_cvt_f32_ubyte2_e32 v138, v75
	v_cvt_f32_ubyte3_e32 v139, v75
	v_fmac_f32_e32 v178, s25, v132
	v_fmac_f32_e32 v179, s25, v133
	v_fmac_f32_e32 v180, s25, v134
	v_fmac_f32_e32 v181, s25, v135
	v_fmac_f32_e32 v182, s25, v136
	v_fmac_f32_e32 v183, s25, v137
	v_fmac_f32_e32 v184, s25, v138
	v_fmac_f32_e32 v185, s25, v139
	s_waitcnt vmcnt(5)
	v_readlane_b32 s25, v247, 58
	v_cvt_f32_ubyte0_e32 v124, v76
	v_cvt_f32_ubyte1_e32 v125, v76
	v_cvt_f32_ubyte2_e32 v126, v76
	v_cvt_f32_ubyte3_e32 v127, v76
	v_cvt_f32_ubyte0_e32 v128, v77
	v_cvt_f32_ubyte1_e32 v129, v77
	v_cvt_f32_ubyte2_e32 v130, v77
	v_cvt_f32_ubyte3_e32 v131, v77
	v_fmac_f32_e32 v178, s25, v124
	v_fmac_f32_e32 v179, s25, v125
	v_fmac_f32_e32 v180, s25, v126
	v_fmac_f32_e32 v181, s25, v127
	v_fmac_f32_e32 v182, s25, v128
	v_fmac_f32_e32 v183, s25, v129
	v_fmac_f32_e32 v184, s25, v130
	v_fmac_f32_e32 v185, s25, v131
	s_waitcnt vmcnt(4)
	v_readlane_b32 s25, v247, 59
	v_cvt_f32_ubyte0_e32 v132, v78
	v_cvt_f32_ubyte1_e32 v133, v78
	v_cvt_f32_ubyte2_e32 v134, v78
	v_cvt_f32_ubyte3_e32 v135, v78
	v_cvt_f32_ubyte0_e32 v136, v79
	v_cvt_f32_ubyte1_e32 v137, v79
	v_cvt_f32_ubyte2_e32 v138, v79
	v_cvt_f32_ubyte3_e32 v139, v79
	v_fmac_f32_e32 v178, s25, v132
	v_fmac_f32_e32 v179, s25, v133
	v_fmac_f32_e32 v180, s25, v134
	v_fmac_f32_e32 v181, s25, v135
	v_fmac_f32_e32 v182, s25, v136
	v_fmac_f32_e32 v183, s25, v137
	v_fmac_f32_e32 v184, s25, v138
	v_fmac_f32_e32 v185, s25, v139
	s_waitcnt vmcnt(3)
	v_readlane_b32 s25, v247, 60
	v_cvt_f32_ubyte0_e32 v124, v80
	v_cvt_f32_ubyte1_e32 v125, v80
	v_cvt_f32_ubyte2_e32 v126, v80
	v_cvt_f32_ubyte3_e32 v127, v80
	v_cvt_f32_ubyte0_e32 v128, v81
	v_cvt_f32_ubyte1_e32 v129, v81
	v_cvt_f32_ubyte2_e32 v130, v81
	v_cvt_f32_ubyte3_e32 v131, v81
	v_fmac_f32_e32 v178, s25, v124
	v_fmac_f32_e32 v179, s25, v125
	v_fmac_f32_e32 v180, s25, v126
	v_fmac_f32_e32 v181, s25, v127
	v_fmac_f32_e32 v182, s25, v128
	v_fmac_f32_e32 v183, s25, v129
	v_fmac_f32_e32 v184, s25, v130
	v_fmac_f32_e32 v185, s25, v131
	s_waitcnt vmcnt(2)
	v_readlane_b32 s25, v247, 61
	v_cvt_f32_ubyte0_e32 v132, v82
	v_cvt_f32_ubyte1_e32 v133, v82
	v_cvt_f32_ubyte2_e32 v134, v82
	v_cvt_f32_ubyte3_e32 v135, v82
	v_cvt_f32_ubyte0_e32 v136, v83
	v_cvt_f32_ubyte1_e32 v137, v83
	v_cvt_f32_ubyte2_e32 v138, v83
	v_cvt_f32_ubyte3_e32 v139, v83
	v_fmac_f32_e32 v178, s25, v132
	v_fmac_f32_e32 v179, s25, v133
	v_fmac_f32_e32 v180, s25, v134
	v_fmac_f32_e32 v181, s25, v135
	v_fmac_f32_e32 v182, s25, v136
	v_fmac_f32_e32 v183, s25, v137
	v_fmac_f32_e32 v184, s25, v138
	v_fmac_f32_e32 v185, s25, v139
	s_waitcnt vmcnt(1)
	v_readlane_b32 s25, v247, 62
	v_cvt_f32_ubyte0_e32 v124, v84
	v_cvt_f32_ubyte1_e32 v125, v84
	v_cvt_f32_ubyte2_e32 v126, v84
	v_cvt_f32_ubyte3_e32 v127, v84
	v_cvt_f32_ubyte0_e32 v128, v85
	v_cvt_f32_ubyte1_e32 v129, v85
	v_cvt_f32_ubyte2_e32 v130, v85
	v_cvt_f32_ubyte3_e32 v131, v85
	v_fmac_f32_e32 v178, s25, v124
	v_fmac_f32_e32 v179, s25, v125
	v_fmac_f32_e32 v180, s25, v126
	v_fmac_f32_e32 v181, s25, v127
	v_fmac_f32_e32 v182, s25, v128
	v_fmac_f32_e32 v183, s25, v129
	v_fmac_f32_e32 v184, s25, v130
	v_fmac_f32_e32 v185, s25, v131
	s_waitcnt vmcnt(0)
	v_readlane_b32 s25, v247, 63
	v_cvt_f32_ubyte0_e32 v132, v86
	v_cvt_f32_ubyte1_e32 v133, v86
	v_cvt_f32_ubyte2_e32 v134, v86
	v_cvt_f32_ubyte3_e32 v135, v86
	v_cvt_f32_ubyte0_e32 v136, v87
	v_cvt_f32_ubyte1_e32 v137, v87
	v_cvt_f32_ubyte2_e32 v138, v87
	v_cvt_f32_ubyte3_e32 v139, v87
	v_fmac_f32_e32 v178, s25, v132
	v_fmac_f32_e32 v179, s25, v133
	v_fmac_f32_e32 v180, s25, v134
	v_fmac_f32_e32 v181, s25, v135
	v_fmac_f32_e32 v182, s25, v136
	v_fmac_f32_e32 v183, s25, v137
	v_fmac_f32_e32 v184, s25, v138
	v_fmac_f32_e32 v185, s25, v139
	v_lshlrev_b32_e32 v132, 16, v242
	v_and_b32_e32 v133, 0xffff0000, v242
	v_lshlrev_b32_e32 v134, 16, v243
	v_and_b32_e32 v135, 0xffff0000, v243
	v_lshlrev_b32_e32 v136, 16, v244
	v_and_b32_e32 v137, 0xffff0000, v244
	v_lshlrev_b32_e32 v138, 16, v245
	v_and_b32_e32 v139, 0xffff0000, v245
	v_add_f32_e32 v178, v178, v248
	v_add_f32_e32 v179, v179, v248
	v_add_f32_e32 v180, v180, v248
	v_add_f32_e32 v181, v181, v248
	v_add_f32_e32 v182, v182, v248
	v_add_f32_e32 v183, v183, v248
	v_add_f32_e32 v184, v184, v248
	v_add_f32_e32 v185, v185, v248
	v_add_f32_e32 v124, v132, v178
	v_add_f32_e32 v125, v133, v179
	v_add_f32_e32 v126, v134, v180
	v_add_f32_e32 v127, v135, v181
	v_add_f32_e32 v128, v136, v182
	v_add_f32_e32 v129, v137, v183
	v_add_f32_e32 v130, v138, v184
	v_add_f32_e32 v131, v139, v185
	v_mul_f32_e32 v16, v124, v124
	v_fmac_f32_e32 v16, v125, v125
	v_fmac_f32_e32 v16, v126, v126
	v_fmac_f32_e32 v16, v127, v127
	v_fmac_f32_e32 v16, v128, v128
	v_fmac_f32_e32 v16, v129, v129
	v_fmac_f32_e32 v16, v130, v130
	v_fmac_f32_e32 v16, v131, v131
	s_nop 1
	v_add_f32_dpp v17, v16, v16 quad_perm:[1,0,3,2] row_mask:0xf bank_mask:0xf
	s_nop 1
	v_add_f32_dpp v16, v17, v17 quad_perm:[2,3,0,1] row_mask:0xf bank_mask:0xf
	s_nop 1
	v_add_f32_dpp v17, v16, v16 row_half_mirror row_mask:0xf bank_mask:0xf
	s_nop 1
	v_add_f32_dpp v16, v17, v17 row_ror:8 row_mask:0xf bank_mask:0xf
	v_mov_b32_e32 v17, v16
	s_nop 1
	v_permlane16_swap_b32_e32 v16, v17
	v_add_f32_e32 v16, v16, v17
	v_mov_b32_e32 v17, v16
	s_nop 1
	v_permlane32_swap_b32_e32 v16, v17
	v_add_f32_e32 v16, v16, v17
	global_store_dwordx4 v[20:21], v[124:127], off
	global_store_dwordx4 v[20:21], v[128:131], off offset:16
	s_lshl_b32 s30, s16, 7
	s_add_u32 s28, s62, s30
	s_addc_u32 s29, s63, 0
	v_lshlrev_b32_e32 v18, 1, v1
	s_mov_b64 exec, s[2:3]
	global_store_dword v18, v16, s[28:29]
	s_mov_b64 exec, -1
	v_readlane_b32 s30, v122, 0
	s_lshl_b32 s30, s30, 12
	s_add_u32 s28, s26, s30
	s_addc_u32 s29, s27, 0
	global_load_dwordx2 v[24:25], v162, s[28:29]
	v_readlane_b32 s30, v122, 1
	s_lshl_b32 s30, s30, 12
	s_add_u32 s28, s26, s30
	s_addc_u32 s29, s27, 0
	global_load_dwordx2 v[26:27], v162, s[28:29]
	v_readlane_b32 s30, v122, 2
	s_lshl_b32 s30, s30, 12
	s_add_u32 s28, s26, s30
	s_addc_u32 s29, s27, 0
	global_load_dwordx2 v[28:29], v162, s[28:29]
	v_readlane_b32 s30, v122, 3
	s_lshl_b32 s30, s30, 12
	s_add_u32 s28, s26, s30
	s_addc_u32 s29, s27, 0
	global_load_dwordx2 v[30:31], v162, s[28:29]
	v_readlane_b32 s30, v122, 4
	s_lshl_b32 s30, s30, 12
	s_add_u32 s28, s26, s30
	s_addc_u32 s29, s27, 0
	global_load_dwordx2 v[32:33], v162, s[28:29]
	v_readlane_b32 s30, v122, 5
	s_lshl_b32 s30, s30, 12
	s_add_u32 s28, s26, s30
	s_addc_u32 s29, s27, 0
	global_load_dwordx2 v[34:35], v162, s[28:29]
	v_readlane_b32 s30, v122, 6
	s_lshl_b32 s30, s30, 12
	s_add_u32 s28, s26, s30
	s_addc_u32 s29, s27, 0
	global_load_dwordx2 v[36:37], v162, s[28:29]
	v_readlane_b32 s30, v122, 7
	s_lshl_b32 s30, s30, 12
	s_add_u32 s28, s26, s30
	s_addc_u32 s29, s27, 0
	global_load_dwordx2 v[38:39], v162, s[28:29]
	v_readlane_b32 s30, v122, 8
	s_lshl_b32 s30, s30, 12
	s_add_u32 s28, s26, s30
	s_addc_u32 s29, s27, 0
	global_load_dwordx2 v[40:41], v162, s[28:29]
	v_readlane_b32 s30, v122, 9
	s_lshl_b32 s30, s30, 12
	s_add_u32 s28, s26, s30
	s_addc_u32 s29, s27, 0
	global_load_dwordx2 v[42:43], v162, s[28:29]
	v_readlane_b32 s30, v122, 10
	s_lshl_b32 s30, s30, 12
	s_add_u32 s28, s26, s30
	s_addc_u32 s29, s27, 0
	global_load_dwordx2 v[44:45], v162, s[28:29]
	v_readlane_b32 s30, v122, 11
	s_lshl_b32 s30, s30, 12
	s_add_u32 s28, s26, s30
	s_addc_u32 s29, s27, 0
	global_load_dwordx2 v[46:47], v162, s[28:29]
	v_readlane_b32 s30, v122, 12
	s_lshl_b32 s30, s30, 12
	s_add_u32 s28, s26, s30
	s_addc_u32 s29, s27, 0
	global_load_dwordx2 v[48:49], v162, s[28:29]
	v_readlane_b32 s30, v122, 13
	s_lshl_b32 s30, s30, 12
	s_add_u32 s28, s26, s30
	s_addc_u32 s29, s27, 0
	global_load_dwordx2 v[50:51], v162, s[28:29]
	v_readlane_b32 s30, v122, 14
	s_lshl_b32 s30, s30, 12
	s_add_u32 s28, s26, s30
	s_addc_u32 s29, s27, 0
	global_load_dwordx2 v[52:53], v162, s[28:29]
	v_readlane_b32 s30, v122, 15
	s_lshl_b32 s30, s30, 12
	s_add_u32 s28, s26, s30
	s_addc_u32 s29, s27, 0
	global_load_dwordx2 v[54:55], v162, s[28:29]
	v_readlane_b32 s30, v122, 16
	s_lshl_b32 s30, s30, 12
	s_add_u32 s28, s26, s30
	s_addc_u32 s29, s27, 0
	global_load_dwordx2 v[56:57], v162, s[28:29]
	v_readlane_b32 s30, v122, 17
	s_lshl_b32 s30, s30, 12
	s_add_u32 s28, s26, s30
	s_addc_u32 s29, s27, 0
	global_load_dwordx2 v[58:59], v162, s[28:29]
	v_readlane_b32 s30, v122, 18
	s_lshl_b32 s30, s30, 12
	s_add_u32 s28, s26, s30
	s_addc_u32 s29, s27, 0
	global_load_dwordx2 v[60:61], v162, s[28:29]
	v_readlane_b32 s30, v122, 19
	s_lshl_b32 s30, s30, 12
	s_add_u32 s28, s26, s30
	s_addc_u32 s29, s27, 0
	global_load_dwordx2 v[62:63], v162, s[28:29]
	v_readlane_b32 s30, v122, 20
	s_lshl_b32 s30, s30, 12
	s_add_u32 s28, s26, s30
	s_addc_u32 s29, s27, 0
	global_load_dwordx2 v[64:65], v162, s[28:29]
	v_readlane_b32 s30, v122, 21
	s_lshl_b32 s30, s30, 12
	s_add_u32 s28, s26, s30
	s_addc_u32 s29, s27, 0
	global_load_dwordx2 v[66:67], v162, s[28:29]
	v_readlane_b32 s30, v122, 22
	s_lshl_b32 s30, s30, 12
	s_add_u32 s28, s26, s30
	s_addc_u32 s29, s27, 0
	global_load_dwordx2 v[68:69], v162, s[28:29]
	v_readlane_b32 s30, v122, 23
	s_lshl_b32 s30, s30, 12
	s_add_u32 s28, s26, s30
	s_addc_u32 s29, s27, 0
	global_load_dwordx2 v[70:71], v162, s[28:29]
	v_readlane_b32 s30, v122, 24
	s_lshl_b32 s30, s30, 12
	s_add_u32 s28, s26, s30
	s_addc_u32 s29, s27, 0
	global_load_dwordx2 v[72:73], v162, s[28:29]
	v_readlane_b32 s30, v122, 25
	s_lshl_b32 s30, s30, 12
	s_add_u32 s28, s26, s30
	s_addc_u32 s29, s27, 0
	global_load_dwordx2 v[74:75], v162, s[28:29]
	v_readlane_b32 s30, v122, 26
	s_lshl_b32 s30, s30, 12
	s_add_u32 s28, s26, s30
	s_addc_u32 s29, s27, 0
	global_load_dwordx2 v[76:77], v162, s[28:29]
	v_readlane_b32 s30, v122, 27
	s_lshl_b32 s30, s30, 12
	s_add_u32 s28, s26, s30
	s_addc_u32 s29, s27, 0
	global_load_dwordx2 v[78:79], v162, s[28:29]
	v_readlane_b32 s30, v122, 28
	s_lshl_b32 s30, s30, 12
	s_add_u32 s28, s26, s30
	s_addc_u32 s29, s27, 0
	global_load_dwordx2 v[80:81], v162, s[28:29]
	v_readlane_b32 s30, v122, 29
	s_lshl_b32 s30, s30, 12
	s_add_u32 s28, s26, s30
	s_addc_u32 s29, s27, 0
	global_load_dwordx2 v[82:83], v162, s[28:29]
	v_readlane_b32 s30, v122, 30
	s_lshl_b32 s30, s30, 12
	s_add_u32 s28, s26, s30
	s_addc_u32 s29, s27, 0
	global_load_dwordx2 v[84:85], v162, s[28:29]
	v_readlane_b32 s30, v122, 31
	s_lshl_b32 s30, s30, 12
	s_add_u32 s28, s26, s30
	s_addc_u32 s29, s27, 0
	global_load_dwordx2 v[86:87], v162, s[28:29]
	s_add_i32 s16, s16, 1
	s_cmp_lt_i32 s16, s17
	s_cbranch_scc1 .Lpb_tok
	s_waitcnt vmcnt(0)
	s_waitcnt vmcnt(0)
	v_cmp_eq_u32_e32 vcc, 0, v0
	s_waitcnt vmcnt(0) lgkmcnt(0)
	s_barrier
	s_and_saveexec_b64 s[2:3], vcc
	s_cbranch_execz .Lgbc_1444
	v_readlane_b32 s4, v237, 5
	s_waitcnt vmcnt(0) expcnt(0) lgkmcnt(0)
	s_nop 0
	v_mov_b32_e32 v1, s4
	ds_read_b32 v3, v1
	ds_read_b32 v1, v1 offset:4
	s_waitcnt lgkmcnt(1)
	v_cmp_ne_u32_e32 vcc, 0, v3
	s_branch .Lgbc_1412
	v_readlane_b32 s4, v237, 2
	v_readlane_b32 s5, v237, 3
	s_load_dwordx2 s[8:9], s[6:7], 0x4
	s_lshl_b64 s[4:5], s[4:5], 2
	v_readlane_b32 s6, v237, 0
	s_add_u32 s4, s6, s4
	v_readlane_b32 s6, v237, 1
	s_addc_u32 s5, s6, s5
	s_add_u32 s6, s4, 0x1000
	s_addc_u32 s7, s5, 0
	s_waitcnt lgkmcnt(0)
	s_mul_i32 s20, s8, s38
	s_add_u32 s8, s4, 0x1100
	s_mul_i32 s20, s20, s9
	s_addc_u32 s9, s5, 0
	s_add_u32 s10, s4, 0x1200
	s_addc_u32 s11, s5, 0
	s_add_u32 s12, s4, 0x1300
	s_addc_u32 s13, s5, 0
	s_mov_b32 s21, 1
	v_mov_b32_e32 v17, 0
	s_branch .Lgbc_1400

.Lgbc_1444:
	s_or_b64 exec, exec, s[2:3]
	s_waitcnt lgkmcnt(0)
	s_barrier
	s_mov_b64 exec, -1
	s_load_dwordx2 s[12:13], s[0:1], 0xc0
	s_load_dwordx2 s[4:5], s[0:1], 0xb8
	s_load_dwordx2 s[6:7], s[0:1], 0xb0
	v_lshlrev_b32_e32 v2, 5, v0
	v_mov_b32_e32 v3, 0
	v_mov_b32_e32 v173, 0x358637bd
	v_mov_b32_e32 v174, 0x260
	s_mov_b32 s51, 0xf800000
	s_mov_b32 s31, 0
	s_lshl_b32 s16, s33, 5
	s_add_i32 s17, s16, 32
	s_waitcnt lgkmcnt(0)
	v_lshl_add_u64 v[4:5], v[2:3], 0, s[6:7]
	global_load_dwordx4 v[100:103], v[4:5], off
	global_load_dwordx4 v[104:107], v[4:5], off offset:16
	v_lshl_add_u64 v[6:7], v[2:3], 0, s[4:5]
	s_add_u32 s20, s12, 0x27c00000
	s_addc_u32 s21, s13, 0
	v_lshl_add_u64 v[32:33], v[2:3], 0, s[20:21]
	s_add_u32 s62, s12, 0x26c00000
	s_addc_u32 s63, s13, 0
	v_and_b32_e32 v8, 7, v0
	v_mov_b32_e32 v9, 0
	v_lshlrev_b32_e32 v8, 20, v8
	v_lshl_add_u64 v[26:27], v[8:9], 0, s[62:63]
.Lpc_tok:
	s_lshl_b32 s30, s16, 14
	v_lshl_add_u64 v[4:5], v[6:7], 0, s[30:31]
	v_lshl_add_u64 v[34:35], v[32:33], 0, s[30:31]
	global_load_dwordx4 v[10:13], v[34:35], off
	global_load_dwordx4 v[14:17], v[34:35], off offset:16
	s_lshl_b32 s30, s16, 7
	v_lshl_add_u64 v[24:25], v[26:27], 0, s[30:31]
	global_load_dword v18, v[24:25], off
	s_waitcnt vmcnt(0)
	s_nop 1
	v_add_f32_dpp v19, v18, v18 quad_perm:[1,0,3,2] row_mask:0xf bank_mask:0xf
	s_nop 1
	v_add_f32_dpp v18, v19, v19 quad_perm:[2,3,0,1] row_mask:0xf bank_mask:0xf
	s_nop 1
	v_add_f32_dpp v18, v18, v18 row_half_mirror row_mask:0xf bank_mask:0xf
	v_fmamk_f32 v18, v18, 0x39800000, v173
	v_mul_f32_e32 v19, 0x4f800000, v18
	v_cmp_gt_f32_e32 vcc, s51, v18
	s_nop 1
	v_cndmask_b32_e32 v18, v18, v19, vcc
	v_sqrt_f32_e32 v19, v18
	s_nop 0
	v_add_u32_e32 v20, -1, v19
	v_fma_f32 v22, -v20, v19, v18
	v_add_u32_e32 v21, 1, v19
	v_cmp_ge_f32_e64 s[14:15], 0, v22
	s_nop 1
	v_cndmask_b32_e64 v20, v19, v20, s[14:15]
	v_fma_f32 v19, -v21, v19, v18
	v_cmp_lt_f32_e64 s[14:15], 0, v19
	s_nop 1
	v_cndmask_b32_e64 v19, v20, v21, s[14:15]
	v_mul_f32_e32 v20, 0x37800000, v19
	v_cndmask_b32_e32 v19, v19, v20, vcc
	v_cmp_class_f32_e32 vcc, v18, v174
	s_nop 1
	v_cndmask_b32_e32 v18, v19, v18, vcc
	v_div_scale_f32 v19, s[14:15], v18, v18, 1.0
	v_rcp_f32_e32 v20, v19
	s_nop 0
	v_fma_f32 v21, -v19, v20, 1.0
	v_fmac_f32_e32 v20, v21, v20
	v_div_scale_f32 v21, vcc, 1.0, v18, 1.0
	v_mul_f32_e32 v22, v21, v20
	v_fma_f32 v23, -v19, v22, v21
	v_fmac_f32_e32 v22, v23, v20
	v_fma_f32 v19, -v19, v22, v21
	v_div_fmas_f32 v19, v19, v20, v22
	v_div_fixup_f32 v18, v19, v18, 1.0
	v_pk_mul_f32 v[10:11], v[10:11], v[18:19] op_sel_hi:[1,0]
	v_pk_mul_f32 v[12:13], v[12:13], v[18:19] op_sel_hi:[1,0]
	v_pk_mul_f32 v[14:15], v[14:15], v[18:19] op_sel_hi:[1,0]
	v_pk_mul_f32 v[16:17], v[16:17], v[18:19] op_sel_hi:[1,0]
	v_pk_mul_f32 v[10:11], v[10:11], v[100:101]
	v_pk_mul_f32 v[12:13], v[12:13], v[102:103]
	v_pk_mul_f32 v[14:15], v[14:15], v[104:105]
	v_pk_mul_f32 v[16:17], v[16:17], v[106:107]
	global_store_dwordx4 v[4:5], v[10:13], off
	global_store_dwordx4 v[4:5], v[14:17], off offset:16
	s_nop 1
	s_add_i32 s16, s16, 1
	s_cmp_lt_i32 s16, s17
	s_cbranch_scc1 .Lpc_tok
	s_waitcnt vmcnt(0)
	s_branch .LBB0_1485
	s_cmp_gt_i32 s56, 12
	s_cselect_b64 s[2:3], -1, 0
	s_cmp_lt_i32 s57, 13
	s_cselect_b64 s[4:5], -1, 0
	s_or_b64 s[2:3], s[2:3], s[4:5]
	s_and_b64 vcc, exec, s[2:3]
	s_cbranch_vccnz .LBB0_1485
	s_load_dword s25, s[0:1], 0xd8
	s_waitcnt lgkmcnt(0)
	s_and_b32 s2, s25, 7
	s_cmp_lg_u32 s2, 0
	v_readfirstlane_b32 s2, v0
	s_cbranch_scc1 .LBB0_1466
	s_ashr_i32 s4, s33, 31
	s_lshr_b32 s4, s4, 29
	s_add_i32 s4, s33, s4
	s_ashr_i32 s5, s4, 3
	s_and_b32 s4, s4, -8
	s_ashr_i32 s3, s25, 3
	s_sub_i32 s4, s33, s4
	s_mul_i32 s3, s3, s4
	s_add_i32 s33, s3, s5
